# grid barrier: non-leader workgroups poll the top-level generation word directly (one hop fewer); P9: fcanonicalize copies in front of the sorting networks removed
# speedup vs baseline: 1.0036x; 1.0036x over previous
; __device__ __forceinline__ unsigned xb_ld(unsigned* p)              { return __hip_atomic_load(p, __ATOMIC_RELAXED, __HIP_MEMORY_SCOPE_AGENT); }
; __device__ __forceinline__ unsigned xb_add(unsigned* p, unsigned v) { return __hip_atomic_fetch_add(p, v, __ATOMIC_RELAXED, __HIP_MEMORY_SCOPE_AGENT); }
; #define XB_SPIN(cond, bar) do { unsigned _sp = 0; while (cond) { __builtin_amdgcn_s_sleep(1); \
;     if ((++_sp & 255u) == 0u) { if (xb_ld(&(bar)[XB_TMO])) break; if (_sp > XB_SPIN_CAP) { atomicAdd(&(bar)[XB_TMO], 1u); break; } } } } while (0)
; __device__ __forceinline__ void xcd_barrier(const XcdBarrier& b) {
;     ...
;         const unsigned old = xb_add(&bar[XB_XSUB(b.x)], 1u);
;         const unsigned gen = old / nloc;
;         if (old + 1u == (gen + 1u) * nloc) {
;             __builtin_amdgcn_fence(__ATOMIC_RELEASE, "agent");
;             asm volatile("s_waitcnt vmcnt(0)" ::: "memory");
;             const unsigned og = xb_add(&bar[XB_TOP], 1u);
;             const unsigned tg = og / nx;
;             if (og + 1u == (tg + 1u) * nx) xb_add(&bar[XB_TOPGEN], 1u);
;             else XB_SPIN(xb_ld(&bar[XB_TOPGEN]) == tg, bar);
;             __builtin_amdgcn_fence(__ATOMIC_ACQUIRE, "agent");
;             xb_add(&bar[XB_XGEN(b.x)], 1u);
;             asm volatile("s_waitcnt vmcnt(0)" ::: "memory");
;         } else {
;             XB_SPIN(xb_ld(&bar[XB_XGEN(b.x)]) == gen, bar);
.LBB0_81:
	s_or_b64 exec, exec, s[10:11]
	v_cvt_f32_u32_e32 v5, v3
	s_waitcnt vmcnt(0)
	v_readfirstlane_b32 s0, v4
	v_sub_u32_e32 v4, 0, v3
	v_rcp_iflag_f32_e32 v5, v5
	v_add_u32_e32 v6, s0, v2
	v_mul_f32_e32 v5, 0x4f7ffffe, v5
	v_cvt_u32_f32_e32 v5, v5
	v_mul_lo_u32 v2, v4, v5
	v_mul_hi_u32 v2, v5, v2
	v_add_u32_e32 v2, v5, v2
	v_mul_hi_u32 v2, v6, v2
	v_mul_lo_u32 v4, v2, v3
	v_sub_u32_e32 v4, v6, v4
	v_add_u32_e32 v5, 1, v2
	v_cmp_ge_u32_e32 vcc, v4, v3
	s_nop 1
	v_cndmask_b32_e32 v2, v2, v5, vcc
	v_sub_u32_e32 v5, v4, v3
	v_cndmask_b32_e32 v4, v4, v5, vcc
	v_add_u32_e32 v5, 1, v2
	v_cmp_ge_u32_e32 vcc, v4, v3
	v_add_u32_e32 v4, 1, v6
	s_nop 0
	v_cndmask_b32_e32 v2, v2, v5, vcc
	v_mul_lo_u32 v5, v3, v2
	v_add_u32_e32 v3, v5, v3
	v_cmp_ne_u32_e32 vcc, v4, v3
	s_and_saveexec_b64 s[0:1], vcc
	s_xor_b64 s[10:11], exec, s[0:1]
	s_cbranch_execz .LBB0_95
	s_waitcnt lgkmcnt(0)
	v_mov_b32_e32 v1, 0x3100
	global_load_dword v1, v1, s[42:43] offset:1024 sc1
	s_add_u32 s12, s42, 0x3500
	s_addc_u32 s13, s43, 0
	s_waitcnt vmcnt(0)
	v_cmp_eq_u32_e32 vcc, v1, v2
	s_and_saveexec_b64 s[0:1], vcc
	s_cbranch_execz .LBB0_94
	s_mov_b32 s28, 1
	s_mov_b64 s[14:15], 0
	v_mov_b32_e32 v1, 0
	s_branch .LBB0_85

; __device__ __forceinline__ unsigned xb_ld(unsigned* p)              { return __hip_atomic_load(p, __ATOMIC_RELAXED, __HIP_MEMORY_SCOPE_AGENT); }
; __device__ __forceinline__ unsigned xb_add(unsigned* p, unsigned v) { return __hip_atomic_fetch_add(p, v, __ATOMIC_RELAXED, __HIP_MEMORY_SCOPE_AGENT); }
; #define XB_SPIN(cond, bar) do { unsigned _sp = 0; while (cond) { __builtin_amdgcn_s_sleep(1); \
;     if ((++_sp & 255u) == 0u) { if (xb_ld(&(bar)[XB_TMO])) break; if (_sp > XB_SPIN_CAP) { atomicAdd(&(bar)[XB_TMO], 1u); break; } } } } while (0)
; __device__ __forceinline__ void xcd_barrier(const XcdBarrier& b) {
;     ...
;         const unsigned old = xb_add(&bar[XB_XSUB(b.x)], 1u);
;         const unsigned gen = old / nloc;
;         if (old + 1u == (gen + 1u) * nloc) {
;             __builtin_amdgcn_fence(__ATOMIC_RELEASE, "agent");
;             asm volatile("s_waitcnt vmcnt(0)" ::: "memory");
;             const unsigned og = xb_add(&bar[XB_TOP], 1u);
;             const unsigned tg = og / nx;
;             if (og + 1u == (tg + 1u) * nx) xb_add(&bar[XB_TOPGEN], 1u);
;             else XB_SPIN(xb_ld(&bar[XB_TOPGEN]) == tg, bar);
;             __builtin_amdgcn_fence(__ATOMIC_ACQUIRE, "agent");
;             xb_add(&bar[XB_XGEN(b.x)], 1u);
;             asm volatile("s_waitcnt vmcnt(0)" ::: "memory");
;         } else {
;             XB_SPIN(xb_ld(&bar[XB_XGEN(b.x)]) == gen, bar);
.LBB0_159:
	s_or_b64 exec, exec, s[10:11]
	v_cvt_f32_u32_e32 v5, v3
	s_waitcnt vmcnt(0)
	v_readfirstlane_b32 s0, v4
	v_sub_u32_e32 v4, 0, v3
	v_rcp_iflag_f32_e32 v5, v5
	v_add_u32_e32 v6, s0, v2
	v_mul_f32_e32 v5, 0x4f7ffffe, v5
	v_cvt_u32_f32_e32 v5, v5
	v_mul_lo_u32 v2, v4, v5
	v_mul_hi_u32 v2, v5, v2
	v_add_u32_e32 v2, v5, v2
	v_mul_hi_u32 v2, v6, v2
	v_mul_lo_u32 v4, v2, v3
	v_sub_u32_e32 v4, v6, v4
	v_add_u32_e32 v5, 1, v2
	v_cmp_ge_u32_e32 vcc, v4, v3
	s_nop 1
	v_cndmask_b32_e32 v2, v2, v5, vcc
	v_sub_u32_e32 v5, v4, v3
	v_cndmask_b32_e32 v4, v4, v5, vcc
	v_add_u32_e32 v5, 1, v2
	v_cmp_ge_u32_e32 vcc, v4, v3
	v_add_u32_e32 v4, 1, v6
	s_nop 0
	v_cndmask_b32_e32 v2, v2, v5, vcc
	v_mul_lo_u32 v5, v3, v2
	v_add_u32_e32 v3, v5, v3
	v_cmp_ne_u32_e32 vcc, v4, v3
	s_and_saveexec_b64 s[0:1], vcc
	s_xor_b64 s[10:11], exec, s[0:1]
	s_cbranch_execz .LBB0_173
	s_waitcnt lgkmcnt(0)
	v_mov_b32_e32 v1, 0x3100
	global_load_dword v1, v1, s[42:43] offset:1024 sc1
	s_add_u32 s12, s42, 0x3500
	s_addc_u32 s13, s43, 0
	s_waitcnt vmcnt(0)
	v_cmp_eq_u32_e32 vcc, v1, v2
	s_and_saveexec_b64 s[0:1], vcc
	s_cbranch_execz .LBB0_172
	s_mov_b32 s3, 1
	s_mov_b64 s[14:15], 0
	v_mov_b32_e32 v1, 0
	s_branch .LBB0_163

; __device__ __forceinline__ unsigned xb_ld(unsigned* p)              { return __hip_atomic_load(p, __ATOMIC_RELAXED, __HIP_MEMORY_SCOPE_AGENT); }
; __device__ __forceinline__ unsigned xb_add(unsigned* p, unsigned v) { return __hip_atomic_fetch_add(p, v, __ATOMIC_RELAXED, __HIP_MEMORY_SCOPE_AGENT); }
; #define XB_SPIN(cond, bar) do { unsigned _sp = 0; while (cond) { __builtin_amdgcn_s_sleep(1); \
;     if ((++_sp & 255u) == 0u) { if (xb_ld(&(bar)[XB_TMO])) break; if (_sp > XB_SPIN_CAP) { atomicAdd(&(bar)[XB_TMO], 1u); break; } } } } while (0)
; __device__ __forceinline__ void xcd_barrier(const XcdBarrier& b) {
;     ...
;         const unsigned old = xb_add(&bar[XB_XSUB(b.x)], 1u);
;         const unsigned gen = old / nloc;
;         if (old + 1u == (gen + 1u) * nloc) {
;             __builtin_amdgcn_fence(__ATOMIC_RELEASE, "agent");
;             asm volatile("s_waitcnt vmcnt(0)" ::: "memory");
;             const unsigned og = xb_add(&bar[XB_TOP], 1u);
;             const unsigned tg = og / nx;
;             if (og + 1u == (tg + 1u) * nx) xb_add(&bar[XB_TOPGEN], 1u);
;             else XB_SPIN(xb_ld(&bar[XB_TOPGEN]) == tg, bar);
;             __builtin_amdgcn_fence(__ATOMIC_ACQUIRE, "agent");
;             xb_add(&bar[XB_XGEN(b.x)], 1u);
;             asm volatile("s_waitcnt vmcnt(0)" ::: "memory");
;         } else {
;             XB_SPIN(xb_ld(&bar[XB_XGEN(b.x)]) == gen, bar);
.LBB0_652:
	s_or_b64 exec, exec, s[8:9]
	v_cvt_f32_u32_e32 v5, v3
	s_waitcnt vmcnt(0)
	v_readfirstlane_b32 s0, v4
	v_sub_u32_e32 v4, 0, v3
	v_rcp_iflag_f32_e32 v5, v5
	v_add_u32_e32 v6, s0, v2
	v_mul_f32_e32 v5, 0x4f7ffffe, v5
	v_cvt_u32_f32_e32 v5, v5
	v_mul_lo_u32 v2, v4, v5
	v_mul_hi_u32 v2, v5, v2
	v_add_u32_e32 v2, v5, v2
	v_mul_hi_u32 v2, v6, v2
	v_mul_lo_u32 v4, v2, v3
	v_sub_u32_e32 v4, v6, v4
	v_add_u32_e32 v5, 1, v2
	v_cmp_ge_u32_e32 vcc, v4, v3
	s_nop 1
	v_cndmask_b32_e32 v2, v2, v5, vcc
	v_sub_u32_e32 v5, v4, v3
	v_cndmask_b32_e32 v4, v4, v5, vcc
	v_add_u32_e32 v5, 1, v2
	v_cmp_ge_u32_e32 vcc, v4, v3
	v_add_u32_e32 v4, 1, v6
	s_nop 0
	v_cndmask_b32_e32 v2, v2, v5, vcc
	v_mul_lo_u32 v5, v3, v2
	v_add_u32_e32 v3, v5, v3
	v_cmp_ne_u32_e32 vcc, v4, v3
	s_and_saveexec_b64 s[0:1], vcc
	s_xor_b64 s[8:9], exec, s[0:1]
	s_cbranch_execz .LBB0_666
	s_waitcnt lgkmcnt(0)
	v_mov_b32_e32 v1, 0x3100
	global_load_dword v1, v1, s[42:43] offset:1024 sc1
	s_add_u32 s10, s42, 0x3500
	s_addc_u32 s11, s43, 0
	s_waitcnt vmcnt(0)
	v_cmp_eq_u32_e32 vcc, v1, v2
	s_and_saveexec_b64 s[0:1], vcc
	s_cbranch_execz .LBB0_665
	s_mov_b32 s22, 1
	s_mov_b64 s[12:13], 0
	v_mov_b32_e32 v1, 0
	s_branch .LBB0_656

; __device__ __forceinline__ unsigned xb_ld(unsigned* p)              { return __hip_atomic_load(p, __ATOMIC_RELAXED, __HIP_MEMORY_SCOPE_AGENT); }
; __device__ __forceinline__ unsigned xb_add(unsigned* p, unsigned v) { return __hip_atomic_fetch_add(p, v, __ATOMIC_RELAXED, __HIP_MEMORY_SCOPE_AGENT); }
; #define XB_SPIN(cond, bar) do { unsigned _sp = 0; while (cond) { __builtin_amdgcn_s_sleep(1); \
;     if ((++_sp & 255u) == 0u) { if (xb_ld(&(bar)[XB_TMO])) break; if (_sp > XB_SPIN_CAP) { atomicAdd(&(bar)[XB_TMO], 1u); break; } } } } while (0)
; __device__ __forceinline__ void xcd_barrier(const XcdBarrier& b) {
;     ...
;         const unsigned old = xb_add(&bar[XB_XSUB(b.x)], 1u);
;         const unsigned gen = old / nloc;
;         if (old + 1u == (gen + 1u) * nloc) {
;             __builtin_amdgcn_fence(__ATOMIC_RELEASE, "agent");
;             asm volatile("s_waitcnt vmcnt(0)" ::: "memory");
;             const unsigned og = xb_add(&bar[XB_TOP], 1u);
;             const unsigned tg = og / nx;
;             if (og + 1u == (tg + 1u) * nx) xb_add(&bar[XB_TOPGEN], 1u);
;             else XB_SPIN(xb_ld(&bar[XB_TOPGEN]) == tg, bar);
;             __builtin_amdgcn_fence(__ATOMIC_ACQUIRE, "agent");
;             xb_add(&bar[XB_XGEN(b.x)], 1u);
;             asm volatile("s_waitcnt vmcnt(0)" ::: "memory");
;         } else {
;             XB_SPIN(xb_ld(&bar[XB_XGEN(b.x)]) == gen, bar);
.LBB0_727:
	s_or_b64 exec, exec, s[10:11]
	v_cvt_f32_u32_e32 v5, v3
	s_waitcnt vmcnt(0)
	v_readfirstlane_b32 s0, v4
	v_sub_u32_e32 v4, 0, v3
	v_rcp_iflag_f32_e32 v5, v5
	v_add_u32_e32 v6, s0, v2
	v_mul_f32_e32 v5, 0x4f7ffffe, v5
	v_cvt_u32_f32_e32 v5, v5
	v_mul_lo_u32 v2, v4, v5
	v_mul_hi_u32 v2, v5, v2
	v_add_u32_e32 v2, v5, v2
	v_mul_hi_u32 v2, v6, v2
	v_mul_lo_u32 v4, v2, v3
	v_sub_u32_e32 v4, v6, v4
	v_add_u32_e32 v5, 1, v2
	v_cmp_ge_u32_e32 vcc, v4, v3
	s_nop 1
	v_cndmask_b32_e32 v2, v2, v5, vcc
	v_sub_u32_e32 v5, v4, v3
	v_cndmask_b32_e32 v4, v4, v5, vcc
	v_add_u32_e32 v5, 1, v2
	v_cmp_ge_u32_e32 vcc, v4, v3
	v_add_u32_e32 v4, 1, v6
	s_nop 0
	v_cndmask_b32_e32 v2, v2, v5, vcc
	v_mul_lo_u32 v5, v3, v2
	v_add_u32_e32 v3, v5, v3
	v_cmp_ne_u32_e32 vcc, v4, v3
	s_and_saveexec_b64 s[0:1], vcc
	s_xor_b64 s[10:11], exec, s[0:1]
	s_cbranch_execz .LBB0_741
	s_waitcnt lgkmcnt(0)
	v_mov_b32_e32 v1, 0x3100
	global_load_dword v1, v1, s[42:43] offset:1024 sc1
	s_add_u32 s12, s42, 0x3500
	s_addc_u32 s13, s43, 0
	s_waitcnt vmcnt(0)
	v_cmp_eq_u32_e32 vcc, v1, v2
	s_and_saveexec_b64 s[0:1], vcc
	s_cbranch_execz .LBB0_740
	s_mov_b32 s24, 1
	s_mov_b64 s[14:15], 0
	v_mov_b32_e32 v1, 0
	s_branch .LBB0_731

; __device__ __forceinline__ float bf2f(bf16_t v) { return __uint_as_float(((unsigned)v) << 16); }
; #define LAS __attribute__((address_space(3)))
; __device__ __forceinline__ void route_half(float (&top)[16], LAS const unsigned char* keys_lds, const bf16_t* __restrict__ qrow, int r32, int hi) {
;     bf16x8 qf[8]; float ss = 0.f;
; #pragma unroll
;     for (int ks = 0; ks < 8; ++ks) { qf[ks] = __builtin_nontemporal_load((const bf16x8*)(qrow + 16 * ks + 8 * hi));
; #pragma unroll
;         for (int j = 0; j < 8; ++j) { const float f = bf2f((bf16_t)qf[ks][j]); ss += f * f; } }
;     ss += __shfl_xor(ss, 32);
;     const float rn = rsqrtf(ss * (1.f / 128.f) + EPS);
;     f32x16 acc[4];
; #pragma unroll
;     for (int kt = 0; kt < 4; ++kt) {
; #pragma unroll
;         for (int r = 0; r < 16; ++r) acc[kt][r] = 0.f;
; #pragma unroll
;         for (int ks = 0; ks < 8; ++ks) { const bf16x8 kf = *(LAS const bf16x8*)(keys_lds + (32 * kt + r32) * RT_KROW + (16 * ks + 8 * hi) * 2);
;             acc[kt] = __builtin_amdgcn_mfma_f32_32x32x16_bf16(kf, qf[ks], acc[kt], 0, 0, 0); }
.LBB0_910:
	v_ashrrev_i32_e32 v139, 31, v138
	v_lshlrev_b64 v[2:3], 12, v[138:139]
	v_lshl_add_u64 v[140:141], v[136:137], 0, v[2:3]
	global_load_dwordx4 v[18:21], v[140:141], off nt
	global_load_dwordx4 v[98:101], v[140:141], off offset:32 nt
	global_load_dwordx4 v[102:105], v[140:141], off offset:64 nt
	global_load_dwordx4 v[106:109], v[140:141], off offset:96 nt
	global_load_dwordx4 v[110:113], v[140:141], off offset:128 nt
	global_load_dwordx4 v[114:117], v[140:141], off offset:160 nt
	global_load_dwordx4 v[118:121], v[140:141], off offset:192 nt
	global_load_dwordx4 v[122:125], v[140:141], off offset:224 nt
	ds_read_b128 v[2:5], v143
	ds_read_b128 v[22:25], v143 offset:32
	ds_read_b128 v[26:29], v143 offset:64
	ds_read_b128 v[30:33], v143 offset:96
	ds_read_b128 v[34:37], v143 offset:128
	s_waitcnt vmcnt(7) lgkmcnt(4)
	v_mfma_f32_32x32x16_bf16 v[2:17], v[2:5], v[18:21], 0
	v_and_b32_e32 v46, 0xffff0000, v18
	v_lshlrev_b32_e32 v44, 16, v18
	v_mul_f32_e32 v46, v46, v46
	v_lshlrev_b32_e32 v47, 16, v19
	v_fmac_f32_e32 v46, v44, v44
	v_and_b32_e32 v48, 0xffff0000, v19
	v_fmac_f32_e32 v46, v47, v47
	v_lshlrev_b32_e32 v49, 16, v20
	v_fmac_f32_e32 v46, v48, v48
	v_and_b32_e32 v50, 0xffff0000, v20
	v_fmac_f32_e32 v46, v49, v49
	v_lshlrev_b32_e32 v51, 16, v21
	v_fmac_f32_e32 v46, v50, v50
	v_and_b32_e32 v52, 0xffff0000, v21
	v_fmac_f32_e32 v46, v51, v51
	s_waitcnt vmcnt(6)
	v_lshlrev_b32_e32 v53, 16, v98
	v_fmac_f32_e32 v46, v52, v52
	v_and_b32_e32 v54, 0xffff0000, v98
	v_fmac_f32_e32 v46, v53, v53
	v_lshlrev_b32_e32 v55, 16, v99
	v_fmac_f32_e32 v46, v54, v54
	v_and_b32_e32 v56, 0xffff0000, v99
	v_fmac_f32_e32 v46, v55, v55
	v_lshlrev_b32_e32 v57, 16, v100
	v_fmac_f32_e32 v46, v56, v56
	v_and_b32_e32 v58, 0xffff0000, v100
	v_fmac_f32_e32 v46, v57, v57
	v_lshlrev_b32_e32 v59, 16, v101
	v_fmac_f32_e32 v46, v58, v58
	v_and_b32_e32 v60, 0xffff0000, v101
	v_fmac_f32_e32 v46, v59, v59
	s_waitcnt vmcnt(5)
	v_lshlrev_b32_e32 v61, 16, v102
	v_fmac_f32_e32 v46, v60, v60
	v_and_b32_e32 v62, 0xffff0000, v102
	v_fmac_f32_e32 v46, v61, v61
	v_lshlrev_b32_e32 v63, 16, v103
	v_fmac_f32_e32 v46, v62, v62
	v_and_b32_e32 v64, 0xffff0000, v103
	v_fmac_f32_e32 v46, v63, v63
	v_lshlrev_b32_e32 v65, 16, v104
	v_fmac_f32_e32 v46, v64, v64
	v_and_b32_e32 v149, 0xffff0000, v104
	v_fmac_f32_e32 v46, v65, v65
	v_lshlrev_b32_e32 v150, 16, v105
	v_fmac_f32_e32 v46, v149, v149
	v_and_b32_e32 v151, 0xffff0000, v105
	v_fmac_f32_e32 v46, v150, v150
	s_waitcnt vmcnt(4)
	v_lshlrev_b32_e32 v152, 16, v106
	v_fmac_f32_e32 v46, v151, v151
	v_and_b32_e32 v153, 0xffff0000, v106
	v_fmac_f32_e32 v46, v152, v152
	v_lshlrev_b32_e32 v154, 16, v107
	v_fmac_f32_e32 v46, v153, v153
	v_and_b32_e32 v155, 0xffff0000, v107
	v_fmac_f32_e32 v46, v154, v154
	v_lshlrev_b32_e32 v156, 16, v108
	v_fmac_f32_e32 v46, v155, v155
	v_and_b32_e32 v157, 0xffff0000, v108
	v_fmac_f32_e32 v46, v156, v156
	v_lshlrev_b32_e32 v158, 16, v109
	v_fmac_f32_e32 v46, v157, v157
	v_and_b32_e32 v159, 0xffff0000, v109
	v_fmac_f32_e32 v46, v158, v158
	s_waitcnt vmcnt(3)
	v_lshlrev_b32_e32 v160, 16, v110
	v_fmac_f32_e32 v46, v159, v159
	v_and_b32_e32 v161, 0xffff0000, v110
	v_fmac_f32_e32 v46, v160, v160
	v_lshlrev_b32_e32 v162, 16, v111
	v_fmac_f32_e32 v46, v161, v161
	v_and_b32_e32 v163, 0xffff0000, v111
	v_fmac_f32_e32 v46, v162, v162
	v_lshlrev_b32_e32 v164, 16, v112
	v_fmac_f32_e32 v46, v163, v163
	v_and_b32_e32 v165, 0xffff0000, v112
	v_fmac_f32_e32 v46, v164, v164
	v_lshlrev_b32_e32 v166, 16, v113
	v_fmac_f32_e32 v46, v165, v165
	v_and_b32_e32 v167, 0xffff0000, v113
	v_fmac_f32_e32 v46, v166, v166
	s_waitcnt vmcnt(2)
	v_lshlrev_b32_e32 v168, 16, v114
	s_waitcnt lgkmcnt(3)
	v_mfma_f32_32x32x16_bf16 v[2:17], v[22:25], v[98:101], v[2:17]
	v_fmac_f32_e32 v46, v167, v167
	v_and_b32_e32 v169, 0xffff0000, v114
	v_fmac_f32_e32 v46, v168, v168
	v_lshlrev_b32_e32 v170, 16, v115
	v_fmac_f32_e32 v46, v169, v169
	v_and_b32_e32 v171, 0xffff0000, v115
	v_fmac_f32_e32 v46, v170, v170
	v_lshlrev_b32_e32 v172, 16, v116
	v_fmac_f32_e32 v46, v171, v171
	v_and_b32_e32 v173, 0xffff0000, v116
	v_fmac_f32_e32 v46, v172, v172
	v_lshlrev_b32_e32 v174, 16, v117
	v_fmac_f32_e32 v46, v173, v173
	v_and_b32_e32 v175, 0xffff0000, v117
	v_fmac_f32_e32 v46, v174, v174
	s_waitcnt vmcnt(1)
	v_lshlrev_b32_e32 v176, 16, v118
	s_waitcnt lgkmcnt(2)
	v_mfma_f32_32x32x16_bf16 v[2:17], v[26:29], v[102:105], v[2:17]
	v_fmac_f32_e32 v46, v175, v175
	v_and_b32_e32 v177, 0xffff0000, v118
	v_fmac_f32_e32 v46, v176, v176
	v_lshlrev_b32_e32 v178, 16, v119
	v_fmac_f32_e32 v46, v177, v177
	v_and_b32_e32 v179, 0xffff0000, v119
	v_fmac_f32_e32 v46, v178, v178
	v_lshlrev_b32_e32 v180, 16, v120
	v_fmac_f32_e32 v46, v179, v179
	v_and_b32_e32 v181, 0xffff0000, v120
	v_and_b32_e32 v39, 0xffff0000, v121
	v_lshlrev_b32_e32 v38, 16, v121
	v_fmac_f32_e32 v46, v180, v180
	v_pk_mul_f32 v[38:39], v[38:39], v[38:39]
	v_fmac_f32_e32 v46, v181, v181
	s_waitcnt vmcnt(0)
	v_and_b32_e32 v41, 0xffff0000, v122
	v_lshlrev_b32_e32 v40, 16, v122
	v_add_f32_e32 v22, v38, v46
	v_pk_mul_f32 v[40:41], v[40:41], v[40:41]
	s_waitcnt lgkmcnt(1)
	v_mfma_f32_32x32x16_bf16 v[2:17], v[30:33], v[106:109], v[2:17]
	v_add_f32_e32 v22, v39, v22
	v_and_b32_e32 v43, 0xffff0000, v123
	v_lshlrev_b32_e32 v42, 16, v123
	v_add_f32_e32 v22, v40, v22
	v_mul_f32_e64 v42, v42, v42
	v_mul_f32_e64 v43, v43, v43
	v_add_f32_e32 v22, v41, v22
	v_and_b32_e32 v45, 0xffff0000, v124
	v_add_f32_e32 v22, v42, v22
	v_lshlrev_b32_e32 v44, 16, v124
	v_add_f32_e32 v22, v43, v22
	v_pk_mul_f32 v[26:27], v[44:45], v[44:45]
	s_waitcnt lgkmcnt(0)
; #define LAS __attribute__((address_space(3)))
; __device__ __forceinline__ void route_half(float (&top)[16], LAS const unsigned char* keys_lds, const bf16_t* __restrict__ qrow, int r32, int hi) {
;     ...
;     ss += __shfl_xor(ss, 32);
;     const float rn = rsqrtf(ss * (1.f / 128.f) + EPS);
;     f32x16 acc[4];
; #pragma unroll
;     for (int kt = 0; kt < 4; ++kt) {
; #pragma unroll
;         for (int r = 0; r < 16; ++r) acc[kt][r] = 0.f;
; #pragma unroll
;         for (int ks = 0; ks < 8; ++ks) { const bf16x8 kf = *(LAS const bf16x8*)(keys_lds + (32 * kt + r32) * RT_KROW + (16 * ks + 8 * hi) * 2);
;             acc[kt] = __builtin_amdgcn_mfma_f32_32x32x16_bf16(kf, qf[ks], acc[kt], 0, 0, 0); }
;         __builtin_amdgcn_sched_barrier(0);
;     }
;     const unsigned hi4 = (unsigned)hi << 2;
;     float g[4][16];
; #pragma unroll
;     for (int kt = 0; kt < 4; ++kt)
; #pragma unroll
;         for (int r = 0; r < 16; ++r) { const unsigned base = (unsigned)(32 * kt + (r & 3) + 8 * (r >> 2)); g[kt][r] = __uint_as_float((__float_as_uint(acc[kt][r] * rn) & 0xFFFFFF80u) | base); }
	v_mfma_f32_32x32x16_bf16 v[2:17], v[34:37], v[110:113], v[2:17]
	v_add_f32_e32 v26, v26, v22
	v_add_f32_e32 v28, v27, v26
	v_and_b32_e32 v27, 0xffff0000, v125
	v_lshlrev_b32_e32 v26, 16, v125
	ds_read_b128 v[22:25], v143 offset:160
	v_pk_mul_f32 v[26:27], v[26:27], v[26:27]
	s_nop 0
	v_add_f32_e32 v26, v26, v28
	v_add_f32_e32 v26, v27, v26
	ds_bpermute_b32 v27, v142, v26
	s_waitcnt lgkmcnt(0)
	v_add_f32_e32 v26, v26, v27
	v_fmamk_f32 v30, v26, 0x3c000000, v146
	ds_read_b128 v[26:29], v143 offset:224
	v_mfma_f32_32x32x16_bf16 v[2:17], v[22:25], v[114:117], v[2:17]
	ds_read_b128 v[22:25], v143 offset:192
	v_mul_f32_e32 v31, 0x4b800000, v30
	v_cmp_gt_f32_e32 vcc, s40, v30
	s_waitcnt lgkmcnt(0)
	v_mfma_f32_32x32x16_bf16 v[2:17], v[22:25], v[118:121], v[2:17]
	v_cndmask_b32_e32 v22, v30, v31, vcc
	v_rsq_f32_e32 v149, v22
	s_nop 0
	v_mul_f32_e32 v154, 0x45800000, v149
	v_mfma_f32_32x32x16_bf16 v[2:17], v[26:29], v[122:125], v[2:17]
	ds_read_b128 v[22:25], v143 offset:8704
	ds_read_b128 v[26:29], v143 offset:8736
	s_waitcnt lgkmcnt(1)
	v_mfma_f32_32x32x16_bf16 v[50:65], v[22:25], v[18:21], 0
	s_waitcnt lgkmcnt(0)
	v_mfma_f32_32x32x16_bf16 v[50:65], v[26:29], v[98:101], v[50:65]
	ds_read_b128 v[22:25], v143 offset:8768
	ds_read_b128 v[26:29], v143 offset:8800
	s_waitcnt lgkmcnt(1)
	v_mfma_f32_32x32x16_bf16 v[50:65], v[22:25], v[102:105], v[50:65]
	s_waitcnt lgkmcnt(0)
	v_mfma_f32_32x32x16_bf16 v[50:65], v[26:29], v[106:109], v[50:65]
	ds_read_b128 v[22:25], v143 offset:8832
	ds_read_b128 v[26:29], v143 offset:8864
	s_waitcnt lgkmcnt(1)
	v_mfma_f32_32x32x16_bf16 v[50:65], v[22:25], v[110:113], v[50:65]
	s_waitcnt lgkmcnt(0)
	v_mfma_f32_32x32x16_bf16 v[50:65], v[26:29], v[114:117], v[50:65]
	ds_read_b128 v[22:25], v143 offset:8896
	ds_read_b128 v[26:29], v143 offset:8928
	s_waitcnt lgkmcnt(1)
	v_mfma_f32_32x32x16_bf16 v[50:65], v[22:25], v[118:121], v[50:65]
	s_waitcnt lgkmcnt(0)
	v_mfma_f32_32x32x16_bf16 v[50:65], v[26:29], v[122:125], v[50:65]
	ds_read_b128 v[22:25], v143 offset:17408
	ds_read_b128 v[26:29], v143 offset:17440
	s_waitcnt lgkmcnt(1)
	v_mfma_f32_32x32x16_bf16 v[34:49], v[22:25], v[18:21], 0
	s_waitcnt lgkmcnt(0)
	v_mfma_f32_32x32x16_bf16 v[34:49], v[26:29], v[98:101], v[34:49]
	ds_read_b128 v[22:25], v143 offset:17472
	ds_read_b128 v[26:29], v143 offset:17504
	s_waitcnt lgkmcnt(1)
	v_mfma_f32_32x32x16_bf16 v[34:49], v[22:25], v[102:105], v[34:49]
	s_waitcnt lgkmcnt(0)
	v_mfma_f32_32x32x16_bf16 v[34:49], v[26:29], v[106:109], v[34:49]
	ds_read_b128 v[22:25], v143 offset:17536
	ds_read_b128 v[26:29], v143 offset:17568
	s_waitcnt lgkmcnt(1)
	v_mfma_f32_32x32x16_bf16 v[34:49], v[22:25], v[110:113], v[34:49]
	s_waitcnt lgkmcnt(0)
	v_mfma_f32_32x32x16_bf16 v[34:49], v[26:29], v[114:117], v[34:49]
	ds_read_b128 v[22:25], v143 offset:17600
	ds_read_b128 v[26:29], v143 offset:17632
	s_waitcnt lgkmcnt(1)
	v_mfma_f32_32x32x16_bf16 v[34:49], v[22:25], v[118:121], v[34:49]
	s_waitcnt lgkmcnt(0)
	v_mfma_f32_32x32x16_bf16 v[34:49], v[26:29], v[122:125], v[34:49]
	ds_read_b128 v[22:25], v143 offset:26112
	ds_read_b128 v[150:153], v143 offset:26144
	s_waitcnt lgkmcnt(1)
	v_mfma_f32_32x32x16_bf16 v[18:33], v[22:25], v[18:21], 0
	s_waitcnt lgkmcnt(0)
	v_mfma_f32_32x32x16_bf16 v[18:33], v[150:153], v[98:101], v[18:33]
	ds_read_b128 v[98:101], v143 offset:26176
	ds_read_b128 v[150:153], v143 offset:26208
	s_waitcnt lgkmcnt(1)
	v_mfma_f32_32x32x16_bf16 v[18:33], v[98:101], v[102:105], v[18:33]
	ds_read_b128 v[98:101], v143 offset:26240
	ds_read_b128 v[102:105], v143 offset:26272
	s_waitcnt lgkmcnt(2)
	v_mfma_f32_32x32x16_bf16 v[18:33], v[150:153], v[106:109], v[18:33]
	s_waitcnt lgkmcnt(1)
	v_mfma_f32_32x32x16_bf16 v[18:33], v[98:101], v[110:113], v[18:33]
	s_waitcnt lgkmcnt(0)
	v_mfma_f32_32x32x16_bf16 v[18:33], v[102:105], v[114:117], v[18:33]
	ds_read_b128 v[98:101], v143 offset:26304
	ds_read_b128 v[102:105], v143 offset:26336
	s_waitcnt lgkmcnt(1)
	v_mfma_f32_32x32x16_bf16 v[18:33], v[98:101], v[118:121], v[18:33]
	s_waitcnt lgkmcnt(0)
	v_mfma_f32_32x32x16_bf16 v[18:33], v[102:105], v[122:125], v[18:33]
	v_cndmask_b32_e32 v98, v149, v154, vcc
	v_mul_f32_e32 v2, v2, v98
	v_and_b32_e32 v99, 0xffffff80, v2
	v_mul_f32_e32 v2, v3, v98
	v_and_or_b32 v100, v2, s41, 1
	v_mul_f32_e32 v2, v4, v98
	v_and_or_b32 v101, v2, s41, 2
	v_mul_f32_e32 v2, v5, v98
	v_and_or_b32 v102, v2, s41, 3
	v_mul_f32_e32 v2, v6, v98
	v_and_or_b32 v103, v2, s41, 8
	v_mul_f32_e32 v2, v7, v98
	v_and_or_b32 v104, v2, s41, 9
	v_mul_f32_e32 v2, v8, v98
	v_and_or_b32 v105, v2, s41, 10
	v_mul_f32_e32 v2, v9, v98
	v_and_or_b32 v106, v2, s41, 11
	v_mul_f32_e32 v2, v10, v98
	v_and_or_b32 v107, v2, s41, 16
	v_mul_f32_e32 v2, v11, v98
	v_and_or_b32 v108, v2, s41, 17
	v_mul_f32_e32 v2, v12, v98
	v_and_or_b32 v109, v2, s41, 18
	v_mul_f32_e32 v2, v13, v98
	v_and_or_b32 v110, v2, s41, 19
	v_mul_f32_e32 v2, v14, v98
	v_and_or_b32 v111, v2, s41, 24
	v_mul_f32_e32 v2, v15, v98
	v_and_or_b32 v112, v2, s41, 25
	v_mul_f32_e32 v2, v16, v98
	v_and_or_b32 v113, v2, s41, 26
	v_mul_f32_e32 v2, v17, v98
	v_and_or_b32 v114, v2, s41, 27
	v_mul_f32_e32 v2, v50, v98
	v_and_or_b32 v50, v2, s41, 32
	v_mul_f32_e32 v2, v51, v98
	v_and_or_b32 v51, v2, s41, 33
	v_mul_f32_e32 v2, v52, v98
	v_and_or_b32 v52, v2, s41, 34
	v_mul_f32_e32 v2, v53, v98
	v_and_or_b32 v53, v2, s41, 35
	v_mul_f32_e32 v2, v54, v98
	v_and_or_b32 v54, v2, s41, 40
	v_mul_f32_e32 v2, v55, v98
	v_and_or_b32 v55, v2, s41, 41
	v_mul_f32_e32 v2, v56, v98
	v_and_or_b32 v56, v2, s41, 42
	v_mul_f32_e32 v2, v57, v98
	v_and_or_b32 v57, v2, s41, 43
	v_mul_f32_e32 v2, v58, v98
	v_and_or_b32 v58, v2, s41, 48
	v_mul_f32_e32 v2, v59, v98
	v_and_or_b32 v59, v2, s41, 49
; #define CE_DESC(a, b) do { const float _t = fmaxf(a, b); b = fminf(a, b); a = _t; } while (0)
; __device__ __forceinline__ void sort16_desc(float (&v)[16]) {
; #pragma unroll
;     for (int k = 2; k <= 16; k <<= 1)
; #pragma unroll
;         for (int j = k >> 1; j > 0; j >>= 1)
; #pragma unroll
;             for (int i = 0; i < 16; ++i) { const int l = i ^ j; if (l > i) { if ((i & k) == 0 || k == 16) CE_DESC(v[i], v[l]); else CE_DESC(v[l], v[i]); } }
; }
; __device__ __forceinline__ void route_half(float (&top)[16], LAS const unsigned char* keys_lds, const bf16_t* __restrict__ qrow, int r32, int hi) {
;     ...
;         for (int r = 0; r < 16; ++r) { const unsigned base = (unsigned)(32 * kt + (r & 3) + 8 * (r >> 2)); g[kt][r] = __uint_as_float((__float_as_uint(acc[kt][r] * rn) & 0xFFFFFF80u) | base); }
; #pragma unroll
;     for (int kt = 0; kt < 4; ++kt) sort16_desc(g[kt]);
	v_mul_f32_e32 v2, v60, v98
	v_and_or_b32 v60, v2, s41, 50
	v_mul_f32_e32 v2, v61, v98
	v_and_or_b32 v61, v2, s41, 51
	v_mul_f32_e32 v2, v62, v98
	v_and_or_b32 v62, v2, s41, 56
	v_mul_f32_e32 v2, v63, v98
	v_and_or_b32 v63, v2, s41, 57
	v_mul_f32_e32 v2, v64, v98
	v_and_or_b32 v64, v2, s41, 58
	v_mul_f32_e32 v2, v65, v98
	v_and_or_b32 v65, v2, s41, 59
	v_mul_f32_e32 v2, v34, v98
	v_and_or_b32 v115, v2, s41, 64
	v_mul_f32_e32 v2, v35, v98
	v_and_b32_e32 v2, 0xffffff80, v2
	v_or_b32_e32 v116, 0x41, v2
	v_mul_f32_e32 v2, v36, v98
	v_and_b32_e32 v2, 0xffffff80, v2
	v_or_b32_e32 v117, 0x42, v2
	v_mul_f32_e32 v2, v37, v98
	v_and_b32_e32 v2, 0xffffff80, v2
	v_or_b32_e32 v118, 0x43, v2
	v_mul_f32_e32 v2, v38, v98
	v_and_b32_e32 v2, 0xffffff80, v2
	v_or_b32_e32 v119, 0x48, v2
	v_mul_f32_e32 v2, v39, v98
	v_and_b32_e32 v2, 0xffffff80, v2
	v_or_b32_e32 v120, 0x49, v2
	v_mul_f32_e32 v2, v40, v98
	v_and_b32_e32 v2, 0xffffff80, v2
	v_or_b32_e32 v121, 0x4a, v2
	v_mul_f32_e32 v2, v41, v98
	v_and_b32_e32 v2, 0xffffff80, v2
	v_or_b32_e32 v122, 0x4b, v2
	v_mul_f32_e32 v2, v42, v98
	v_and_b32_e32 v2, 0xffffff80, v2
	v_or_b32_e32 v42, 0x50, v2
	v_mul_f32_e32 v2, v43, v98
	v_and_b32_e32 v2, 0xffffff80, v2
	v_or_b32_e32 v43, 0x51, v2
	v_mul_f32_e32 v2, v44, v98
	v_and_b32_e32 v2, 0xffffff80, v2
	v_or_b32_e32 v44, 0x52, v2
	v_mul_f32_e32 v2, v45, v98
	v_and_b32_e32 v2, 0xffffff80, v2
	v_or_b32_e32 v45, 0x53, v2
	v_mul_f32_e32 v2, v46, v98
	v_and_b32_e32 v2, 0xffffff80, v2
	v_or_b32_e32 v46, 0x58, v2
	v_mul_f32_e32 v2, v47, v98
	v_and_b32_e32 v2, 0xffffff80, v2
	v_or_b32_e32 v47, 0x59, v2
	v_mul_f32_e32 v2, v48, v98
	v_and_b32_e32 v2, 0xffffff80, v2
	v_or_b32_e32 v48, 0x5a, v2
	v_mul_f32_e32 v2, v49, v98
	v_and_b32_e32 v2, 0xffffff80, v2
	v_mul_f32_e32 v3, v98, v19
	v_or_b32_e32 v49, 0x5b, v2
	v_mul_f32_e32 v2, v98, v18
	v_and_b32_e32 v3, 0xffffff80, v3
	v_mul_f32_e32 v5, v98, v21
	v_or_b32_e32 v4, 0x61, v3
	v_mul_f32_e32 v3, v98, v20
	v_and_b32_e32 v5, 0xffffff80, v5
	v_mul_f32_e32 v7, v98, v23
	v_max_f32_e32 v20, v99, v100
	v_min_f32_e32 v18, v99, v100
	v_or_b32_e32 v6, 0x63, v5
	v_mul_f32_e32 v5, v98, v22
	v_and_b32_e32 v7, 0xffffff80, v7
	v_mul_f32_e32 v9, v98, v25
	v_max_f32_e32 v22, v102, v101
	v_min_f32_e32 v19, v102, v101
	v_or_b32_e32 v8, 0x69, v7
	v_mul_f32_e32 v7, v98, v24
	v_and_b32_e32 v9, 0xffffff80, v9
	v_mul_f32_e32 v11, v98, v27
	v_max_f32_e32 v24, v103, v104
	v_min_f32_e32 v21, v103, v104
	v_and_b32_e32 v2, 0xffffff80, v2
	v_or_b32_e32 v10, 0x6b, v9
	v_mul_f32_e32 v9, v98, v26
	v_and_b32_e32 v11, 0xffffff80, v11
	v_mul_f32_e32 v13, v98, v29
	v_max_f32_e32 v26, v106, v105
	v_min_f32_e32 v23, v106, v105
	v_or_b32_e32 v2, 0x60, v2
	v_and_b32_e32 v3, 0xffffff80, v3
	v_or_b32_e32 v12, 0x71, v11
	v_mul_f32_e32 v11, v98, v28
	v_and_b32_e32 v13, 0xffffff80, v13
	v_mul_f32_e32 v15, v98, v31
	v_max_f32_e32 v28, v107, v108
	v_min_f32_e32 v25, v107, v108
	v_or_b32_e32 v3, 0x62, v3
	v_and_b32_e32 v5, 0xffffff80, v5
	v_or_b32_e32 v14, 0x73, v13
	v_mul_f32_e32 v13, v98, v30
	v_and_b32_e32 v15, 0xffffff80, v15
	v_max_f32_e32 v30, v110, v109
	v_min_f32_e32 v27, v110, v109
	v_or_b32_e32 v5, 0x68, v5
	v_and_b32_e32 v7, 0xffffff80, v7
	v_or_b32_e32 v16, 0x79, v15
	v_mul_f32_e32 v15, v98, v32
	v_mul_f32_e32 v17, v98, v33
	v_max_f32_e32 v32, v111, v112
	v_min_f32_e32 v29, v111, v112
	v_max_f32_e32 v31, v113, v113
	v_max_f32_e32 v98, v50, v51
	v_min_f32_e32 v50, v50, v51
	v_max_f32_e32 v51, v52, v52
	v_max_f32_e32 v52, v53, v53
	v_max_f32_e32 v113, v122, v122
	v_max_f32_e32 v122, v2, v4
	v_min_f32_e32 v2, v2, v4
	v_max_f32_e32 v4, v6, v6
	v_or_b32_e32 v7, 0x6a, v7
	v_and_b32_e32 v9, 0xffffff80, v9
	v_max_f32_e32 v53, v52, v51
	v_min_f32_e32 v51, v52, v51
	v_max_f32_e32 v52, v55, v55
	v_max_f32_e32 v108, v115, v116
	v_min_f32_e32 v106, v115, v116
	v_max_f32_e32 v6, v4, v3
	v_min_f32_e32 v3, v4, v3
	v_max_f32_e32 v4, v8, v8
	v_or_b32_e32 v9, 0x70, v9
	v_and_b32_e32 v11, 0xffffff80, v11
	v_max_f32_e32 v55, v54, v52
	v_min_f32_e32 v52, v54, v52
	v_max_f32_e32 v54, v56, v56
	v_max_f32_e32 v56, v57, v57
	v_max_f32_e32 v110, v118, v117
	v_min_f32_e32 v107, v118, v117
	v_max_f32_e32 v8, v5, v4
	v_min_f32_e32 v4, v5, v4
	v_max_f32_e32 v5, v7, v7
	v_max_f32_e32 v7, v10, v10
	v_or_b32_e32 v11, 0x72, v11
	v_and_b32_e32 v13, 0xffffff80, v13
	v_max_f32_e32 v57, v56, v54
	v_min_f32_e32 v54, v56, v54
	v_max_f32_e32 v56, v59, v59
	v_max_f32_e32 v112, v119, v120
	v_min_f32_e32 v109, v119, v120
	v_max_f32_e32 v10, v7, v5
	v_min_f32_e32 v5, v7, v5
	v_max_f32_e32 v7, v12, v12
	v_or_b32_e32 v13, 0x78, v13
	v_and_b32_e32 v15, 0xffffff80, v15
	v_and_b32_e32 v17, 0xffffff80, v17
	v_max_f32_e32 v33, v114, v114
	v_max_f32_e32 v59, v58, v56
	v_min_f32_e32 v56, v58, v56
	v_max_f32_e32 v58, v60, v60
	v_max_f32_e32 v60, v61, v61
	v_max_f32_e32 v114, v113, v121
	v_min_f32_e32 v111, v113, v121
	v_max_f32_e32 v113, v42, v43
	v_min_f32_e32 v42, v42, v43
	v_max_f32_e32 v43, v44, v44
	v_max_f32_e32 v44, v45, v45
	v_max_f32_e32 v12, v9, v7
	v_min_f32_e32 v7, v9, v7
	v_max_f32_e32 v9, v11, v11
	v_max_f32_e32 v11, v14, v14
	v_or_b32_e32 v15, 0x7a, v15
	v_or_b32_e32 v17, 0x7b, v17
	v_max_f32_e32 v61, v60, v58
	v_min_f32_e32 v58, v60, v58
	v_max_f32_e32 v60, v63, v63
	v_max_f32_e32 v45, v44, v43
	v_min_f32_e32 v43, v44, v43
	v_max_f32_e32 v44, v47, v47
	v_max_f32_e32 v14, v11, v9
	v_min_f32_e32 v9, v11, v9
	v_max_f32_e32 v11, v16, v16
	v_max_f32_e32 v63, v62, v60
	v_min_f32_e32 v60, v62, v60
	v_max_f32_e32 v62, v64, v64
	v_max_f32_e32 v64, v65, v65
	v_max_f32_e32 v47, v46, v44
	v_min_f32_e32 v44, v46, v44
	v_max_f32_e32 v46, v48, v48
	v_max_f32_e32 v48, v49, v49
	v_max_f32_e32 v16, v13, v11
; #define CE_DESC(a, b) do { const float _t = fmaxf(a, b); b = fminf(a, b); a = _t; } while (0)
; __device__ __forceinline__ void sort16_desc(float (&v)[16]) {
; #pragma unroll
;     for (int k = 2; k <= 16; k <<= 1)
; #pragma unroll
;         for (int j = k >> 1; j > 0; j >>= 1)
; #pragma unroll
;             for (int i = 0; i < 16; ++i) { const int l = i ^ j; if (l > i) { if ((i & k) == 0 || k == 16) CE_DESC(v[i], v[l]); else CE_DESC(v[l], v[i]); } }
; }
	v_min_f32_e32 v11, v13, v11
	v_max_f32_e32 v13, v15, v15
	v_max_f32_e32 v15, v17, v17
	v_max_f32_e32 v34, v33, v31
	v_min_f32_e32 v31, v33, v31
	v_max_f32_e32 v65, v64, v62
	v_min_f32_e32 v62, v64, v62
	v_max_f32_e32 v49, v48, v46
	v_min_f32_e32 v46, v48, v46
	v_max_f32_e32 v17, v15, v13
	v_min_f32_e32 v13, v15, v13
	v_max_f32_e32 v33, v20, v19
	v_min_f32_e32 v19, v20, v19
	v_max_f32_e32 v20, v18, v22
	v_min_f32_e32 v18, v18, v22
	v_max_f32_e32 v22, v23, v24
	v_min_f32_e32 v23, v23, v24
	v_max_f32_e32 v24, v26, v21
	v_min_f32_e32 v21, v26, v21
	v_max_f32_e32 v26, v28, v27
	v_min_f32_e32 v27, v28, v27
	v_max_f32_e32 v28, v25, v30
	v_min_f32_e32 v25, v25, v30
	v_max_f32_e32 v30, v31, v32
	v_min_f32_e32 v31, v31, v32
	v_max_f32_e32 v32, v34, v29
	v_min_f32_e32 v29, v34, v29
	v_max_f32_e32 v64, v98, v51
	v_min_f32_e32 v51, v98, v51
	v_max_f32_e32 v98, v50, v53
	v_min_f32_e32 v50, v50, v53
	v_max_f32_e32 v53, v54, v55
	v_min_f32_e32 v54, v54, v55
	v_max_f32_e32 v55, v57, v52
	v_min_f32_e32 v52, v57, v52
	v_max_f32_e32 v57, v59, v58
	v_min_f32_e32 v58, v59, v58
	v_max_f32_e32 v59, v56, v61
	v_min_f32_e32 v56, v56, v61
	v_max_f32_e32 v61, v62, v63
	v_min_f32_e32 v62, v62, v63
	v_max_f32_e32 v63, v65, v60
	v_min_f32_e32 v60, v65, v60
	v_max_f32_e32 v48, v108, v107
	v_min_f32_e32 v107, v108, v107
	v_max_f32_e32 v108, v106, v110
	v_min_f32_e32 v106, v106, v110
	v_max_f32_e32 v110, v111, v112
	v_min_f32_e32 v111, v111, v112
	v_max_f32_e32 v112, v114, v109
	v_min_f32_e32 v109, v114, v109
	v_max_f32_e32 v114, v113, v43
	v_min_f32_e32 v43, v113, v43
	v_max_f32_e32 v113, v42, v45
	v_min_f32_e32 v42, v42, v45
	v_max_f32_e32 v45, v46, v47
	v_min_f32_e32 v46, v46, v47
	v_max_f32_e32 v47, v49, v44
	v_min_f32_e32 v44, v49, v44
	v_max_f32_e32 v15, v122, v3
	v_min_f32_e32 v3, v122, v3
	v_max_f32_e32 v122, v2, v6
	v_min_f32_e32 v2, v2, v6
	v_max_f32_e32 v6, v5, v8
	v_min_f32_e32 v5, v5, v8
	v_max_f32_e32 v8, v10, v4
	v_min_f32_e32 v4, v10, v4
	v_max_f32_e32 v10, v12, v9
	v_min_f32_e32 v9, v12, v9
	v_max_f32_e32 v12, v7, v14
	v_min_f32_e32 v7, v7, v14
	v_max_f32_e32 v14, v13, v16
	v_min_f32_e32 v13, v13, v16
	v_max_f32_e32 v16, v17, v11
	v_min_f32_e32 v11, v17, v11
	v_max_f32_e32 v34, v33, v20
	v_min_f32_e32 v20, v33, v20
	v_max_f32_e32 v33, v19, v18
	v_min_f32_e32 v18, v19, v18
	v_max_f32_e32 v19, v21, v23
	v_min_f32_e32 v21, v21, v23
	v_max_f32_e32 v23, v24, v22
	v_min_f32_e32 v22, v24, v22
	v_max_f32_e32 v24, v26, v28
	v_min_f32_e32 v26, v26, v28
	v_max_f32_e32 v28, v27, v25
	v_min_f32_e32 v25, v27, v25
	v_max_f32_e32 v27, v29, v31
	v_min_f32_e32 v29, v29, v31
	v_max_f32_e32 v31, v32, v30
	v_min_f32_e32 v30, v32, v30
	v_max_f32_e32 v65, v64, v98
	v_min_f32_e32 v64, v64, v98
	v_max_f32_e32 v98, v51, v50
	v_min_f32_e32 v50, v51, v50
	v_max_f32_e32 v51, v52, v54
	v_min_f32_e32 v52, v52, v54
	v_max_f32_e32 v54, v55, v53
	v_min_f32_e32 v53, v55, v53
	v_max_f32_e32 v55, v57, v59
	v_min_f32_e32 v57, v57, v59
	v_max_f32_e32 v59, v58, v56
	v_min_f32_e32 v56, v58, v56
	v_max_f32_e32 v58, v60, v62
	v_min_f32_e32 v60, v60, v62
	v_max_f32_e32 v62, v63, v61
	v_min_f32_e32 v61, v63, v61
	v_max_f32_e32 v49, v48, v108
	v_min_f32_e32 v48, v48, v108
	v_max_f32_e32 v108, v107, v106
	v_min_f32_e32 v106, v107, v106
	v_max_f32_e32 v107, v109, v111
	v_min_f32_e32 v109, v109, v111
	v_max_f32_e32 v111, v112, v110
	v_min_f32_e32 v110, v112, v110
	v_max_f32_e32 v112, v114, v113
	v_min_f32_e32 v113, v114, v113
	v_max_f32_e32 v114, v43, v42
	v_min_f32_e32 v42, v43, v42
	v_max_f32_e32 v43, v44, v46
	v_min_f32_e32 v44, v44, v46
	v_max_f32_e32 v46, v47, v45
	v_min_f32_e32 v45, v47, v45
	v_max_f32_e32 v17, v15, v122
	v_min_f32_e32 v15, v15, v122
	v_max_f32_e32 v122, v3, v2
	v_min_f32_e32 v2, v3, v2
	v_max_f32_e32 v3, v4, v5
	v_min_f32_e32 v4, v4, v5
	v_max_f32_e32 v5, v8, v6
	v_min_f32_e32 v6, v8, v6
	v_max_f32_e32 v8, v10, v12
	v_min_f32_e32 v10, v10, v12
	v_max_f32_e32 v12, v9, v7
	v_min_f32_e32 v7, v9, v7
	v_max_f32_e32 v9, v11, v13
	v_min_f32_e32 v11, v11, v13
	v_max_f32_e32 v13, v16, v14
	v_min_f32_e32 v14, v16, v14
	v_max_f32_e32 v32, v34, v21
	v_min_f32_e32 v21, v34, v21
	v_max_f32_e32 v34, v20, v19
	v_min_f32_e32 v19, v20, v19
	v_max_f32_e32 v20, v33, v22
	v_min_f32_e32 v22, v33, v22
	v_max_f32_e32 v33, v18, v23
	v_min_f32_e32 v18, v18, v23
	v_max_f32_e32 v23, v29, v24
	v_min_f32_e32 v24, v29, v24
	v_max_f32_e32 v29, v27, v26
	v_min_f32_e32 v26, v27, v26
	v_max_f32_e32 v27, v30, v28
	v_min_f32_e32 v28, v30, v28
	v_max_f32_e32 v30, v31, v25
	v_min_f32_e32 v25, v31, v25
	v_max_f32_e32 v63, v65, v52
	v_min_f32_e32 v52, v65, v52
	v_max_f32_e32 v65, v64, v51
	v_min_f32_e32 v51, v64, v51
	v_max_f32_e32 v64, v98, v53
	v_min_f32_e32 v53, v98, v53
	v_max_f32_e32 v98, v50, v54
	v_min_f32_e32 v50, v50, v54
	v_max_f32_e32 v54, v60, v55
	v_min_f32_e32 v55, v60, v55
	v_max_f32_e32 v60, v58, v57
	v_min_f32_e32 v57, v58, v57
	v_max_f32_e32 v58, v61, v59
	v_min_f32_e32 v59, v61, v59
	v_max_f32_e32 v61, v62, v56
	v_min_f32_e32 v56, v62, v56
	v_max_f32_e32 v47, v49, v109
	v_min_f32_e32 v49, v49, v109
	v_max_f32_e32 v109, v48, v107
	v_min_f32_e32 v48, v48, v107
	v_max_f32_e32 v107, v108, v110
	v_min_f32_e32 v108, v108, v110
	v_max_f32_e32 v110, v106, v111
	v_min_f32_e32 v106, v106, v111
	v_max_f32_e32 v111, v44, v112
	v_min_f32_e32 v44, v44, v112
	v_max_f32_e32 v112, v43, v113
	v_min_f32_e32 v43, v43, v113
	v_max_f32_e32 v113, v45, v114
	v_min_f32_e32 v45, v45, v114
	v_max_f32_e32 v114, v46, v42
	v_min_f32_e32 v42, v46, v42
	v_max_f32_e32 v16, v17, v4
	v_min_f32_e32 v4, v17, v4
	v_max_f32_e32 v17, v15, v3
	v_min_f32_e32 v3, v15, v3
	v_max_f32_e32 v15, v122, v6
	v_min_f32_e32 v6, v122, v6
; #define CE_DESC(a, b) do { const float _t = fmaxf(a, b); b = fminf(a, b); a = _t; } while (0)
; __device__ __forceinline__ void sort16_desc(float (&v)[16]) {
; #pragma unroll
;     for (int k = 2; k <= 16; k <<= 1)
; #pragma unroll
;         for (int j = k >> 1; j > 0; j >>= 1)
; #pragma unroll
;             for (int i = 0; i < 16; ++i) { const int l = i ^ j; if (l > i) { if ((i & k) == 0 || k == 16) CE_DESC(v[i], v[l]); else CE_DESC(v[l], v[i]); } }
; }
	v_max_f32_e32 v122, v2, v5
	v_min_f32_e32 v2, v2, v5
	v_max_f32_e32 v5, v11, v8
	v_min_f32_e32 v8, v11, v8
	v_max_f32_e32 v11, v9, v10
	v_min_f32_e32 v9, v9, v10
	v_max_f32_e32 v10, v14, v12
	v_min_f32_e32 v12, v14, v12
	v_max_f32_e32 v14, v13, v7
	v_min_f32_e32 v7, v13, v7
	v_max_f32_e32 v31, v32, v20
	v_min_f32_e32 v20, v32, v20
	v_max_f32_e32 v32, v34, v33
	v_min_f32_e32 v33, v34, v33
	v_max_f32_e32 v34, v21, v22
	v_min_f32_e32 v21, v21, v22
	v_max_f32_e32 v22, v19, v18
	v_min_f32_e32 v18, v19, v18
	v_max_f32_e32 v19, v28, v24
	v_min_f32_e32 v24, v28, v24
	v_max_f32_e32 v28, v25, v26
	v_min_f32_e32 v25, v25, v26
	v_max_f32_e32 v26, v27, v23
	v_min_f32_e32 v23, v27, v23
	v_max_f32_e32 v27, v30, v29
	v_min_f32_e32 v29, v30, v29
	v_max_f32_e32 v62, v63, v64
	v_min_f32_e32 v63, v63, v64
	v_max_f32_e32 v64, v65, v98
	v_min_f32_e32 v65, v65, v98
	v_max_f32_e32 v98, v52, v53
	v_min_f32_e32 v52, v52, v53
	v_max_f32_e32 v53, v51, v50
	v_min_f32_e32 v50, v51, v50
	v_max_f32_e32 v51, v59, v55
	v_min_f32_e32 v55, v59, v55
	v_max_f32_e32 v59, v56, v57
	v_min_f32_e32 v56, v56, v57
	v_max_f32_e32 v57, v58, v54
	v_min_f32_e32 v54, v58, v54
	v_max_f32_e32 v58, v61, v60
	v_min_f32_e32 v60, v61, v60
	v_max_f32_e32 v46, v47, v107
	v_min_f32_e32 v47, v47, v107
	v_max_f32_e32 v107, v109, v110
	v_min_f32_e32 v109, v109, v110
	v_max_f32_e32 v110, v49, v108
	v_min_f32_e32 v49, v49, v108
	v_max_f32_e32 v108, v48, v106
	v_min_f32_e32 v48, v48, v106
	v_max_f32_e32 v106, v45, v44
	v_min_f32_e32 v44, v45, v44
	v_max_f32_e32 v45, v42, v43
	v_min_f32_e32 v42, v42, v43
	v_max_f32_e32 v43, v113, v111
	v_min_f32_e32 v111, v113, v111
	v_max_f32_e32 v113, v114, v112
	v_min_f32_e32 v112, v114, v112
	v_max_f32_e32 v13, v16, v15
	v_min_f32_e32 v15, v16, v15
	v_max_f32_e32 v16, v17, v122
	v_min_f32_e32 v17, v17, v122
	v_max_f32_e32 v122, v4, v6
	v_min_f32_e32 v4, v4, v6
	v_max_f32_e32 v6, v3, v2
	v_min_f32_e32 v2, v3, v2
	v_max_f32_e32 v3, v12, v8
	v_min_f32_e32 v8, v12, v8
	v_max_f32_e32 v12, v7, v9
	v_min_f32_e32 v7, v7, v9
	v_max_f32_e32 v9, v10, v5
	v_min_f32_e32 v5, v10, v5
	v_max_f32_e32 v10, v14, v11
	v_min_f32_e32 v11, v14, v11
	v_max_f32_e32 v30, v31, v32
	v_min_f32_e32 v31, v31, v32
	v_max_f32_e32 v32, v20, v33
	v_min_f32_e32 v20, v20, v33
	v_max_f32_e32 v33, v34, v22
	v_min_f32_e32 v22, v34, v22
	v_max_f32_e32 v34, v21, v18
	v_min_f32_e32 v18, v21, v18
	v_max_f32_e32 v21, v25, v24
	v_min_f32_e32 v24, v25, v24
	v_max_f32_e32 v25, v28, v19
	v_min_f32_e32 v19, v28, v19
	v_max_f32_e32 v28, v29, v23
	v_min_f32_e32 v23, v29, v23
	v_max_f32_e32 v29, v27, v26
	v_min_f32_e32 v26, v27, v26
	v_max_f32_e32 v61, v62, v64
	v_min_f32_e32 v62, v62, v64
	v_max_f32_e32 v64, v63, v65
	v_min_f32_e32 v63, v63, v65
	v_max_f32_e32 v65, v98, v53
	v_min_f32_e32 v53, v98, v53
	v_max_f32_e32 v98, v52, v50
	v_min_f32_e32 v50, v52, v50
	v_max_f32_e32 v52, v56, v55
	v_min_f32_e32 v55, v56, v55
	v_max_f32_e32 v56, v59, v51
	v_min_f32_e32 v51, v59, v51
	v_max_f32_e32 v59, v60, v54
	v_min_f32_e32 v54, v60, v54
	v_max_f32_e32 v60, v58, v57
	v_min_f32_e32 v57, v58, v57
	v_max_f32_e32 v114, v46, v107
	v_min_f32_e32 v46, v46, v107
	v_max_f32_e32 v107, v47, v109
	v_min_f32_e32 v47, v47, v109
	v_max_f32_e32 v109, v110, v108
	v_min_f32_e32 v108, v110, v108
	v_max_f32_e32 v110, v49, v48
	v_min_f32_e32 v48, v49, v48
	v_max_f32_e32 v49, v42, v44
	v_min_f32_e32 v42, v42, v44
	v_max_f32_e32 v44, v45, v106
	v_min_f32_e32 v45, v45, v106
	v_max_f32_e32 v106, v112, v111
	v_min_f32_e32 v111, v112, v111
	v_max_f32_e32 v112, v113, v43
	v_min_f32_e32 v43, v113, v43
	v_max_f32_e32 v14, v13, v16
	v_min_f32_e32 v13, v13, v16
	v_max_f32_e32 v16, v15, v17
	v_min_f32_e32 v15, v15, v17
	v_max_f32_e32 v17, v122, v6
	v_min_f32_e32 v6, v122, v6
	v_max_f32_e32 v122, v4, v2
	v_min_f32_e32 v2, v4, v2
	v_max_f32_e32 v4, v7, v8
	v_min_f32_e32 v7, v7, v8
	v_max_f32_e32 v8, v12, v3
	v_min_f32_e32 v3, v12, v3
	v_max_f32_e32 v12, v11, v5
	v_min_f32_e32 v5, v11, v5
	v_max_f32_e32 v11, v10, v9
	v_min_f32_e32 v9, v10, v9
	v_max_f32_e32 v27, v30, v24
	v_min_f32_e32 v24, v30, v24
	v_max_f32_e32 v30, v31, v21
	v_min_f32_e32 v21, v31, v21
	v_max_f32_e32 v31, v32, v19
	v_min_f32_e32 v19, v32, v19
	v_max_f32_e32 v32, v20, v25
	v_min_f32_e32 v20, v20, v25
	v_max_f32_e32 v25, v33, v23
	v_min_f32_e32 v23, v33, v23
	v_max_f32_e32 v33, v22, v28
	v_min_f32_e32 v22, v22, v28
	v_max_f32_e32 v28, v34, v26
	v_min_f32_e32 v26, v34, v26
	v_max_f32_e32 v34, v18, v29
	v_min_f32_e32 v18, v18, v29
	v_max_f32_e32 v58, v61, v55
	v_min_f32_e32 v55, v61, v55
	v_max_f32_e32 v61, v62, v52
	v_min_f32_e32 v52, v62, v52
	v_max_f32_e32 v62, v64, v51
	v_min_f32_e32 v51, v64, v51
	v_max_f32_e32 v64, v63, v56
	v_min_f32_e32 v56, v63, v56
	v_max_f32_e32 v63, v65, v54
	v_min_f32_e32 v54, v65, v54
	v_max_f32_e32 v65, v53, v59
	v_min_f32_e32 v53, v53, v59
	v_max_f32_e32 v59, v98, v57
	v_min_f32_e32 v57, v98, v57
	v_max_f32_e32 v98, v50, v60
	v_min_f32_e32 v50, v50, v60
	v_max_f32_e32 v113, v114, v42
	v_min_f32_e32 v42, v114, v42
	v_max_f32_e32 v114, v46, v49
	v_min_f32_e32 v46, v46, v49
	v_max_f32_e32 v49, v107, v45
	v_min_f32_e32 v45, v107, v45
	v_max_f32_e32 v107, v47, v44
	v_min_f32_e32 v44, v47, v44
	v_max_f32_e32 v47, v109, v111
	v_min_f32_e32 v109, v109, v111
	v_max_f32_e32 v111, v108, v106
	v_min_f32_e32 v106, v108, v106
	v_max_f32_e32 v108, v110, v43
	v_min_f32_e32 v43, v110, v43
	v_max_f32_e32 v110, v48, v112
	v_min_f32_e32 v48, v48, v112
	v_max_f32_e32 v10, v14, v7
	v_min_f32_e32 v7, v14, v7
	v_max_f32_e32 v14, v13, v4
	v_min_f32_e32 v4, v13, v4
	v_max_f32_e32 v13, v16, v3
	v_min_f32_e32 v3, v16, v3
	v_max_f32_e32 v16, v15, v8
	v_min_f32_e32 v8, v15, v8
; #define CE_DESC(a, b) do { const float _t = fmaxf(a, b); b = fminf(a, b); a = _t; } while (0)
; __device__ __forceinline__ void sort16_desc(float (&v)[16]) {
; #pragma unroll
;     for (int k = 2; k <= 16; k <<= 1)
; #pragma unroll
;         for (int j = k >> 1; j > 0; j >>= 1)
; #pragma unroll
;             for (int i = 0; i < 16; ++i) { const int l = i ^ j; if (l > i) { if ((i & k) == 0 || k == 16) CE_DESC(v[i], v[l]); else CE_DESC(v[l], v[i]); } }
; }
; __device__ __forceinline__ void merge16_desc(float (&a)[16], const float (&b)[16]) {
; #pragma unroll
;     for (int i = 0; i < 16; ++i) a[i] = fmaxf(a[i], b[15 - i]);
; #pragma unroll
;     for (int j = 8; j > 0; j >>= 1)
; #pragma unroll
;         for (int i = 0; i < 16; ++i) { const int l = i ^ j; if (l > i) CE_DESC(a[i], a[l]); }
; }
	v_max_f32_e32 v15, v17, v5
	v_min_f32_e32 v5, v17, v5
	v_max_f32_e32 v17, v6, v12
	v_min_f32_e32 v6, v6, v12
	v_max_f32_e32 v12, v122, v9
	v_min_f32_e32 v9, v122, v9
	v_max_f32_e32 v122, v2, v11
	v_min_f32_e32 v2, v2, v11
	v_max_f32_e32 v29, v27, v25
	v_min_f32_e32 v25, v27, v25
	v_max_f32_e32 v27, v30, v33
	v_min_f32_e32 v33, v30, v33
	v_max_f32_e32 v30, v31, v28
	v_min_f32_e32 v28, v31, v28
	v_max_f32_e32 v31, v32, v34
	v_min_f32_e32 v32, v32, v34
	v_max_f32_e32 v34, v24, v23
	v_min_f32_e32 v35, v24, v23
	v_max_f32_e32 v36, v21, v22
	v_min_f32_e32 v37, v21, v22
	v_max_f32_e32 v21, v19, v26
	v_min_f32_e32 v38, v19, v26
	v_max_f32_e32 v39, v20, v18
	v_min_f32_e32 v40, v20, v18
	v_max_f32_e32 v60, v58, v63
	v_min_f32_e32 v58, v58, v63
	v_max_f32_e32 v63, v61, v65
	v_min_f32_e32 v61, v61, v65
	v_max_f32_e32 v65, v62, v59
	v_min_f32_e32 v59, v62, v59
	v_max_f32_e32 v62, v64, v98
	v_min_f32_e32 v64, v64, v98
	v_max_f32_e32 v98, v55, v54
	v_min_f32_e32 v54, v55, v54
	v_max_f32_e32 v55, v52, v53
	v_min_f32_e32 v52, v52, v53
	v_max_f32_e32 v53, v51, v57
	v_min_f32_e32 v51, v51, v57
	v_max_f32_e32 v57, v56, v50
	v_min_f32_e32 v50, v56, v50
	v_max_f32_e32 v112, v113, v47
	v_min_f32_e32 v47, v113, v47
	v_max_f32_e32 v113, v114, v111
	v_min_f32_e32 v111, v114, v111
	v_max_f32_e32 v114, v49, v108
	v_min_f32_e32 v49, v49, v108
	v_max_f32_e32 v108, v107, v110
	v_min_f32_e32 v107, v107, v110
	v_max_f32_e32 v110, v42, v109
	v_min_f32_e32 v42, v42, v109
	v_max_f32_e32 v109, v46, v106
	v_min_f32_e32 v46, v46, v106
	v_max_f32_e32 v106, v45, v43
	v_min_f32_e32 v43, v45, v43
	v_max_f32_e32 v45, v44, v48
	v_min_f32_e32 v44, v44, v48
	v_max_f32_e32 v11, v10, v15
	v_min_f32_e32 v10, v10, v15
	v_max_f32_e32 v15, v14, v17
	v_min_f32_e32 v14, v14, v17
	v_max_f32_e32 v17, v13, v12
	v_min_f32_e32 v12, v13, v12
	v_max_f32_e32 v13, v16, v122
	v_min_f32_e32 v16, v16, v122
	v_max_f32_e32 v122, v7, v5
	v_min_f32_e32 v5, v7, v5
	v_max_f32_e32 v7, v4, v6
	v_min_f32_e32 v4, v4, v6
	v_max_f32_e32 v6, v3, v9
	v_min_f32_e32 v3, v3, v9
	v_max_f32_e32 v9, v8, v2
	v_min_f32_e32 v2, v8, v2
	v_max_f32_e32 v22, v29, v30
	v_min_f32_e32 v18, v29, v30
	v_max_f32_e32 v30, v27, v31
	v_min_f32_e32 v26, v27, v31
	v_max_f32_e32 v23, v25, v28
	v_min_f32_e32 v19, v25, v28
	v_max_f32_e32 v31, v33, v32
	v_min_f32_e32 v27, v33, v32
	v_max_f32_e32 v24, v34, v21
	v_min_f32_e32 v20, v34, v21
	v_max_f32_e32 v32, v36, v39
	v_min_f32_e32 v28, v36, v39
	v_max_f32_e32 v25, v35, v38
	v_min_f32_e32 v21, v35, v38
	v_max_f32_e32 v33, v37, v40
	v_min_f32_e32 v29, v37, v40
	v_max_f32_e32 v56, v60, v65
	v_min_f32_e32 v60, v60, v65
	v_max_f32_e32 v65, v63, v62
	v_min_f32_e32 v62, v63, v62
	v_max_f32_e32 v63, v58, v59
	v_min_f32_e32 v58, v58, v59
	v_max_f32_e32 v59, v61, v64
	v_min_f32_e32 v61, v61, v64
	v_max_f32_e32 v64, v98, v53
	v_min_f32_e32 v53, v98, v53
	v_max_f32_e32 v98, v55, v57
	v_min_f32_e32 v55, v55, v57
	v_max_f32_e32 v57, v54, v51
	v_min_f32_e32 v51, v54, v51
	v_max_f32_e32 v54, v52, v50
	v_min_f32_e32 v50, v52, v50
	v_max_f32_e32 v48, v112, v114
	v_min_f32_e32 v112, v112, v114
	v_max_f32_e32 v114, v113, v108
	v_min_f32_e32 v108, v113, v108
	v_max_f32_e32 v113, v47, v49
	v_min_f32_e32 v47, v47, v49
	v_max_f32_e32 v49, v111, v107
	v_min_f32_e32 v107, v111, v107
	v_max_f32_e32 v111, v110, v106
	v_min_f32_e32 v106, v110, v106
	v_max_f32_e32 v110, v109, v45
	v_min_f32_e32 v45, v109, v45
	v_max_f32_e32 v109, v42, v43
	v_min_f32_e32 v42, v42, v43
	v_max_f32_e32 v43, v46, v44
	v_min_f32_e32 v44, v46, v44
	v_max_f32_e32 v8, v11, v17
	v_min_f32_e32 v11, v11, v17
	v_max_f32_e32 v17, v15, v13
	v_min_f32_e32 v13, v15, v13
	v_max_f32_e32 v15, v10, v12
	v_min_f32_e32 v10, v10, v12
	v_max_f32_e32 v12, v14, v16
	v_min_f32_e32 v14, v14, v16
	v_max_f32_e32 v16, v122, v6
	v_min_f32_e32 v6, v122, v6
	v_max_f32_e32 v122, v7, v9
	v_min_f32_e32 v7, v7, v9
	v_max_f32_e32 v9, v5, v3
	v_min_f32_e32 v3, v5, v3
	v_max_f32_e32 v5, v4, v2
	v_min_f32_e32 v2, v4, v2
	v_min_f32_e32 v41, v22, v30
	v_min_f32_e32 v40, v18, v26
	v_min_f32_e32 v39, v23, v31
	v_min_f32_e32 v38, v19, v27
	v_min_f32_e32 v37, v24, v32
	v_min_f32_e32 v36, v20, v28
	v_min_f32_e32 v35, v25, v33
	v_min_f32_e32 v34, v21, v29
	v_min_f32_e32 v52, v56, v65
	v_min_f32_e32 v99, v60, v62
	v_min_f32_e32 v100, v63, v59
	v_min_f32_e32 v101, v58, v61
	v_min_f32_e32 v102, v64, v98
	v_min_f32_e32 v103, v53, v55
	v_min_f32_e32 v104, v57, v54
	v_min_f32_e32 v105, v51, v50
	v_min_f32_e32 v46, v48, v114
	v_min_f32_e32 v115, v112, v108
	v_min_f32_e32 v116, v113, v49
	v_min_f32_e32 v117, v47, v107
	v_min_f32_e32 v118, v111, v110
	v_min_f32_e32 v119, v106, v45
	v_min_f32_e32 v120, v109, v43
	v_min_f32_e32 v121, v42, v44
	v_min_f32_e32 v4, v8, v17
	v_min_f32_e32 v123, v11, v13
	v_min_f32_e32 v124, v15, v12
	v_min_f32_e32 v125, v10, v14
	v_min_f32_e32 v149, v16, v122
	v_min_f32_e32 v150, v6, v7
	v_min_f32_e32 v151, v9, v5
	v_min_f32_e32 v152, v3, v2
	v_max3_f32 v22, v22, v30, v105
	v_max3_f32 v30, v41, v51, v50
	v_max3_f32 v18, v18, v26, v104
	v_max3_f32 v26, v40, v57, v54
	v_max3_f32 v23, v23, v31, v103
	v_max3_f32 v31, v39, v53, v55
	v_max3_f32 v19, v19, v27, v102
	v_max3_f32 v27, v38, v64, v98
	v_max3_f32 v24, v24, v32, v101
	v_max3_f32 v32, v37, v58, v61
	v_max3_f32 v20, v20, v28, v100
	v_max3_f32 v28, v36, v63, v59
	v_max3_f32 v25, v25, v33, v99
	v_max3_f32 v33, v35, v60, v62
	v_max3_f32 v21, v21, v29, v52
	v_max3_f32 v29, v34, v56, v65
	v_max3_f32 v48, v48, v114, v152
	v_max3_f32 v2, v46, v3, v2
	v_max3_f32 v3, v112, v108, v151
	v_max3_f32 v5, v115, v9, v5
	v_max3_f32 v9, v113, v49, v150
	v_max3_f32 v6, v116, v6, v7
	v_max3_f32 v7, v47, v107, v149
	v_max3_f32 v16, v117, v16, v122
; #define CE_DESC(a, b) do { const float _t = fmaxf(a, b); b = fminf(a, b); a = _t; } while (0)
; __device__ __forceinline__ void merge16_desc(float (&a)[16], const float (&b)[16]) {
; #pragma unroll
;     for (int i = 0; i < 16; ++i) a[i] = fmaxf(a[i], b[15 - i]);
; #pragma unroll
;     for (int j = 8; j > 0; j >>= 1)
; #pragma unroll
;         for (int i = 0; i < 16; ++i) { const int l = i ^ j; if (l > i) CE_DESC(a[i], a[l]); }
; }
; __device__ __forceinline__ void route_half(float (&top)[16], LAS const unsigned char* keys_lds, const bf16_t* __restrict__ qrow, int r32, int hi) {
;     ...
;     merge16_desc(g[0], g[1]); merge16_desc(g[2], g[3]); merge16_desc(g[0], g[2]);
;     float o[16];
; #pragma unroll
;     for (int i = 0; i < 16; ++i) { g[0][i] = __uint_as_float(__float_as_uint(g[0][i]) | hi4); o[i] = __shfl_xor(g[0][i], 32); }
;     merge16_desc(g[0], o);
	v_max3_f32 v46, v111, v110, v125
	v_max3_f32 v10, v118, v10, v14
	v_max3_f32 v14, v106, v45, v124
	v_max3_f32 v12, v119, v15, v12
	v_max3_f32 v15, v109, v43, v123
	v_max3_f32 v11, v120, v11, v13
	v_max3_f32 v4, v42, v44, v4
	v_max3_f32 v8, v121, v8, v17
	v_max_f32_e32 v34, v22, v24
	v_min_f32_e32 v22, v22, v24
	v_max_f32_e32 v24, v30, v32
	v_min_f32_e32 v30, v30, v32
	v_max_f32_e32 v32, v18, v20
	v_min_f32_e32 v18, v18, v20
	v_max_f32_e32 v20, v26, v28
	v_min_f32_e32 v26, v26, v28
	v_max_f32_e32 v28, v23, v25
	v_min_f32_e32 v23, v23, v25
	v_max_f32_e32 v25, v31, v33
	v_min_f32_e32 v31, v31, v33
	v_max_f32_e32 v33, v19, v21
	v_min_f32_e32 v19, v19, v21
	v_max_f32_e32 v21, v27, v29
	v_min_f32_e32 v27, v27, v29
	v_max_f32_e32 v13, v48, v46
	v_min_f32_e32 v17, v48, v46
	v_max_f32_e32 v42, v2, v10
	v_min_f32_e32 v2, v2, v10
	v_max_f32_e32 v10, v3, v14
	v_min_f32_e32 v3, v3, v14
	v_max_f32_e32 v14, v5, v12
	v_min_f32_e32 v5, v5, v12
	v_max_f32_e32 v12, v9, v15
	v_min_f32_e32 v9, v9, v15
	v_max_f32_e32 v15, v6, v11
	v_min_f32_e32 v6, v6, v11
	v_max_f32_e32 v11, v7, v4
	v_min_f32_e32 v4, v7, v4
	v_max_f32_e32 v7, v16, v8
	v_min_f32_e32 v8, v16, v8
	v_max_f32_e32 v29, v34, v28
	v_min_f32_e32 v28, v34, v28
	v_max_f32_e32 v34, v24, v25
	v_min_f32_e32 v24, v24, v25
	v_max_f32_e32 v25, v32, v33
	v_min_f32_e32 v32, v32, v33
	v_max_f32_e32 v33, v20, v21
	v_min_f32_e32 v20, v20, v21
	v_max_f32_e32 v21, v22, v23
	v_min_f32_e32 v22, v22, v23
	v_max_f32_e32 v23, v30, v31
	v_min_f32_e32 v30, v30, v31
	v_max_f32_e32 v31, v18, v19
	v_min_f32_e32 v18, v18, v19
	v_max_f32_e32 v19, v26, v27
	v_min_f32_e32 v26, v26, v27
	v_max_f32_e32 v16, v13, v12
	v_min_f32_e32 v12, v13, v12
	v_max_f32_e32 v13, v42, v15
	v_min_f32_e32 v15, v42, v15
	v_max_f32_e32 v42, v10, v11
	v_min_f32_e32 v10, v10, v11
	v_max_f32_e32 v11, v14, v7
	v_min_f32_e32 v7, v14, v7
	v_max_f32_e32 v14, v17, v9
	v_min_f32_e32 v9, v17, v9
	v_max_f32_e32 v17, v2, v6
	v_min_f32_e32 v2, v2, v6
	v_max_f32_e32 v6, v3, v4
	v_min_f32_e32 v3, v3, v4
	v_max_f32_e32 v4, v5, v8
	v_min_f32_e32 v5, v5, v8
	v_max_f32_e32 v27, v29, v25
	v_min_f32_e32 v25, v29, v25
	v_max_f32_e32 v29, v34, v33
	v_min_f32_e32 v33, v34, v33
	v_max_f32_e32 v34, v28, v32
	v_min_f32_e32 v28, v28, v32
	v_max_f32_e32 v32, v24, v20
	v_min_f32_e32 v20, v24, v20
	v_max_f32_e32 v24, v21, v31
	v_min_f32_e32 v21, v21, v31
	v_max_f32_e32 v31, v23, v19
	v_min_f32_e32 v19, v23, v19
	v_max_f32_e32 v23, v22, v18
	v_min_f32_e32 v18, v22, v18
	v_max_f32_e32 v22, v30, v26
	v_min_f32_e32 v26, v30, v26
	v_max_f32_e32 v8, v16, v42
	v_min_f32_e32 v16, v16, v42
	v_max_f32_e32 v42, v13, v11
	v_min_f32_e32 v11, v13, v11
	v_max_f32_e32 v13, v12, v10
	v_min_f32_e32 v10, v12, v10
	v_max_f32_e32 v12, v15, v7
	v_min_f32_e32 v7, v15, v7
	v_max_f32_e32 v15, v14, v6
	v_min_f32_e32 v6, v14, v6
	v_max_f32_e32 v14, v17, v4
	v_min_f32_e32 v4, v17, v4
	v_max_f32_e32 v17, v9, v3
	v_min_f32_e32 v3, v9, v3
	v_max_f32_e32 v9, v2, v5
	v_min_f32_e32 v2, v2, v5
	v_min_f32_e32 v30, v27, v29
	v_min_f32_e32 v35, v25, v33
	v_min_f32_e32 v36, v34, v32
	v_min_f32_e32 v37, v28, v20
	v_min_f32_e32 v38, v24, v31
	v_min_f32_e32 v39, v21, v19
	v_min_f32_e32 v40, v23, v22
	v_min_f32_e32 v41, v18, v26
	v_min_f32_e32 v5, v8, v42
	v_min_f32_e32 v43, v16, v11
	v_min_f32_e32 v44, v13, v12
	v_min_f32_e32 v45, v10, v7
	v_min_f32_e32 v46, v15, v14
	v_min_f32_e32 v47, v6, v4
	v_min_f32_e32 v48, v17, v9
	v_min_f32_e32 v49, v3, v2
	v_max3_f32 v27, v27, v29, v49
	v_max3_f32 v2, v30, v3, v2
	v_max3_f32 v3, v25, v33, v48
	v_max3_f32 v9, v35, v17, v9
	v_max3_f32 v17, v34, v32, v47
	v_max3_f32 v4, v36, v6, v4
	v_max3_f32 v6, v28, v20, v46
	v_max3_f32 v14, v37, v15, v14
	v_max3_f32 v15, v24, v31, v45
	v_max3_f32 v7, v38, v10, v7
	v_max3_f32 v10, v21, v19, v44
	v_max3_f32 v12, v39, v13, v12
	v_max3_f32 v13, v23, v22, v43
	v_max3_f32 v11, v40, v16, v11
	v_max3_f32 v5, v18, v26, v5
	v_max3_f32 v8, v41, v8, v42
	v_max_f32_e32 v16, v27, v15
	v_min_f32_e32 v15, v27, v15
	v_max_f32_e32 v18, v2, v7
	v_min_f32_e32 v2, v2, v7
	v_max_f32_e32 v7, v3, v10
	v_min_f32_e32 v3, v3, v10
	v_max_f32_e32 v10, v9, v12
	v_min_f32_e32 v9, v9, v12
	v_max_f32_e32 v12, v17, v13
	v_min_f32_e32 v13, v17, v13
	v_max_f32_e32 v17, v4, v11
	v_min_f32_e32 v4, v4, v11
	v_max_f32_e32 v11, v6, v5
	v_min_f32_e32 v5, v6, v5
	v_max_f32_e32 v6, v14, v8
	v_min_f32_e32 v8, v14, v8
	v_max_f32_e32 v14, v16, v12
	v_min_f32_e32 v12, v16, v12
	v_max_f32_e32 v16, v18, v17
	v_min_f32_e32 v17, v18, v17
	v_max_f32_e32 v18, v7, v11
	v_min_f32_e32 v7, v7, v11
	v_max_f32_e32 v11, v10, v6
	v_min_f32_e32 v6, v10, v6
	v_max_f32_e32 v10, v15, v13
	v_min_f32_e32 v13, v15, v13
	v_max_f32_e32 v15, v2, v4
	v_min_f32_e32 v2, v2, v4
	v_max_f32_e32 v4, v3, v5
	v_min_f32_e32 v3, v3, v5
	v_max_f32_e32 v5, v9, v8
	v_min_f32_e32 v8, v9, v8
	v_max_f32_e32 v9, v14, v18
	v_min_f32_e32 v14, v14, v18
	v_max_f32_e32 v18, v16, v11
	v_min_f32_e32 v11, v16, v11
	v_max_f32_e32 v16, v12, v7
	v_min_f32_e32 v7, v12, v7
	v_max_f32_e32 v12, v17, v6
	v_min_f32_e32 v6, v17, v6
	v_max_f32_e32 v17, v10, v4
	v_min_f32_e32 v4, v10, v4
	v_max_f32_e32 v10, v15, v5
	v_min_f32_e32 v5, v15, v5
	v_max_f32_e32 v15, v13, v3
	v_min_f32_e32 v3, v13, v3
	v_max_f32_e32 v13, v2, v8
	v_min_f32_e32 v2, v2, v8
	v_max_f32_e32 v8, v9, v18
	v_min_f32_e32 v9, v9, v18
	v_max_f32_e32 v18, v14, v11
	v_min_f32_e32 v11, v14, v11
	v_max_f32_e32 v14, v16, v12
	v_min_f32_e32 v12, v16, v12
	v_max_f32_e32 v16, v7, v6
	v_min_f32_e32 v6, v7, v6
	v_max_f32_e32 v7, v17, v10
	v_min_f32_e32 v10, v17, v10
	v_max_f32_e32 v17, v4, v5
	v_min_f32_e32 v4, v4, v5
	v_max_f32_e32 v5, v15, v13
	v_min_f32_e32 v13, v15, v13
	v_max_f32_e32 v15, v3, v2
	v_min_f32_e32 v2, v3, v2
	v_or_b32_e32 v173, v144, v8
	v_or_b32_e32 v172, v144, v9
	v_or_b32_e32 v171, v144, v18
	v_or_b32_e32 v169, v144, v11
	v_or_b32_e32 v168, v144, v14
	v_or_b32_e32 v167, v144, v12
	v_or_b32_e32 v166, v144, v16
	v_or_b32_e32 v165, v144, v6
	v_or_b32_e32 v164, v144, v7
	v_or_b32_e32 v162, v144, v10
	v_or_b32_e32 v161, v144, v17
	v_or_b32_e32 v160, v144, v4
	v_or_b32_e32 v159, v144, v5
	v_or_b32_e32 v158, v144, v13
	v_or_b32_e32 v156, v144, v15
	v_or_b32_e32 v155, v144, v2
	ds_bpermute_b32 v149, v142, v173
	ds_bpermute_b32 v150, v142, v172
	ds_bpermute_b32 v151, v142, v171
	ds_bpermute_b32 v152, v142, v169
	ds_bpermute_b32 v153, v142, v168
	ds_bpermute_b32 v154, v142, v167
	ds_bpermute_b32 v157, v142, v166
	ds_bpermute_b32 v163, v142, v165
	ds_bpermute_b32 v170, v142, v164
	ds_bpermute_b32 v174, v142, v162
	ds_bpermute_b32 v175, v142, v161
	ds_bpermute_b32 v176, v142, v160
	ds_bpermute_b32 v177, v142, v159
	ds_bpermute_b32 v178, v142, v158
	ds_bpermute_b32 v179, v142, v156
	ds_bpermute_b32 v180, v142, v155
	s_and_b64 vcc, exec, s[10:11]
	s_cbranch_vccnz .LBB0_916
; template <bool SIGNED4> __device__ __forceinline__ void qrow_store(const f32x4 (&v)[4], unsigned char* q, float* scale, int row, int lane) {
;     float ss = 0.f;
; #pragma unroll
;     for (int j = 0; j < 4; ++j) ss += v[j].x * v[j].x + v[j].y * v[j].y + v[j].z * v[j].z + v[j].w * v[j].w;
;     ss = wave_sum(ss);
;     const float sc = ss > 0.f ? 0.3352f * sqrtf(ss * (1.f / 1024.f)) : 1.f, inv = __builtin_amdgcn_rcpf(sc);
;     unsigned n[16];
; #pragma unroll
;     for (int j = 0; j < 4; ++j) {
; #pragma unroll
;         for (int i = 0; i < 4; ++i) { const float f = floorf(v[j][i] * inv) + 8.f; n[4 * j + i] = (unsigned)fminf(fmaxf(f, 0.f), 15.f); } }
;     u32x2 o;
; #pragma unroll
;     for (int m = 0; m < 2; ++m) { unsigned w = 0;
; #pragma unroll
;         for (int b = 0; b < 4; ++b) w |= (n[8 * m + b] | (n[8 * m + 4 + b] << 4)) << (8 * b);
;         o[m] = SIGNED4 ? (w ^ 0x88888888u) : w; }
;     *(u32x2*)(q + (size_t)row * 1024 + lane * 16) = o;
;     if (lane == 0) scale[row] = sc;
; }
	v_mul_f32_e32 v2, v67, v67
	v_mul_f32_e32 v3, v71, v71
	v_fmac_f32_e32 v2, v66, v66
	v_fmac_f32_e32 v3, v70, v70
	v_fmac_f32_e32 v2, v68, v68
	v_fmac_f32_e32 v3, v72, v72
	v_fmac_f32_e32 v2, v69, v69
	v_fmac_f32_e32 v3, v73, v73
	v_add_f32_e32 v2, v2, v3
	v_mul_f32_e32 v3, v75, v75
	v_fmac_f32_e32 v3, v74, v74
	v_fmac_f32_e32 v3, v76, v76
	v_fmac_f32_e32 v3, v77, v77
	v_add_f32_e32 v2, v3, v2
	v_mul_f32_e32 v3, v83, v83
	v_fmac_f32_e32 v3, v82, v82
	v_fmac_f32_e32 v3, v84, v84
	v_fmac_f32_e32 v3, v85, v85
	v_add_f32_e32 v2, v3, v2
	s_ashr_i32 s27, s26, 31
	s_lshl_b64 s[0:1], s[26:27], 10
	v_add_f32_dpp v2, v2, v2 quad_perm:[1,0,3,2] row_mask:0xf bank_mask:0xf bound_ctrl:1
	s_nop 1
	v_add_f32_dpp v2, v2, v2 quad_perm:[2,3,0,1] row_mask:0xf bank_mask:0xf bound_ctrl:1
	s_nop 1
	v_add_f32_dpp v2, v2, v2 row_ror:4 row_mask:0xf bank_mask:0xf bound_ctrl:1
	s_nop 1
	v_add_f32_dpp v2, v2, v2 row_ror:8 row_mask:0xf bank_mask:0xf bound_ctrl:1
	v_mov_b32_e32 v3, v2
	s_nop 1
	v_permlane16_swap_b32_e32 v2, v3
	v_add_f32_e32 v2, v2, v3
	v_mov_b32_e32 v3, v2
	s_nop 1
	v_permlane32_swap_b32_e32 v2, v3
	v_add_f32_e32 v2, v2, v3
	v_mul_f32_e32 v3, 0x3a800000, v2
	v_mul_f32_e32 v4, 0x4f800000, v3
	v_cmp_gt_f32_e32 vcc, s44, v3
	s_nop 1
	v_cndmask_b32_e32 v3, v3, v4, vcc
	v_sqrt_f32_e32 v4, v3
	s_nop 0
	v_add_u32_e32 v5, -1, v4
	v_fma_f32 v6, -v5, v4, v3
	v_cmp_ge_f32_e64 s[12:13], 0, v6
	v_add_u32_e32 v6, 1, v4
	s_nop 0
	v_cndmask_b32_e64 v5, v4, v5, s[12:13]
	v_fma_f32 v4, -v6, v4, v3
	v_cmp_lt_f32_e64 s[12:13], 0, v4
	s_nop 1
	v_cndmask_b32_e64 v4, v5, v6, s[12:13]
	v_mul_f32_e32 v5, 0x37800000, v4
	v_cndmask_b32_e32 v4, v4, v5, vcc
	v_cmp_class_f32_e32 vcc, v3, v147
	s_nop 1
	v_cndmask_b32_e32 v3, v4, v3, vcc
	v_mul_f32_e32 v3, 0x3eab9f56, v3
	v_cmp_lt_f32_e32 vcc, 0, v2
	s_nop 1
	v_cndmask_b32_e32 v2, 1.0, v3, vcc
	v_rcp_f32_e32 v3, v2
	s_nop 0
	v_mul_f32_e32 v11, v73, v3
	v_mul_f32_e32 v4, v66, v3
	v_mul_f32_e32 v7, v69, v3
	v_mul_f32_e32 v10, v72, v3
	v_floor_f32_e32 v11, v11
	v_floor_f32_e32 v4, v4
	v_mul_f32_e32 v5, v67, v3
	v_mul_f32_e32 v6, v68, v3
	v_floor_f32_e32 v7, v7
	v_mul_f32_e32 v9, v71, v3
	v_floor_f32_e32 v10, v10
	v_add_f32_e32 v11, 0x41000000, v11
	v_add_f32_e32 v4, 0x41000000, v4
	v_floor_f32_e32 v5, v5
	v_floor_f32_e32 v6, v6
	v_add_f32_e32 v7, 0x41000000, v7
	v_mul_f32_e32 v8, v70, v3
	v_floor_f32_e32 v9, v9
	v_add_f32_e32 v10, 0x41000000, v10
	v_med3_f32 v11, v11, 0, v148
	v_mul_f32_e32 v12, v74, v3
	v_mul_f32_e32 v13, v75, v3
	v_mul_f32_e32 v14, v76, v3
	v_mul_f32_e32 v15, v77, v3
	v_mul_f32_e32 v16, v82, v3
	v_mul_f32_e32 v17, v83, v3
	v_mul_f32_e32 v18, v84, v3
	v_mul_f32_e32 v3, v85, v3
	v_med3_f32 v4, v4, 0, v148
	v_add_f32_e32 v5, 0x41000000, v5
	v_add_f32_e32 v6, 0x41000000, v6
	v_med3_f32 v7, v7, 0, v148
	v_floor_f32_e32 v8, v8
	v_add_f32_e32 v9, 0x41000000, v9
	v_med3_f32 v10, v10, 0, v148
	v_cvt_u32_f32_e32 v11, v11
	v_floor_f32_e32 v3, v3
	v_cvt_u32_f32_e32 v4, v4
	v_med3_f32 v5, v5, 0, v148
	v_med3_f32 v6, v6, 0, v148
	v_cvt_u32_f32_sdwa v7, v7 dst_sel:BYTE_3 dst_unused:UNUSED_PAD src0_sel:DWORD
	v_add_f32_e32 v8, 0x41000000, v8
	v_med3_f32 v9, v9, 0, v148
	v_cvt_u32_f32_e32 v10, v10
	v_floor_f32_e32 v12, v12
	v_floor_f32_e32 v15, v15
	v_floor_f32_e32 v18, v18
	v_add_f32_e32 v3, 0x41000000, v3
	v_cvt_u32_f32_e32 v5, v5
	v_cvt_u32_f32_sdwa v6, v6 dst_sel:WORD_1 dst_unused:UNUSED_PAD src0_sel:DWORD
	v_med3_f32 v8, v8, 0, v148
	v_cvt_u32_f32_e32 v9, v9
	v_add_f32_e32 v12, 0x41000000, v12
	v_floor_f32_e32 v13, v13
	v_floor_f32_e32 v14, v14
	v_add_f32_e32 v15, 0x41000000, v15
	v_floor_f32_e32 v17, v17
	v_add_f32_e32 v18, 0x41000000, v18
	v_med3_f32 v3, v3, 0, v148
	v_cvt_u32_f32_e32 v8, v8
	v_med3_f32 v12, v12, 0, v148
	v_add_f32_e32 v13, 0x41000000, v13
	v_add_f32_e32 v14, 0x41000000, v14
	v_med3_f32 v15, v15, 0, v148
	v_floor_f32_e32 v16, v16
	v_add_f32_e32 v17, 0x41000000, v17
	v_med3_f32 v18, v18, 0, v148
	v_cvt_u32_f32_e32 v3, v3
	v_cvt_u32_f32_e32 v12, v12
	v_med3_f32 v13, v13, 0, v148
	v_med3_f32 v14, v14, 0, v148
	v_cvt_u32_f32_sdwa v15, v15 dst_sel:BYTE_3 dst_unused:UNUSED_PAD src0_sel:DWORD
	v_add_f32_e32 v16, 0x41000000, v16
	v_med3_f32 v17, v17, 0, v148
	v_cvt_u32_f32_e32 v18, v18
	v_lshlrev_b32_e32 v11, 28, v11
	v_cvt_u32_f32_e32 v13, v13
	v_cvt_u32_f32_sdwa v14, v14 dst_sel:WORD_1 dst_unused:UNUSED_PAD src0_sel:DWORD
	v_med3_f32 v16, v16, 0, v148
	v_cvt_u32_f32_e32 v17, v17
	v_lshlrev_b32_e32 v10, 20, v10
	v_or3_b32 v4, v7, v4, v11
	v_cvt_u32_f32_e32 v16, v16
	v_lshlrev_b32_e32 v9, 12, v9
	v_lshlrev_b32_e32 v5, 8, v5
	v_or3_b32 v4, v4, v6, v10
	v_lshlrev_b32_e32 v8, 4, v8
	v_or3_b32 v4, v4, v5, v9
	v_lshlrev_b32_e32 v3, 28, v3
	v_bitop3_b32 v4, v4, s45, v8 bitop3:0x36
	v_lshlrev_b32_e32 v8, 20, v18
	v_or3_b32 v3, v15, v12, v3
	v_lshlrev_b32_e32 v6, 12, v17
	v_lshlrev_b32_e32 v7, 8, v13
	v_or3_b32 v3, v3, v14, v8
	v_lshlrev_b32_e32 v5, 4, v16
	v_or3_b32 v3, v3, v7, v6
	v_bitop3_b32 v5, v3, s45, v5 bitop3:0x36
	v_lshl_add_u64 v[6:7], v[130:131], 0, s[0:1]
	global_store_dwordx2 v[6:7], v[4:5], off
	s_and_saveexec_b64 s[0:1], s[2:3]
	s_cbranch_execz .LBB0_913
	s_lshl_b64 s[4:5], s[26:27], 2
	s_add_u32 s4, s34, s4
	s_addc_u32 s5, s35, s5
	global_store_dword v127, v2, s[4:5]

; __device__ __forceinline__ float bf2f(bf16_t v) { return __uint_as_float(((unsigned)v) << 16); }
; #define LAS __attribute__((address_space(3)))
; __device__ __forceinline__ void route_half(float (&top)[16], LAS const unsigned char* keys_lds, const bf16_t* __restrict__ qrow, int r32, int hi) {
;     bf16x8 qf[8]; float ss = 0.f;
; #pragma unroll
;     for (int ks = 0; ks < 8; ++ks) { qf[ks] = __builtin_nontemporal_load((const bf16x8*)(qrow + 16 * ks + 8 * hi));
; #pragma unroll
;         for (int j = 0; j < 8; ++j) { const float f = bf2f((bf16_t)qf[ks][j]); ss += f * f; } }
;     ss += __shfl_xor(ss, 32);
;     const float rn = rsqrtf(ss * (1.f / 128.f) + EPS);
;     f32x16 acc[4];
; #pragma unroll
;     for (int kt = 0; kt < 4; ++kt) {
; #pragma unroll
;         for (int r = 0; r < 16; ++r) acc[kt][r] = 0.f;
; #pragma unroll
;         for (int ks = 0; ks < 8; ++ks) { const bf16x8 kf = *(LAS const bf16x8*)(keys_lds + (32 * kt + r32) * RT_KROW + (16 * ks + 8 * hi) * 2);
;             acc[kt] = __builtin_amdgcn_mfma_f32_32x32x16_bf16(kf, qf[ks], acc[kt], 0, 0, 0); }
.LBB0_922:
	global_load_dwordx4 v[18:21], v[140:141], off offset:256 nt
	global_load_dwordx4 v[98:101], v[140:141], off offset:288 nt
	global_load_dwordx4 v[102:105], v[140:141], off offset:320 nt
	global_load_dwordx4 v[106:109], v[140:141], off offset:352 nt
	global_load_dwordx4 v[110:113], v[140:141], off offset:384 nt
	global_load_dwordx4 v[114:117], v[140:141], off offset:416 nt
	global_load_dwordx4 v[118:121], v[140:141], off offset:448 nt
	global_load_dwordx4 v[122:125], v[140:141], off offset:480 nt
	ds_read_b128 v[2:5], v143 offset:34816
	ds_read_b128 v[22:25], v143 offset:34848
	ds_read_b128 v[26:29], v143 offset:34880
	ds_read_b128 v[30:33], v143 offset:34912
	ds_read_b128 v[34:37], v143 offset:34944
	s_waitcnt vmcnt(7) lgkmcnt(4)
	v_mfma_f32_32x32x16_bf16 v[2:17], v[2:5], v[18:21], 0
	v_and_b32_e32 v46, 0xffff0000, v18
	v_lshlrev_b32_e32 v44, 16, v18
	v_mul_f32_e32 v46, v46, v46
	v_lshlrev_b32_e32 v47, 16, v19
	v_fmac_f32_e32 v46, v44, v44
	v_and_b32_e32 v48, 0xffff0000, v19
	v_fmac_f32_e32 v46, v47, v47
	v_lshlrev_b32_e32 v49, 16, v20
	v_fmac_f32_e32 v46, v48, v48
	v_and_b32_e32 v50, 0xffff0000, v20
	v_fmac_f32_e32 v46, v49, v49
	v_lshlrev_b32_e32 v51, 16, v21
	v_fmac_f32_e32 v46, v50, v50
	v_and_b32_e32 v52, 0xffff0000, v21
	v_fmac_f32_e32 v46, v51, v51
	s_waitcnt vmcnt(6)
	v_lshlrev_b32_e32 v53, 16, v98
	v_fmac_f32_e32 v46, v52, v52
	v_and_b32_e32 v54, 0xffff0000, v98
	v_fmac_f32_e32 v46, v53, v53
	v_lshlrev_b32_e32 v55, 16, v99
	v_fmac_f32_e32 v46, v54, v54
	v_and_b32_e32 v56, 0xffff0000, v99
	v_fmac_f32_e32 v46, v55, v55
	v_lshlrev_b32_e32 v57, 16, v100
	v_fmac_f32_e32 v46, v56, v56
	v_and_b32_e32 v58, 0xffff0000, v100
	v_fmac_f32_e32 v46, v57, v57
	v_lshlrev_b32_e32 v59, 16, v101
	v_fmac_f32_e32 v46, v58, v58
	v_and_b32_e32 v60, 0xffff0000, v101
	v_fmac_f32_e32 v46, v59, v59
	s_waitcnt vmcnt(5)
	v_lshlrev_b32_e32 v61, 16, v102
	v_fmac_f32_e32 v46, v60, v60
	v_and_b32_e32 v62, 0xffff0000, v102
	v_fmac_f32_e32 v46, v61, v61
	v_lshlrev_b32_e32 v63, 16, v103
	v_fmac_f32_e32 v46, v62, v62
	v_and_b32_e32 v64, 0xffff0000, v103
	v_fmac_f32_e32 v46, v63, v63
	v_lshlrev_b32_e32 v65, 16, v104
	v_fmac_f32_e32 v46, v64, v64
	v_and_b32_e32 v140, 0xffff0000, v104
	v_fmac_f32_e32 v46, v65, v65
	v_lshlrev_b32_e32 v141, 16, v105
	v_fmac_f32_e32 v46, v140, v140
	v_and_b32_e32 v181, 0xffff0000, v105
	v_fmac_f32_e32 v46, v141, v141
	s_waitcnt vmcnt(4)
	v_lshlrev_b32_e32 v182, 16, v106
	v_fmac_f32_e32 v46, v181, v181
	v_and_b32_e32 v183, 0xffff0000, v106
	v_fmac_f32_e32 v46, v182, v182
	v_lshlrev_b32_e32 v184, 16, v107
	v_fmac_f32_e32 v46, v183, v183
	v_and_b32_e32 v185, 0xffff0000, v107
	v_fmac_f32_e32 v46, v184, v184
	v_lshlrev_b32_e32 v186, 16, v108
	v_fmac_f32_e32 v46, v185, v185
	v_and_b32_e32 v187, 0xffff0000, v108
	v_fmac_f32_e32 v46, v186, v186
	v_lshlrev_b32_e32 v188, 16, v109
	v_fmac_f32_e32 v46, v187, v187
	v_and_b32_e32 v189, 0xffff0000, v109
	v_fmac_f32_e32 v46, v188, v188
	s_waitcnt vmcnt(3)
	v_lshlrev_b32_e32 v190, 16, v110
	v_fmac_f32_e32 v46, v189, v189
	v_and_b32_e32 v191, 0xffff0000, v110
	v_fmac_f32_e32 v46, v190, v190
	v_lshlrev_b32_e32 v192, 16, v111
	v_fmac_f32_e32 v46, v191, v191
	v_and_b32_e32 v193, 0xffff0000, v111
	v_fmac_f32_e32 v46, v192, v192
	v_lshlrev_b32_e32 v194, 16, v112
	v_fmac_f32_e32 v46, v193, v193
	v_and_b32_e32 v195, 0xffff0000, v112
	v_fmac_f32_e32 v46, v194, v194
	v_lshlrev_b32_e32 v196, 16, v113
	v_fmac_f32_e32 v46, v195, v195
	v_and_b32_e32 v197, 0xffff0000, v113
	v_fmac_f32_e32 v46, v196, v196
	s_waitcnt vmcnt(2)
	v_lshlrev_b32_e32 v198, 16, v114
	s_waitcnt lgkmcnt(3)
	v_mfma_f32_32x32x16_bf16 v[2:17], v[22:25], v[98:101], v[2:17]
	v_fmac_f32_e32 v46, v197, v197
	v_and_b32_e32 v199, 0xffff0000, v114
	v_fmac_f32_e32 v46, v198, v198
	v_lshlrev_b32_e32 v200, 16, v115
	v_fmac_f32_e32 v46, v199, v199
	v_and_b32_e32 v201, 0xffff0000, v115
	v_fmac_f32_e32 v46, v200, v200
	v_lshlrev_b32_e32 v202, 16, v116
	v_fmac_f32_e32 v46, v201, v201
	v_and_b32_e32 v203, 0xffff0000, v116
	v_fmac_f32_e32 v46, v202, v202
	v_lshlrev_b32_e32 v204, 16, v117
	v_fmac_f32_e32 v46, v203, v203
	v_and_b32_e32 v205, 0xffff0000, v117
	v_fmac_f32_e32 v46, v204, v204
	s_waitcnt vmcnt(1)
	v_lshlrev_b32_e32 v206, 16, v118
	s_waitcnt lgkmcnt(2)
	v_mfma_f32_32x32x16_bf16 v[2:17], v[26:29], v[102:105], v[2:17]
	v_fmac_f32_e32 v46, v205, v205
	v_and_b32_e32 v207, 0xffff0000, v118
	v_fmac_f32_e32 v46, v206, v206
	v_lshlrev_b32_e32 v208, 16, v119
	v_fmac_f32_e32 v46, v207, v207
	v_and_b32_e32 v209, 0xffff0000, v119
	v_fmac_f32_e32 v46, v208, v208
	v_lshlrev_b32_e32 v210, 16, v120
	v_fmac_f32_e32 v46, v209, v209
	v_and_b32_e32 v211, 0xffff0000, v120
	v_and_b32_e32 v39, 0xffff0000, v121
	v_lshlrev_b32_e32 v38, 16, v121
	v_fmac_f32_e32 v46, v210, v210
	v_pk_mul_f32 v[38:39], v[38:39], v[38:39]
	v_fmac_f32_e32 v46, v211, v211
	s_waitcnt vmcnt(0)
	v_and_b32_e32 v41, 0xffff0000, v122
	v_lshlrev_b32_e32 v40, 16, v122
	v_add_f32_e32 v22, v38, v46
	v_pk_mul_f32 v[40:41], v[40:41], v[40:41]
	s_waitcnt lgkmcnt(1)
	v_mfma_f32_32x32x16_bf16 v[2:17], v[30:33], v[106:109], v[2:17]
	v_add_f32_e32 v22, v39, v22
	v_and_b32_e32 v43, 0xffff0000, v123
	v_lshlrev_b32_e32 v42, 16, v123
	v_add_f32_e32 v22, v40, v22
	v_mul_f32_e64 v42, v42, v42
	v_mul_f32_e64 v43, v43, v43
	v_add_f32_e32 v22, v41, v22
	v_and_b32_e32 v45, 0xffff0000, v124
	v_add_f32_e32 v22, v42, v22
	v_lshlrev_b32_e32 v44, 16, v124
	v_add_f32_e32 v22, v43, v22
	v_pk_mul_f32 v[26:27], v[44:45], v[44:45]
	s_waitcnt lgkmcnt(0)
; __device__ __forceinline__ float bf2f(bf16_t v) { return __uint_as_float(((unsigned)v) << 16); }
; #define LAS __attribute__((address_space(3)))
; __device__ __forceinline__ void route_half(float (&top)[16], LAS const unsigned char* keys_lds, const bf16_t* __restrict__ qrow, int r32, int hi) {
;     ...
;     for (int ks = 0; ks < 8; ++ks) { qf[ks] = __builtin_nontemporal_load((const bf16x8*)(qrow + 16 * ks + 8 * hi));
; #pragma unroll
;         for (int j = 0; j < 8; ++j) { const float f = bf2f((bf16_t)qf[ks][j]); ss += f * f; } }
;     ss += __shfl_xor(ss, 32);
;     const float rn = rsqrtf(ss * (1.f / 128.f) + EPS);
;     f32x16 acc[4];
; #pragma unroll
;     for (int kt = 0; kt < 4; ++kt) {
; #pragma unroll
;         for (int r = 0; r < 16; ++r) acc[kt][r] = 0.f;
; #pragma unroll
;         for (int ks = 0; ks < 8; ++ks) { const bf16x8 kf = *(LAS const bf16x8*)(keys_lds + (32 * kt + r32) * RT_KROW + (16 * ks + 8 * hi) * 2);
;             acc[kt] = __builtin_amdgcn_mfma_f32_32x32x16_bf16(kf, qf[ks], acc[kt], 0, 0, 0); }
;         __builtin_amdgcn_sched_barrier(0);
;     }
;     const unsigned hi4 = (unsigned)hi << 2;
;     float g[4][16];
; #pragma unroll
;     for (int kt = 0; kt < 4; ++kt)
; #pragma unroll
;         for (int r = 0; r < 16; ++r) { const unsigned base = (unsigned)(32 * kt + (r & 3) + 8 * (r >> 2)); g[kt][r] = __uint_as_float((__float_as_uint(acc[kt][r] * rn) & 0xFFFFFF80u) | base); }
	v_mfma_f32_32x32x16_bf16 v[2:17], v[34:37], v[110:113], v[2:17]
	v_add_f32_e32 v26, v26, v22
	v_add_f32_e32 v28, v27, v26
	v_and_b32_e32 v27, 0xffff0000, v125
	v_lshlrev_b32_e32 v26, 16, v125
	ds_read_b128 v[22:25], v143 offset:34976
	v_pk_mul_f32 v[26:27], v[26:27], v[26:27]
	s_nop 0
	v_add_f32_e32 v26, v26, v28
	v_add_f32_e32 v26, v27, v26
	ds_bpermute_b32 v27, v142, v26
	s_waitcnt lgkmcnt(0)
	v_add_f32_e32 v26, v26, v27
	v_fmamk_f32 v30, v26, 0x3c000000, v146
	ds_read_b128 v[26:29], v143 offset:35040
	v_mfma_f32_32x32x16_bf16 v[2:17], v[22:25], v[114:117], v[2:17]
	ds_read_b128 v[22:25], v143 offset:35008
	v_mul_f32_e32 v31, 0x4b800000, v30
	v_cmp_gt_f32_e32 vcc, s40, v30
	s_waitcnt lgkmcnt(0)
	v_mfma_f32_32x32x16_bf16 v[2:17], v[22:25], v[118:121], v[2:17]
	v_cndmask_b32_e32 v22, v30, v31, vcc
	v_rsq_f32_e32 v140, v22
	s_nop 0
	v_mul_f32_e32 v141, 0x45800000, v140
	v_mfma_f32_32x32x16_bf16 v[2:17], v[26:29], v[122:125], v[2:17]
	ds_read_b128 v[22:25], v143 offset:43520
	ds_read_b128 v[26:29], v143 offset:43552
	s_waitcnt lgkmcnt(1)
	v_mfma_f32_32x32x16_bf16 v[50:65], v[22:25], v[18:21], 0
	s_waitcnt lgkmcnt(0)
	v_mfma_f32_32x32x16_bf16 v[50:65], v[26:29], v[98:101], v[50:65]
	ds_read_b128 v[22:25], v143 offset:43584
	ds_read_b128 v[26:29], v143 offset:43616
	s_waitcnt lgkmcnt(1)
	v_mfma_f32_32x32x16_bf16 v[50:65], v[22:25], v[102:105], v[50:65]
	s_waitcnt lgkmcnt(0)
	v_mfma_f32_32x32x16_bf16 v[50:65], v[26:29], v[106:109], v[50:65]
	ds_read_b128 v[22:25], v143 offset:43648
	ds_read_b128 v[26:29], v143 offset:43680
	s_waitcnt lgkmcnt(1)
	v_mfma_f32_32x32x16_bf16 v[50:65], v[22:25], v[110:113], v[50:65]
	s_waitcnt lgkmcnt(0)
	v_mfma_f32_32x32x16_bf16 v[50:65], v[26:29], v[114:117], v[50:65]
	ds_read_b128 v[22:25], v143 offset:43712
	ds_read_b128 v[26:29], v143 offset:43744
	s_waitcnt lgkmcnt(1)
	v_mfma_f32_32x32x16_bf16 v[50:65], v[22:25], v[118:121], v[50:65]
	s_waitcnt lgkmcnt(0)
	v_mfma_f32_32x32x16_bf16 v[50:65], v[26:29], v[122:125], v[50:65]
	ds_read_b128 v[22:25], v143 offset:52224
	ds_read_b128 v[26:29], v143 offset:52256
	s_waitcnt lgkmcnt(1)
	v_mfma_f32_32x32x16_bf16 v[34:49], v[22:25], v[18:21], 0
	s_waitcnt lgkmcnt(0)
	v_mfma_f32_32x32x16_bf16 v[34:49], v[26:29], v[98:101], v[34:49]
	ds_read_b128 v[22:25], v143 offset:52288
	ds_read_b128 v[26:29], v143 offset:52320
	s_waitcnt lgkmcnt(1)
	v_mfma_f32_32x32x16_bf16 v[34:49], v[22:25], v[102:105], v[34:49]
	s_waitcnt lgkmcnt(0)
	v_mfma_f32_32x32x16_bf16 v[34:49], v[26:29], v[106:109], v[34:49]
	ds_read_b128 v[22:25], v143 offset:52352
	ds_read_b128 v[26:29], v143 offset:52384
	s_waitcnt lgkmcnt(1)
	v_mfma_f32_32x32x16_bf16 v[34:49], v[22:25], v[110:113], v[34:49]
	s_waitcnt lgkmcnt(0)
	v_mfma_f32_32x32x16_bf16 v[34:49], v[26:29], v[114:117], v[34:49]
	ds_read_b128 v[22:25], v143 offset:52416
	ds_read_b128 v[26:29], v143 offset:52448
	s_waitcnt lgkmcnt(1)
	v_mfma_f32_32x32x16_bf16 v[34:49], v[22:25], v[118:121], v[34:49]
	s_waitcnt lgkmcnt(0)
	v_mfma_f32_32x32x16_bf16 v[34:49], v[26:29], v[122:125], v[34:49]
	ds_read_b128 v[22:25], v143 offset:60928
	ds_read_b128 v[182:185], v143 offset:60960
	s_waitcnt lgkmcnt(1)
	v_mfma_f32_32x32x16_bf16 v[18:33], v[22:25], v[18:21], 0
	s_waitcnt lgkmcnt(0)
	v_mfma_f32_32x32x16_bf16 v[18:33], v[182:185], v[98:101], v[18:33]
	ds_read_b128 v[98:101], v143 offset:60992
	ds_read_b128 v[182:185], v143 offset:61024
	s_waitcnt lgkmcnt(1)
	v_mfma_f32_32x32x16_bf16 v[18:33], v[98:101], v[102:105], v[18:33]
	ds_read_b128 v[98:101], v143 offset:61056
	ds_read_b128 v[102:105], v143 offset:61088
	s_waitcnt lgkmcnt(2)
	v_mfma_f32_32x32x16_bf16 v[18:33], v[182:185], v[106:109], v[18:33]
	s_waitcnt lgkmcnt(1)
	v_mfma_f32_32x32x16_bf16 v[18:33], v[98:101], v[110:113], v[18:33]
	s_waitcnt lgkmcnt(0)
	v_mfma_f32_32x32x16_bf16 v[18:33], v[102:105], v[114:117], v[18:33]
	ds_read_b128 v[98:101], v143 offset:61120
	ds_read_b128 v[102:105], v143 offset:61152
	s_waitcnt lgkmcnt(1)
	v_mfma_f32_32x32x16_bf16 v[18:33], v[98:101], v[118:121], v[18:33]
	s_waitcnt lgkmcnt(0)
	v_mfma_f32_32x32x16_bf16 v[18:33], v[102:105], v[122:125], v[18:33]
	v_cndmask_b32_e32 v98, v140, v141, vcc
	v_mul_f32_e32 v2, v2, v98
	v_and_b32_e32 v99, 0xffffff80, v2
	v_mul_f32_e32 v2, v3, v98
	v_and_or_b32 v100, v2, s41, 1
	v_mul_f32_e32 v2, v4, v98
	v_and_or_b32 v101, v2, s41, 2
	v_mul_f32_e32 v2, v5, v98
	v_and_or_b32 v102, v2, s41, 3
	v_mul_f32_e32 v2, v6, v98
	v_and_or_b32 v103, v2, s41, 8
	v_mul_f32_e32 v2, v7, v98
	v_and_or_b32 v104, v2, s41, 9
	v_mul_f32_e32 v2, v8, v98
	v_and_or_b32 v105, v2, s41, 10
	v_mul_f32_e32 v2, v9, v98
	v_and_or_b32 v106, v2, s41, 11
	v_mul_f32_e32 v2, v10, v98
	v_and_or_b32 v107, v2, s41, 16
	v_mul_f32_e32 v2, v11, v98
	v_and_or_b32 v108, v2, s41, 17
	v_mul_f32_e32 v2, v12, v98
	v_and_or_b32 v109, v2, s41, 18
	v_mul_f32_e32 v2, v13, v98
	v_and_or_b32 v110, v2, s41, 19
	v_mul_f32_e32 v2, v14, v98
	v_and_or_b32 v111, v2, s41, 24
	v_mul_f32_e32 v2, v15, v98
	v_and_or_b32 v112, v2, s41, 25
	v_mul_f32_e32 v2, v16, v98
	v_and_or_b32 v113, v2, s41, 26
	v_mul_f32_e32 v2, v17, v98
	v_and_or_b32 v114, v2, s41, 27
	v_mul_f32_e32 v2, v50, v98
	v_and_or_b32 v50, v2, s41, 32
	v_mul_f32_e32 v2, v51, v98
	v_and_or_b32 v51, v2, s41, 33
	v_mul_f32_e32 v2, v52, v98
	v_and_or_b32 v52, v2, s41, 34
	v_mul_f32_e32 v2, v53, v98
	v_and_or_b32 v53, v2, s41, 35
	v_mul_f32_e32 v2, v54, v98
	v_and_or_b32 v54, v2, s41, 40
	v_mul_f32_e32 v2, v55, v98
	v_and_or_b32 v55, v2, s41, 41
	v_mul_f32_e32 v2, v56, v98
	v_and_or_b32 v56, v2, s41, 42
	v_mul_f32_e32 v2, v57, v98
	v_and_or_b32 v57, v2, s41, 43
	v_mul_f32_e32 v2, v58, v98
	v_and_or_b32 v58, v2, s41, 48
	v_mul_f32_e32 v2, v59, v98
; #define CE_DESC(a, b) do { const float _t = fmaxf(a, b); b = fminf(a, b); a = _t; } while (0)
; __device__ __forceinline__ void sort16_desc(float (&v)[16]) {
; #pragma unroll
;     for (int k = 2; k <= 16; k <<= 1)
; #pragma unroll
;         for (int j = k >> 1; j > 0; j >>= 1)
; #pragma unroll
;             for (int i = 0; i < 16; ++i) { const int l = i ^ j; if (l > i) { if ((i & k) == 0 || k == 16) CE_DESC(v[i], v[l]); else CE_DESC(v[l], v[i]); } }
; }
; __device__ __forceinline__ void route_half(float (&top)[16], LAS const unsigned char* keys_lds, const bf16_t* __restrict__ qrow, int r32, int hi) {
;     ...
;         for (int r = 0; r < 16; ++r) { const unsigned base = (unsigned)(32 * kt + (r & 3) + 8 * (r >> 2)); g[kt][r] = __uint_as_float((__float_as_uint(acc[kt][r] * rn) & 0xFFFFFF80u) | base); }
; #pragma unroll
;     for (int kt = 0; kt < 4; ++kt) sort16_desc(g[kt]);
	v_and_or_b32 v59, v2, s41, 49
	v_mul_f32_e32 v2, v60, v98
	v_and_or_b32 v60, v2, s41, 50
	v_mul_f32_e32 v2, v61, v98
	v_and_or_b32 v61, v2, s41, 51
	v_mul_f32_e32 v2, v62, v98
	v_and_or_b32 v62, v2, s41, 56
	v_mul_f32_e32 v2, v63, v98
	v_and_or_b32 v63, v2, s41, 57
	v_mul_f32_e32 v2, v64, v98
	v_and_or_b32 v64, v2, s41, 58
	v_mul_f32_e32 v2, v65, v98
	v_and_or_b32 v65, v2, s41, 59
	v_mul_f32_e32 v2, v34, v98
	v_and_or_b32 v115, v2, s41, 64
	v_mul_f32_e32 v2, v35, v98
	v_and_b32_e32 v2, 0xffffff80, v2
	v_or_b32_e32 v116, 0x41, v2
	v_mul_f32_e32 v2, v36, v98
	v_and_b32_e32 v2, 0xffffff80, v2
	v_or_b32_e32 v117, 0x42, v2
	v_mul_f32_e32 v2, v37, v98
	v_and_b32_e32 v2, 0xffffff80, v2
	v_or_b32_e32 v118, 0x43, v2
	v_mul_f32_e32 v2, v38, v98
	v_and_b32_e32 v2, 0xffffff80, v2
	v_or_b32_e32 v119, 0x48, v2
	v_mul_f32_e32 v2, v39, v98
	v_and_b32_e32 v2, 0xffffff80, v2
	v_or_b32_e32 v120, 0x49, v2
	v_mul_f32_e32 v2, v40, v98
	v_and_b32_e32 v2, 0xffffff80, v2
	v_or_b32_e32 v121, 0x4a, v2
	v_mul_f32_e32 v2, v41, v98
	v_and_b32_e32 v2, 0xffffff80, v2
	v_or_b32_e32 v122, 0x4b, v2
	v_mul_f32_e32 v2, v42, v98
	v_and_b32_e32 v2, 0xffffff80, v2
	v_or_b32_e32 v42, 0x50, v2
	v_mul_f32_e32 v2, v43, v98
	v_and_b32_e32 v2, 0xffffff80, v2
	v_or_b32_e32 v43, 0x51, v2
	v_mul_f32_e32 v2, v44, v98
	v_and_b32_e32 v2, 0xffffff80, v2
	v_or_b32_e32 v44, 0x52, v2
	v_mul_f32_e32 v2, v45, v98
	v_and_b32_e32 v2, 0xffffff80, v2
	v_or_b32_e32 v45, 0x53, v2
	v_mul_f32_e32 v2, v46, v98
	v_and_b32_e32 v2, 0xffffff80, v2
	v_or_b32_e32 v46, 0x58, v2
	v_mul_f32_e32 v2, v47, v98
	v_and_b32_e32 v2, 0xffffff80, v2
	v_or_b32_e32 v47, 0x59, v2
	v_mul_f32_e32 v2, v48, v98
	v_and_b32_e32 v2, 0xffffff80, v2
	v_or_b32_e32 v48, 0x5a, v2
	v_mul_f32_e32 v2, v49, v98
	v_and_b32_e32 v2, 0xffffff80, v2
	v_mul_f32_e32 v3, v98, v19
	v_or_b32_e32 v49, 0x5b, v2
	v_mul_f32_e32 v2, v98, v18
	v_and_b32_e32 v3, 0xffffff80, v3
	v_mul_f32_e32 v5, v98, v21
	v_or_b32_e32 v4, 0x61, v3
	v_mul_f32_e32 v3, v98, v20
	v_and_b32_e32 v5, 0xffffff80, v5
	v_mul_f32_e32 v7, v98, v23
	v_max_f32_e32 v20, v99, v100
	v_min_f32_e32 v18, v99, v100
	v_or_b32_e32 v6, 0x63, v5
	v_mul_f32_e32 v5, v98, v22
	v_and_b32_e32 v7, 0xffffff80, v7
	v_mul_f32_e32 v9, v98, v25
	v_max_f32_e32 v22, v102, v101
	v_min_f32_e32 v19, v102, v101
	v_or_b32_e32 v8, 0x69, v7
	v_mul_f32_e32 v7, v98, v24
	v_and_b32_e32 v9, 0xffffff80, v9
	v_mul_f32_e32 v11, v98, v27
	v_max_f32_e32 v24, v103, v104
	v_min_f32_e32 v21, v103, v104
	v_and_b32_e32 v2, 0xffffff80, v2
	v_or_b32_e32 v10, 0x6b, v9
	v_mul_f32_e32 v9, v98, v26
	v_and_b32_e32 v11, 0xffffff80, v11
	v_mul_f32_e32 v13, v98, v29
	v_max_f32_e32 v26, v106, v105
	v_min_f32_e32 v23, v106, v105
	v_or_b32_e32 v2, 0x60, v2
	v_and_b32_e32 v3, 0xffffff80, v3
	v_or_b32_e32 v12, 0x71, v11
	v_mul_f32_e32 v11, v98, v28
	v_and_b32_e32 v13, 0xffffff80, v13
	v_mul_f32_e32 v15, v98, v31
	v_max_f32_e32 v28, v107, v108
	v_min_f32_e32 v25, v107, v108
	v_or_b32_e32 v3, 0x62, v3
	v_and_b32_e32 v5, 0xffffff80, v5
	v_or_b32_e32 v14, 0x73, v13
	v_mul_f32_e32 v13, v98, v30
	v_and_b32_e32 v15, 0xffffff80, v15
	v_max_f32_e32 v30, v110, v109
	v_min_f32_e32 v27, v110, v109
	v_or_b32_e32 v5, 0x68, v5
	v_and_b32_e32 v7, 0xffffff80, v7
	v_or_b32_e32 v16, 0x79, v15
	v_mul_f32_e32 v15, v98, v32
	v_mul_f32_e32 v17, v98, v33
	v_max_f32_e32 v32, v111, v112
	v_min_f32_e32 v29, v111, v112
	v_max_f32_e32 v31, v113, v113
	v_max_f32_e32 v98, v50, v51
	v_min_f32_e32 v50, v50, v51
	v_max_f32_e32 v51, v52, v52
	v_max_f32_e32 v52, v53, v53
	v_max_f32_e32 v113, v122, v122
	v_max_f32_e32 v122, v2, v4
	v_min_f32_e32 v2, v2, v4
	v_max_f32_e32 v4, v6, v6
	v_or_b32_e32 v7, 0x6a, v7
	v_and_b32_e32 v9, 0xffffff80, v9
	v_max_f32_e32 v53, v52, v51
	v_min_f32_e32 v51, v52, v51
	v_max_f32_e32 v52, v55, v55
	v_max_f32_e32 v108, v115, v116
	v_min_f32_e32 v106, v115, v116
	v_max_f32_e32 v6, v4, v3
	v_min_f32_e32 v3, v4, v3
	v_max_f32_e32 v4, v8, v8
	v_or_b32_e32 v9, 0x70, v9
	v_and_b32_e32 v11, 0xffffff80, v11
	v_max_f32_e32 v55, v54, v52
	v_min_f32_e32 v52, v54, v52
	v_max_f32_e32 v54, v56, v56
	v_max_f32_e32 v56, v57, v57
	v_max_f32_e32 v110, v118, v117
	v_min_f32_e32 v107, v118, v117
	v_max_f32_e32 v8, v5, v4
	v_min_f32_e32 v4, v5, v4
	v_max_f32_e32 v5, v7, v7
	v_max_f32_e32 v7, v10, v10
	v_or_b32_e32 v11, 0x72, v11
	v_and_b32_e32 v13, 0xffffff80, v13
	v_max_f32_e32 v57, v56, v54
	v_min_f32_e32 v54, v56, v54
	v_max_f32_e32 v56, v59, v59
	v_max_f32_e32 v112, v119, v120
	v_min_f32_e32 v109, v119, v120
	v_max_f32_e32 v10, v7, v5
	v_min_f32_e32 v5, v7, v5
	v_max_f32_e32 v7, v12, v12
	v_or_b32_e32 v13, 0x78, v13
	v_and_b32_e32 v15, 0xffffff80, v15
	v_and_b32_e32 v17, 0xffffff80, v17
	v_max_f32_e32 v33, v114, v114
	v_max_f32_e32 v59, v58, v56
	v_min_f32_e32 v56, v58, v56
	v_max_f32_e32 v58, v60, v60
	v_max_f32_e32 v60, v61, v61
	v_max_f32_e32 v114, v113, v121
	v_min_f32_e32 v111, v113, v121
	v_max_f32_e32 v113, v42, v43
	v_min_f32_e32 v42, v42, v43
	v_max_f32_e32 v43, v44, v44
	v_max_f32_e32 v44, v45, v45
	v_max_f32_e32 v12, v9, v7
	v_min_f32_e32 v7, v9, v7
	v_max_f32_e32 v9, v11, v11
	v_max_f32_e32 v11, v14, v14
	v_or_b32_e32 v15, 0x7a, v15
	v_or_b32_e32 v17, 0x7b, v17
	v_max_f32_e32 v61, v60, v58
	v_min_f32_e32 v58, v60, v58
	v_max_f32_e32 v60, v63, v63
	v_max_f32_e32 v45, v44, v43
	v_min_f32_e32 v43, v44, v43
	v_max_f32_e32 v44, v47, v47
	v_max_f32_e32 v14, v11, v9
	v_min_f32_e32 v9, v11, v9
	v_max_f32_e32 v11, v16, v16
	v_max_f32_e32 v63, v62, v60
	v_min_f32_e32 v60, v62, v60
	v_max_f32_e32 v62, v64, v64
	v_max_f32_e32 v64, v65, v65
	v_max_f32_e32 v47, v46, v44
	v_min_f32_e32 v44, v46, v44
	v_max_f32_e32 v46, v48, v48
	v_max_f32_e32 v48, v49, v49
; #define CE_DESC(a, b) do { const float _t = fmaxf(a, b); b = fminf(a, b); a = _t; } while (0)
; __device__ __forceinline__ void sort16_desc(float (&v)[16]) {
; #pragma unroll
;     for (int k = 2; k <= 16; k <<= 1)
; #pragma unroll
;         for (int j = k >> 1; j > 0; j >>= 1)
; #pragma unroll
;             for (int i = 0; i < 16; ++i) { const int l = i ^ j; if (l > i) { if ((i & k) == 0 || k == 16) CE_DESC(v[i], v[l]); else CE_DESC(v[l], v[i]); } }
; }
	v_max_f32_e32 v16, v13, v11
	v_min_f32_e32 v11, v13, v11
	v_max_f32_e32 v13, v15, v15
	v_max_f32_e32 v15, v17, v17
	v_max_f32_e32 v34, v33, v31
	v_min_f32_e32 v31, v33, v31
	v_max_f32_e32 v65, v64, v62
	v_min_f32_e32 v62, v64, v62
	v_max_f32_e32 v49, v48, v46
	v_min_f32_e32 v46, v48, v46
	v_max_f32_e32 v17, v15, v13
	v_min_f32_e32 v13, v15, v13
	v_max_f32_e32 v33, v20, v19
	v_min_f32_e32 v19, v20, v19
	v_max_f32_e32 v20, v18, v22
	v_min_f32_e32 v18, v18, v22
	v_max_f32_e32 v22, v23, v24
	v_min_f32_e32 v23, v23, v24
	v_max_f32_e32 v24, v26, v21
	v_min_f32_e32 v21, v26, v21
	v_max_f32_e32 v26, v28, v27
	v_min_f32_e32 v27, v28, v27
	v_max_f32_e32 v28, v25, v30
	v_min_f32_e32 v25, v25, v30
	v_max_f32_e32 v30, v31, v32
	v_min_f32_e32 v31, v31, v32
	v_max_f32_e32 v32, v34, v29
	v_min_f32_e32 v29, v34, v29
	v_max_f32_e32 v64, v98, v51
	v_min_f32_e32 v51, v98, v51
	v_max_f32_e32 v98, v50, v53
	v_min_f32_e32 v50, v50, v53
	v_max_f32_e32 v53, v54, v55
	v_min_f32_e32 v54, v54, v55
	v_max_f32_e32 v55, v57, v52
	v_min_f32_e32 v52, v57, v52
	v_max_f32_e32 v57, v59, v58
	v_min_f32_e32 v58, v59, v58
	v_max_f32_e32 v59, v56, v61
	v_min_f32_e32 v56, v56, v61
	v_max_f32_e32 v61, v62, v63
	v_min_f32_e32 v62, v62, v63
	v_max_f32_e32 v63, v65, v60
	v_min_f32_e32 v60, v65, v60
	v_max_f32_e32 v48, v108, v107
	v_min_f32_e32 v107, v108, v107
	v_max_f32_e32 v108, v106, v110
	v_min_f32_e32 v106, v106, v110
	v_max_f32_e32 v110, v111, v112
	v_min_f32_e32 v111, v111, v112
	v_max_f32_e32 v112, v114, v109
	v_min_f32_e32 v109, v114, v109
	v_max_f32_e32 v114, v113, v43
	v_min_f32_e32 v43, v113, v43
	v_max_f32_e32 v113, v42, v45
	v_min_f32_e32 v42, v42, v45
	v_max_f32_e32 v45, v46, v47
	v_min_f32_e32 v46, v46, v47
	v_max_f32_e32 v47, v49, v44
	v_min_f32_e32 v44, v49, v44
	v_max_f32_e32 v15, v122, v3
	v_min_f32_e32 v3, v122, v3
	v_max_f32_e32 v122, v2, v6
	v_min_f32_e32 v2, v2, v6
	v_max_f32_e32 v6, v5, v8
	v_min_f32_e32 v5, v5, v8
	v_max_f32_e32 v8, v10, v4
	v_min_f32_e32 v4, v10, v4
	v_max_f32_e32 v10, v12, v9
	v_min_f32_e32 v9, v12, v9
	v_max_f32_e32 v12, v7, v14
	v_min_f32_e32 v7, v7, v14
	v_max_f32_e32 v14, v13, v16
	v_min_f32_e32 v13, v13, v16
	v_max_f32_e32 v16, v17, v11
	v_min_f32_e32 v11, v17, v11
	v_max_f32_e32 v34, v33, v20
	v_min_f32_e32 v20, v33, v20
	v_max_f32_e32 v33, v19, v18
	v_min_f32_e32 v18, v19, v18
	v_max_f32_e32 v19, v21, v23
	v_min_f32_e32 v21, v21, v23
	v_max_f32_e32 v23, v24, v22
	v_min_f32_e32 v22, v24, v22
	v_max_f32_e32 v24, v26, v28
	v_min_f32_e32 v26, v26, v28
	v_max_f32_e32 v28, v27, v25
	v_min_f32_e32 v25, v27, v25
	v_max_f32_e32 v27, v29, v31
	v_min_f32_e32 v29, v29, v31
	v_max_f32_e32 v31, v32, v30
	v_min_f32_e32 v30, v32, v30
	v_max_f32_e32 v65, v64, v98
	v_min_f32_e32 v64, v64, v98
	v_max_f32_e32 v98, v51, v50
	v_min_f32_e32 v50, v51, v50
	v_max_f32_e32 v51, v52, v54
	v_min_f32_e32 v52, v52, v54
	v_max_f32_e32 v54, v55, v53
	v_min_f32_e32 v53, v55, v53
	v_max_f32_e32 v55, v57, v59
	v_min_f32_e32 v57, v57, v59
	v_max_f32_e32 v59, v58, v56
	v_min_f32_e32 v56, v58, v56
	v_max_f32_e32 v58, v60, v62
	v_min_f32_e32 v60, v60, v62
	v_max_f32_e32 v62, v63, v61
	v_min_f32_e32 v61, v63, v61
	v_max_f32_e32 v49, v48, v108
	v_min_f32_e32 v48, v48, v108
	v_max_f32_e32 v108, v107, v106
	v_min_f32_e32 v106, v107, v106
	v_max_f32_e32 v107, v109, v111
	v_min_f32_e32 v109, v109, v111
	v_max_f32_e32 v111, v112, v110
	v_min_f32_e32 v110, v112, v110
	v_max_f32_e32 v112, v114, v113
	v_min_f32_e32 v113, v114, v113
	v_max_f32_e32 v114, v43, v42
	v_min_f32_e32 v42, v43, v42
	v_max_f32_e32 v43, v44, v46
	v_min_f32_e32 v44, v44, v46
	v_max_f32_e32 v46, v47, v45
	v_min_f32_e32 v45, v47, v45
	v_max_f32_e32 v17, v15, v122
	v_min_f32_e32 v15, v15, v122
	v_max_f32_e32 v122, v3, v2
	v_min_f32_e32 v2, v3, v2
	v_max_f32_e32 v3, v4, v5
	v_min_f32_e32 v4, v4, v5
	v_max_f32_e32 v5, v8, v6
	v_min_f32_e32 v6, v8, v6
	v_max_f32_e32 v8, v10, v12
	v_min_f32_e32 v10, v10, v12
	v_max_f32_e32 v12, v9, v7
	v_min_f32_e32 v7, v9, v7
	v_max_f32_e32 v9, v11, v13
	v_min_f32_e32 v11, v11, v13
	v_max_f32_e32 v13, v16, v14
	v_min_f32_e32 v14, v16, v14
	v_max_f32_e32 v32, v34, v21
	v_min_f32_e32 v21, v34, v21
	v_max_f32_e32 v34, v20, v19
	v_min_f32_e32 v19, v20, v19
	v_max_f32_e32 v20, v33, v22
	v_min_f32_e32 v22, v33, v22
	v_max_f32_e32 v33, v18, v23
	v_min_f32_e32 v18, v18, v23
	v_max_f32_e32 v23, v29, v24
	v_min_f32_e32 v24, v29, v24
	v_max_f32_e32 v29, v27, v26
	v_min_f32_e32 v26, v27, v26
	v_max_f32_e32 v27, v30, v28
	v_min_f32_e32 v28, v30, v28
	v_max_f32_e32 v30, v31, v25
	v_min_f32_e32 v25, v31, v25
	v_max_f32_e32 v63, v65, v52
	v_min_f32_e32 v52, v65, v52
	v_max_f32_e32 v65, v64, v51
	v_min_f32_e32 v51, v64, v51
	v_max_f32_e32 v64, v98, v53
	v_min_f32_e32 v53, v98, v53
	v_max_f32_e32 v98, v50, v54
	v_min_f32_e32 v50, v50, v54
	v_max_f32_e32 v54, v60, v55
	v_min_f32_e32 v55, v60, v55
	v_max_f32_e32 v60, v58, v57
	v_min_f32_e32 v57, v58, v57
	v_max_f32_e32 v58, v61, v59
	v_min_f32_e32 v59, v61, v59
	v_max_f32_e32 v61, v62, v56
	v_min_f32_e32 v56, v62, v56
	v_max_f32_e32 v47, v49, v109
	v_min_f32_e32 v49, v49, v109
	v_max_f32_e32 v109, v48, v107
	v_min_f32_e32 v48, v48, v107
	v_max_f32_e32 v107, v108, v110
	v_min_f32_e32 v108, v108, v110
	v_max_f32_e32 v110, v106, v111
	v_min_f32_e32 v106, v106, v111
	v_max_f32_e32 v111, v44, v112
	v_min_f32_e32 v44, v44, v112
	v_max_f32_e32 v112, v43, v113
	v_min_f32_e32 v43, v43, v113
	v_max_f32_e32 v113, v45, v114
	v_min_f32_e32 v45, v45, v114
	v_max_f32_e32 v114, v46, v42
	v_min_f32_e32 v42, v46, v42
	v_max_f32_e32 v16, v17, v4
	v_min_f32_e32 v4, v17, v4
	v_max_f32_e32 v17, v15, v3
	v_min_f32_e32 v3, v15, v3
	v_max_f32_e32 v15, v122, v6
; #define CE_DESC(a, b) do { const float _t = fmaxf(a, b); b = fminf(a, b); a = _t; } while (0)
; __device__ __forceinline__ void sort16_desc(float (&v)[16]) {
; #pragma unroll
;     for (int k = 2; k <= 16; k <<= 1)
; #pragma unroll
;         for (int j = k >> 1; j > 0; j >>= 1)
; #pragma unroll
;             for (int i = 0; i < 16; ++i) { const int l = i ^ j; if (l > i) { if ((i & k) == 0 || k == 16) CE_DESC(v[i], v[l]); else CE_DESC(v[l], v[i]); } }
; }
	v_min_f32_e32 v6, v122, v6
	v_max_f32_e32 v122, v2, v5
	v_min_f32_e32 v2, v2, v5
	v_max_f32_e32 v5, v11, v8
	v_min_f32_e32 v8, v11, v8
	v_max_f32_e32 v11, v9, v10
	v_min_f32_e32 v9, v9, v10
	v_max_f32_e32 v10, v14, v12
	v_min_f32_e32 v12, v14, v12
	v_max_f32_e32 v14, v13, v7
	v_min_f32_e32 v7, v13, v7
	v_max_f32_e32 v31, v32, v20
	v_min_f32_e32 v20, v32, v20
	v_max_f32_e32 v32, v34, v33
	v_min_f32_e32 v33, v34, v33
	v_max_f32_e32 v34, v21, v22
	v_min_f32_e32 v21, v21, v22
	v_max_f32_e32 v22, v19, v18
	v_min_f32_e32 v18, v19, v18
	v_max_f32_e32 v19, v28, v24
	v_min_f32_e32 v24, v28, v24
	v_max_f32_e32 v28, v25, v26
	v_min_f32_e32 v25, v25, v26
	v_max_f32_e32 v26, v27, v23
	v_min_f32_e32 v23, v27, v23
	v_max_f32_e32 v27, v30, v29
	v_min_f32_e32 v29, v30, v29
	v_max_f32_e32 v62, v63, v64
	v_min_f32_e32 v63, v63, v64
	v_max_f32_e32 v64, v65, v98
	v_min_f32_e32 v65, v65, v98
	v_max_f32_e32 v98, v52, v53
	v_min_f32_e32 v52, v52, v53
	v_max_f32_e32 v53, v51, v50
	v_min_f32_e32 v50, v51, v50
	v_max_f32_e32 v51, v59, v55
	v_min_f32_e32 v55, v59, v55
	v_max_f32_e32 v59, v56, v57
	v_min_f32_e32 v56, v56, v57
	v_max_f32_e32 v57, v58, v54
	v_min_f32_e32 v54, v58, v54
	v_max_f32_e32 v58, v61, v60
	v_min_f32_e32 v60, v61, v60
	v_max_f32_e32 v46, v47, v107
	v_min_f32_e32 v47, v47, v107
	v_max_f32_e32 v107, v109, v110
	v_min_f32_e32 v109, v109, v110
	v_max_f32_e32 v110, v49, v108
	v_min_f32_e32 v49, v49, v108
	v_max_f32_e32 v108, v48, v106
	v_min_f32_e32 v48, v48, v106
	v_max_f32_e32 v106, v45, v44
	v_min_f32_e32 v44, v45, v44
	v_max_f32_e32 v45, v42, v43
	v_min_f32_e32 v42, v42, v43
	v_max_f32_e32 v43, v113, v111
	v_min_f32_e32 v111, v113, v111
	v_max_f32_e32 v113, v114, v112
	v_min_f32_e32 v112, v114, v112
	v_max_f32_e32 v13, v16, v15
	v_min_f32_e32 v15, v16, v15
	v_max_f32_e32 v16, v17, v122
	v_min_f32_e32 v17, v17, v122
	v_max_f32_e32 v122, v4, v6
	v_min_f32_e32 v4, v4, v6
	v_max_f32_e32 v6, v3, v2
	v_min_f32_e32 v2, v3, v2
	v_max_f32_e32 v3, v12, v8
	v_min_f32_e32 v8, v12, v8
	v_max_f32_e32 v12, v7, v9
	v_min_f32_e32 v7, v7, v9
	v_max_f32_e32 v9, v10, v5
	v_min_f32_e32 v5, v10, v5
	v_max_f32_e32 v10, v14, v11
	v_min_f32_e32 v11, v14, v11
	v_max_f32_e32 v30, v31, v32
	v_min_f32_e32 v31, v31, v32
	v_max_f32_e32 v32, v20, v33
	v_min_f32_e32 v20, v20, v33
	v_max_f32_e32 v33, v34, v22
	v_min_f32_e32 v22, v34, v22
	v_max_f32_e32 v34, v21, v18
	v_min_f32_e32 v18, v21, v18
	v_max_f32_e32 v21, v25, v24
	v_min_f32_e32 v24, v25, v24
	v_max_f32_e32 v25, v28, v19
	v_min_f32_e32 v19, v28, v19
	v_max_f32_e32 v28, v29, v23
	v_min_f32_e32 v23, v29, v23
	v_max_f32_e32 v29, v27, v26
	v_min_f32_e32 v26, v27, v26
	v_max_f32_e32 v61, v62, v64
	v_min_f32_e32 v62, v62, v64
	v_max_f32_e32 v64, v63, v65
	v_min_f32_e32 v63, v63, v65
	v_max_f32_e32 v65, v98, v53
	v_min_f32_e32 v53, v98, v53
	v_max_f32_e32 v98, v52, v50
	v_min_f32_e32 v50, v52, v50
	v_max_f32_e32 v52, v56, v55
	v_min_f32_e32 v55, v56, v55
	v_max_f32_e32 v56, v59, v51
	v_min_f32_e32 v51, v59, v51
	v_max_f32_e32 v59, v60, v54
	v_min_f32_e32 v54, v60, v54
	v_max_f32_e32 v60, v58, v57
	v_min_f32_e32 v57, v58, v57
	v_max_f32_e32 v114, v46, v107
	v_min_f32_e32 v46, v46, v107
	v_max_f32_e32 v107, v47, v109
	v_min_f32_e32 v47, v47, v109
	v_max_f32_e32 v109, v110, v108
	v_min_f32_e32 v108, v110, v108
	v_max_f32_e32 v110, v49, v48
	v_min_f32_e32 v48, v49, v48
	v_max_f32_e32 v49, v42, v44
	v_min_f32_e32 v42, v42, v44
	v_max_f32_e32 v44, v45, v106
	v_min_f32_e32 v45, v45, v106
	v_max_f32_e32 v106, v112, v111
	v_min_f32_e32 v111, v112, v111
	v_max_f32_e32 v112, v113, v43
	v_min_f32_e32 v43, v113, v43
	v_max_f32_e32 v14, v13, v16
	v_min_f32_e32 v13, v13, v16
	v_max_f32_e32 v16, v15, v17
	v_min_f32_e32 v15, v15, v17
	v_max_f32_e32 v17, v122, v6
	v_min_f32_e32 v6, v122, v6
	v_max_f32_e32 v122, v4, v2
	v_min_f32_e32 v2, v4, v2
	v_max_f32_e32 v4, v7, v8
	v_min_f32_e32 v7, v7, v8
	v_max_f32_e32 v8, v12, v3
	v_min_f32_e32 v3, v12, v3
	v_max_f32_e32 v12, v11, v5
	v_min_f32_e32 v5, v11, v5
	v_max_f32_e32 v11, v10, v9
	v_min_f32_e32 v9, v10, v9
	v_max_f32_e32 v27, v30, v24
	v_min_f32_e32 v24, v30, v24
	v_max_f32_e32 v30, v31, v21
	v_min_f32_e32 v21, v31, v21
	v_max_f32_e32 v31, v32, v19
	v_min_f32_e32 v19, v32, v19
	v_max_f32_e32 v32, v20, v25
	v_min_f32_e32 v20, v20, v25
	v_max_f32_e32 v25, v33, v23
	v_min_f32_e32 v23, v33, v23
	v_max_f32_e32 v33, v22, v28
	v_min_f32_e32 v22, v22, v28
	v_max_f32_e32 v28, v34, v26
	v_min_f32_e32 v26, v34, v26
	v_max_f32_e32 v34, v18, v29
	v_min_f32_e32 v18, v18, v29
	v_max_f32_e32 v58, v61, v55
	v_min_f32_e32 v55, v61, v55
	v_max_f32_e32 v61, v62, v52
	v_min_f32_e32 v52, v62, v52
	v_max_f32_e32 v62, v64, v51
	v_min_f32_e32 v51, v64, v51
	v_max_f32_e32 v64, v63, v56
	v_min_f32_e32 v56, v63, v56
	v_max_f32_e32 v63, v65, v54
	v_min_f32_e32 v54, v65, v54
	v_max_f32_e32 v65, v53, v59
	v_min_f32_e32 v53, v53, v59
	v_max_f32_e32 v59, v98, v57
	v_min_f32_e32 v57, v98, v57
	v_max_f32_e32 v98, v50, v60
	v_min_f32_e32 v50, v50, v60
	v_max_f32_e32 v113, v114, v42
	v_min_f32_e32 v42, v114, v42
	v_max_f32_e32 v114, v46, v49
	v_min_f32_e32 v46, v46, v49
	v_max_f32_e32 v49, v107, v45
	v_min_f32_e32 v45, v107, v45
	v_max_f32_e32 v107, v47, v44
	v_min_f32_e32 v44, v47, v44
	v_max_f32_e32 v47, v109, v111
	v_min_f32_e32 v109, v109, v111
	v_max_f32_e32 v111, v108, v106
	v_min_f32_e32 v106, v108, v106
	v_max_f32_e32 v108, v110, v43
	v_min_f32_e32 v43, v110, v43
	v_max_f32_e32 v110, v48, v112
	v_min_f32_e32 v48, v48, v112
	v_max_f32_e32 v10, v14, v7
	v_min_f32_e32 v7, v14, v7
	v_max_f32_e32 v14, v13, v4
	v_min_f32_e32 v4, v13, v4
	v_max_f32_e32 v13, v16, v3
	v_min_f32_e32 v3, v16, v3
	v_max_f32_e32 v16, v15, v8
; #define CE_DESC(a, b) do { const float _t = fmaxf(a, b); b = fminf(a, b); a = _t; } while (0)
; __device__ __forceinline__ void sort16_desc(float (&v)[16]) {
; #pragma unroll
;     for (int k = 2; k <= 16; k <<= 1)
; #pragma unroll
;         for (int j = k >> 1; j > 0; j >>= 1)
; #pragma unroll
;             for (int i = 0; i < 16; ++i) { const int l = i ^ j; if (l > i) { if ((i & k) == 0 || k == 16) CE_DESC(v[i], v[l]); else CE_DESC(v[l], v[i]); } }
; }
; __device__ __forceinline__ void merge16_desc(float (&a)[16], const float (&b)[16]) {
; #pragma unroll
;     for (int i = 0; i < 16; ++i) a[i] = fmaxf(a[i], b[15 - i]);
; #pragma unroll
;     for (int j = 8; j > 0; j >>= 1)
; #pragma unroll
;         for (int i = 0; i < 16; ++i) { const int l = i ^ j; if (l > i) CE_DESC(a[i], a[l]); }
; }
	v_min_f32_e32 v8, v15, v8
	v_max_f32_e32 v15, v17, v5
	v_min_f32_e32 v5, v17, v5
	v_max_f32_e32 v17, v6, v12
	v_min_f32_e32 v6, v6, v12
	v_max_f32_e32 v12, v122, v9
	v_min_f32_e32 v9, v122, v9
	v_max_f32_e32 v122, v2, v11
	v_min_f32_e32 v2, v2, v11
	v_max_f32_e32 v29, v27, v25
	v_min_f32_e32 v25, v27, v25
	v_max_f32_e32 v27, v30, v33
	v_min_f32_e32 v33, v30, v33
	v_max_f32_e32 v30, v31, v28
	v_min_f32_e32 v28, v31, v28
	v_max_f32_e32 v31, v32, v34
	v_min_f32_e32 v32, v32, v34
	v_max_f32_e32 v34, v24, v23
	v_min_f32_e32 v35, v24, v23
	v_max_f32_e32 v36, v21, v22
	v_min_f32_e32 v37, v21, v22
	v_max_f32_e32 v21, v19, v26
	v_min_f32_e32 v38, v19, v26
	v_max_f32_e32 v39, v20, v18
	v_min_f32_e32 v40, v20, v18
	v_max_f32_e32 v60, v58, v63
	v_min_f32_e32 v58, v58, v63
	v_max_f32_e32 v63, v61, v65
	v_min_f32_e32 v61, v61, v65
	v_max_f32_e32 v65, v62, v59
	v_min_f32_e32 v59, v62, v59
	v_max_f32_e32 v62, v64, v98
	v_min_f32_e32 v64, v64, v98
	v_max_f32_e32 v98, v55, v54
	v_min_f32_e32 v54, v55, v54
	v_max_f32_e32 v55, v52, v53
	v_min_f32_e32 v52, v52, v53
	v_max_f32_e32 v53, v51, v57
	v_min_f32_e32 v51, v51, v57
	v_max_f32_e32 v57, v56, v50
	v_min_f32_e32 v50, v56, v50
	v_max_f32_e32 v112, v113, v47
	v_min_f32_e32 v47, v113, v47
	v_max_f32_e32 v113, v114, v111
	v_min_f32_e32 v111, v114, v111
	v_max_f32_e32 v114, v49, v108
	v_min_f32_e32 v49, v49, v108
	v_max_f32_e32 v108, v107, v110
	v_min_f32_e32 v107, v107, v110
	v_max_f32_e32 v110, v42, v109
	v_min_f32_e32 v42, v42, v109
	v_max_f32_e32 v109, v46, v106
	v_min_f32_e32 v46, v46, v106
	v_max_f32_e32 v106, v45, v43
	v_min_f32_e32 v43, v45, v43
	v_max_f32_e32 v45, v44, v48
	v_min_f32_e32 v44, v44, v48
	v_max_f32_e32 v11, v10, v15
	v_min_f32_e32 v10, v10, v15
	v_max_f32_e32 v15, v14, v17
	v_min_f32_e32 v14, v14, v17
	v_max_f32_e32 v17, v13, v12
	v_min_f32_e32 v12, v13, v12
	v_max_f32_e32 v13, v16, v122
	v_min_f32_e32 v16, v16, v122
	v_max_f32_e32 v122, v7, v5
	v_min_f32_e32 v5, v7, v5
	v_max_f32_e32 v7, v4, v6
	v_min_f32_e32 v4, v4, v6
	v_max_f32_e32 v6, v3, v9
	v_min_f32_e32 v3, v3, v9
	v_max_f32_e32 v9, v8, v2
	v_min_f32_e32 v2, v8, v2
	v_max_f32_e32 v22, v29, v30
	v_min_f32_e32 v18, v29, v30
	v_max_f32_e32 v30, v27, v31
	v_min_f32_e32 v26, v27, v31
	v_max_f32_e32 v23, v25, v28
	v_min_f32_e32 v19, v25, v28
	v_max_f32_e32 v31, v33, v32
	v_min_f32_e32 v27, v33, v32
	v_max_f32_e32 v24, v34, v21
	v_min_f32_e32 v20, v34, v21
	v_max_f32_e32 v32, v36, v39
	v_min_f32_e32 v28, v36, v39
	v_max_f32_e32 v25, v35, v38
	v_min_f32_e32 v21, v35, v38
	v_max_f32_e32 v33, v37, v40
	v_min_f32_e32 v29, v37, v40
	v_max_f32_e32 v56, v60, v65
	v_min_f32_e32 v60, v60, v65
	v_max_f32_e32 v65, v63, v62
	v_min_f32_e32 v62, v63, v62
	v_max_f32_e32 v63, v58, v59
	v_min_f32_e32 v58, v58, v59
	v_max_f32_e32 v59, v61, v64
	v_min_f32_e32 v61, v61, v64
	v_max_f32_e32 v64, v98, v53
	v_min_f32_e32 v53, v98, v53
	v_max_f32_e32 v98, v55, v57
	v_min_f32_e32 v55, v55, v57
	v_max_f32_e32 v57, v54, v51
	v_min_f32_e32 v51, v54, v51
	v_max_f32_e32 v54, v52, v50
	v_min_f32_e32 v50, v52, v50
	v_max_f32_e32 v48, v112, v114
	v_min_f32_e32 v112, v112, v114
	v_max_f32_e32 v114, v113, v108
	v_min_f32_e32 v108, v113, v108
	v_max_f32_e32 v113, v47, v49
	v_min_f32_e32 v47, v47, v49
	v_max_f32_e32 v49, v111, v107
	v_min_f32_e32 v107, v111, v107
	v_max_f32_e32 v111, v110, v106
	v_min_f32_e32 v106, v110, v106
	v_max_f32_e32 v110, v109, v45
	v_min_f32_e32 v45, v109, v45
	v_max_f32_e32 v109, v42, v43
	v_min_f32_e32 v42, v42, v43
	v_max_f32_e32 v43, v46, v44
	v_min_f32_e32 v44, v46, v44
	v_max_f32_e32 v8, v11, v17
	v_min_f32_e32 v11, v11, v17
	v_max_f32_e32 v17, v15, v13
	v_min_f32_e32 v13, v15, v13
	v_max_f32_e32 v15, v10, v12
	v_min_f32_e32 v10, v10, v12
	v_max_f32_e32 v12, v14, v16
	v_min_f32_e32 v14, v14, v16
	v_max_f32_e32 v16, v122, v6
	v_min_f32_e32 v6, v122, v6
	v_max_f32_e32 v122, v7, v9
	v_min_f32_e32 v7, v7, v9
	v_max_f32_e32 v9, v5, v3
	v_min_f32_e32 v3, v5, v3
	v_max_f32_e32 v5, v4, v2
	v_min_f32_e32 v2, v4, v2
	v_min_f32_e32 v41, v22, v30
	v_min_f32_e32 v40, v18, v26
	v_min_f32_e32 v39, v23, v31
	v_min_f32_e32 v38, v19, v27
	v_min_f32_e32 v37, v24, v32
	v_min_f32_e32 v36, v20, v28
	v_min_f32_e32 v35, v25, v33
	v_min_f32_e32 v34, v21, v29
	v_min_f32_e32 v52, v56, v65
	v_min_f32_e32 v99, v60, v62
	v_min_f32_e32 v100, v63, v59
	v_min_f32_e32 v101, v58, v61
	v_min_f32_e32 v102, v64, v98
	v_min_f32_e32 v103, v53, v55
	v_min_f32_e32 v104, v57, v54
	v_min_f32_e32 v105, v51, v50
	v_min_f32_e32 v46, v48, v114
	v_min_f32_e32 v115, v112, v108
	v_min_f32_e32 v116, v113, v49
	v_min_f32_e32 v117, v47, v107
	v_min_f32_e32 v118, v111, v110
	v_min_f32_e32 v119, v106, v45
	v_min_f32_e32 v120, v109, v43
	v_min_f32_e32 v121, v42, v44
	v_min_f32_e32 v4, v8, v17
	v_min_f32_e32 v123, v11, v13
	v_min_f32_e32 v124, v15, v12
	v_min_f32_e32 v125, v10, v14
	v_min_f32_e32 v140, v16, v122
	v_min_f32_e32 v141, v6, v7
	v_min_f32_e32 v181, v9, v5
	v_min_f32_e32 v182, v3, v2
	v_max3_f32 v22, v22, v30, v105
	v_max3_f32 v30, v41, v51, v50
	v_max3_f32 v18, v18, v26, v104
	v_max3_f32 v26, v40, v57, v54
	v_max3_f32 v23, v23, v31, v103
	v_max3_f32 v31, v39, v53, v55
	v_max3_f32 v19, v19, v27, v102
	v_max3_f32 v27, v38, v64, v98
	v_max3_f32 v24, v24, v32, v101
	v_max3_f32 v32, v37, v58, v61
	v_max3_f32 v20, v20, v28, v100
	v_max3_f32 v28, v36, v63, v59
	v_max3_f32 v25, v25, v33, v99
	v_max3_f32 v33, v35, v60, v62
	v_max3_f32 v21, v21, v29, v52
	v_max3_f32 v29, v34, v56, v65
	v_max3_f32 v48, v48, v114, v182
	v_max3_f32 v2, v46, v3, v2
	v_max3_f32 v3, v112, v108, v181
	v_max3_f32 v5, v115, v9, v5
	v_max3_f32 v9, v113, v49, v141
	v_max3_f32 v6, v116, v6, v7
	v_max3_f32 v7, v47, v107, v140
; #define CE_DESC(a, b) do { const float _t = fmaxf(a, b); b = fminf(a, b); a = _t; } while (0)
; __device__ __forceinline__ void merge16_desc(float (&a)[16], const float (&b)[16]) {
; #pragma unroll
;     for (int i = 0; i < 16; ++i) a[i] = fmaxf(a[i], b[15 - i]);
; #pragma unroll
;     for (int j = 8; j > 0; j >>= 1)
; #pragma unroll
;         for (int i = 0; i < 16; ++i) { const int l = i ^ j; if (l > i) CE_DESC(a[i], a[l]); }
; }
; __device__ __forceinline__ void route_half(float (&top)[16], LAS const unsigned char* keys_lds, const bf16_t* __restrict__ qrow, int r32, int hi) {
;     ...
;     merge16_desc(g[0], g[1]); merge16_desc(g[2], g[3]); merge16_desc(g[0], g[2]);
;     float o[16];
; #pragma unroll
;     for (int i = 0; i < 16; ++i) { g[0][i] = __uint_as_float(__float_as_uint(g[0][i]) | hi4); o[i] = __shfl_xor(g[0][i], 32); }
;     merge16_desc(g[0], o);
	v_max3_f32 v16, v117, v16, v122
	v_max3_f32 v46, v111, v110, v125
	v_max3_f32 v10, v118, v10, v14
	v_max3_f32 v14, v106, v45, v124
	v_max3_f32 v12, v119, v15, v12
	v_max3_f32 v15, v109, v43, v123
	v_max3_f32 v11, v120, v11, v13
	v_max3_f32 v4, v42, v44, v4
	v_max3_f32 v8, v121, v8, v17
	v_max_f32_e32 v34, v22, v24
	v_min_f32_e32 v22, v22, v24
	v_max_f32_e32 v24, v30, v32
	v_min_f32_e32 v30, v30, v32
	v_max_f32_e32 v32, v18, v20
	v_min_f32_e32 v18, v18, v20
	v_max_f32_e32 v20, v26, v28
	v_min_f32_e32 v26, v26, v28
	v_max_f32_e32 v28, v23, v25
	v_min_f32_e32 v23, v23, v25
	v_max_f32_e32 v25, v31, v33
	v_min_f32_e32 v31, v31, v33
	v_max_f32_e32 v33, v19, v21
	v_min_f32_e32 v19, v19, v21
	v_max_f32_e32 v21, v27, v29
	v_min_f32_e32 v27, v27, v29
	v_max_f32_e32 v13, v48, v46
	v_min_f32_e32 v17, v48, v46
	v_max_f32_e32 v42, v2, v10
	v_min_f32_e32 v2, v2, v10
	v_max_f32_e32 v10, v3, v14
	v_min_f32_e32 v3, v3, v14
	v_max_f32_e32 v14, v5, v12
	v_min_f32_e32 v5, v5, v12
	v_max_f32_e32 v12, v9, v15
	v_min_f32_e32 v9, v9, v15
	v_max_f32_e32 v15, v6, v11
	v_min_f32_e32 v6, v6, v11
	v_max_f32_e32 v11, v7, v4
	v_min_f32_e32 v4, v7, v4
	v_max_f32_e32 v7, v16, v8
	v_min_f32_e32 v8, v16, v8
	v_max_f32_e32 v29, v34, v28
	v_min_f32_e32 v28, v34, v28
	v_max_f32_e32 v34, v24, v25
	v_min_f32_e32 v24, v24, v25
	v_max_f32_e32 v25, v32, v33
	v_min_f32_e32 v32, v32, v33
	v_max_f32_e32 v33, v20, v21
	v_min_f32_e32 v20, v20, v21
	v_max_f32_e32 v21, v22, v23
	v_min_f32_e32 v22, v22, v23
	v_max_f32_e32 v23, v30, v31
	v_min_f32_e32 v30, v30, v31
	v_max_f32_e32 v31, v18, v19
	v_min_f32_e32 v18, v18, v19
	v_max_f32_e32 v19, v26, v27
	v_min_f32_e32 v26, v26, v27
	v_max_f32_e32 v16, v13, v12
	v_min_f32_e32 v12, v13, v12
	v_max_f32_e32 v13, v42, v15
	v_min_f32_e32 v15, v42, v15
	v_max_f32_e32 v42, v10, v11
	v_min_f32_e32 v10, v10, v11
	v_max_f32_e32 v11, v14, v7
	v_min_f32_e32 v7, v14, v7
	v_max_f32_e32 v14, v17, v9
	v_min_f32_e32 v9, v17, v9
	v_max_f32_e32 v17, v2, v6
	v_min_f32_e32 v2, v2, v6
	v_max_f32_e32 v6, v3, v4
	v_min_f32_e32 v3, v3, v4
	v_max_f32_e32 v4, v5, v8
	v_min_f32_e32 v5, v5, v8
	v_max_f32_e32 v27, v29, v25
	v_min_f32_e32 v25, v29, v25
	v_max_f32_e32 v29, v34, v33
	v_min_f32_e32 v33, v34, v33
	v_max_f32_e32 v34, v28, v32
	v_min_f32_e32 v28, v28, v32
	v_max_f32_e32 v32, v24, v20
	v_min_f32_e32 v20, v24, v20
	v_max_f32_e32 v24, v21, v31
	v_min_f32_e32 v21, v21, v31
	v_max_f32_e32 v31, v23, v19
	v_min_f32_e32 v19, v23, v19
	v_max_f32_e32 v23, v22, v18
	v_min_f32_e32 v18, v22, v18
	v_max_f32_e32 v22, v30, v26
	v_min_f32_e32 v26, v30, v26
	v_max_f32_e32 v8, v16, v42
	v_min_f32_e32 v16, v16, v42
	v_max_f32_e32 v42, v13, v11
	v_min_f32_e32 v11, v13, v11
	v_max_f32_e32 v13, v12, v10
	v_min_f32_e32 v10, v12, v10
	v_max_f32_e32 v12, v15, v7
	v_min_f32_e32 v7, v15, v7
	v_max_f32_e32 v15, v14, v6
	v_min_f32_e32 v6, v14, v6
	v_max_f32_e32 v14, v17, v4
	v_min_f32_e32 v4, v17, v4
	v_max_f32_e32 v17, v9, v3
	v_min_f32_e32 v3, v9, v3
	v_max_f32_e32 v9, v2, v5
	v_min_f32_e32 v2, v2, v5
	v_min_f32_e32 v30, v27, v29
	v_min_f32_e32 v35, v25, v33
	v_min_f32_e32 v36, v34, v32
	v_min_f32_e32 v37, v28, v20
	v_min_f32_e32 v38, v24, v31
	v_min_f32_e32 v39, v21, v19
	v_min_f32_e32 v40, v23, v22
	v_min_f32_e32 v41, v18, v26
	v_min_f32_e32 v5, v8, v42
	v_min_f32_e32 v43, v16, v11
	v_min_f32_e32 v44, v13, v12
	v_min_f32_e32 v45, v10, v7
	v_min_f32_e32 v46, v15, v14
	v_min_f32_e32 v47, v6, v4
	v_min_f32_e32 v48, v17, v9
	v_min_f32_e32 v49, v3, v2
	v_max3_f32 v27, v27, v29, v49
	v_max3_f32 v2, v30, v3, v2
	v_max3_f32 v3, v25, v33, v48
	v_max3_f32 v9, v35, v17, v9
	v_max3_f32 v17, v34, v32, v47
	v_max3_f32 v4, v36, v6, v4
	v_max3_f32 v6, v28, v20, v46
	v_max3_f32 v14, v37, v15, v14
	v_max3_f32 v15, v24, v31, v45
	v_max3_f32 v7, v38, v10, v7
	v_max3_f32 v10, v21, v19, v44
	v_max3_f32 v12, v39, v13, v12
	v_max3_f32 v13, v23, v22, v43
	v_max3_f32 v11, v40, v16, v11
	v_max3_f32 v5, v18, v26, v5
	v_max3_f32 v8, v41, v8, v42
	v_max_f32_e32 v16, v27, v15
	v_min_f32_e32 v15, v27, v15
	v_max_f32_e32 v18, v2, v7
	v_min_f32_e32 v2, v2, v7
	v_max_f32_e32 v7, v3, v10
	v_min_f32_e32 v3, v3, v10
	v_max_f32_e32 v10, v9, v12
	v_min_f32_e32 v9, v9, v12
	v_max_f32_e32 v12, v17, v13
	v_min_f32_e32 v13, v17, v13
	v_max_f32_e32 v17, v4, v11
	v_min_f32_e32 v4, v4, v11
	v_max_f32_e32 v11, v6, v5
	v_min_f32_e32 v5, v6, v5
	v_max_f32_e32 v6, v14, v8
	v_min_f32_e32 v8, v14, v8
	v_max_f32_e32 v14, v16, v12
	v_min_f32_e32 v12, v16, v12
	v_max_f32_e32 v16, v18, v17
	v_min_f32_e32 v17, v18, v17
	v_max_f32_e32 v18, v7, v11
	v_min_f32_e32 v7, v7, v11
	v_max_f32_e32 v11, v10, v6
	v_min_f32_e32 v6, v10, v6
	v_max_f32_e32 v10, v15, v13
	v_min_f32_e32 v13, v15, v13
	v_max_f32_e32 v15, v2, v4
	v_min_f32_e32 v2, v2, v4
	v_max_f32_e32 v4, v3, v5
	v_min_f32_e32 v3, v3, v5
	v_max_f32_e32 v5, v9, v8
	v_min_f32_e32 v8, v9, v8
	v_max_f32_e32 v9, v14, v18
	v_min_f32_e32 v14, v14, v18
	v_max_f32_e32 v18, v16, v11
	v_min_f32_e32 v11, v16, v11
	v_max_f32_e32 v16, v12, v7
	v_min_f32_e32 v7, v12, v7
	v_max_f32_e32 v12, v17, v6
	v_min_f32_e32 v6, v17, v6
	v_max_f32_e32 v17, v10, v4
	v_min_f32_e32 v4, v10, v4
	v_max_f32_e32 v10, v15, v5
	v_min_f32_e32 v5, v15, v5
	v_max_f32_e32 v15, v13, v3
	v_min_f32_e32 v3, v13, v3
	v_max_f32_e32 v13, v2, v8
	v_min_f32_e32 v2, v2, v8
	v_max_f32_e32 v8, v9, v18
	v_min_f32_e32 v9, v9, v18
	v_max_f32_e32 v18, v14, v11
	v_min_f32_e32 v11, v14, v11
	v_max_f32_e32 v14, v16, v12
	v_min_f32_e32 v12, v16, v12
	v_max_f32_e32 v16, v7, v6
	v_min_f32_e32 v23, v7, v6
	v_max_f32_e32 v27, v17, v10
	v_min_f32_e32 v28, v17, v10
	v_max_f32_e32 v29, v4, v5
	v_min_f32_e32 v30, v4, v5
	v_max_f32_e32 v31, v15, v13
	v_min_f32_e32 v32, v15, v13
	v_max_f32_e32 v33, v3, v2
	v_min_f32_e32 v34, v3, v2
	v_or_b32_e32 v26, v144, v8
	v_or_b32_e32 v25, v144, v9
	v_or_b32_e32 v24, v144, v18
	v_or_b32_e32 v22, v144, v11
	v_or_b32_e32 v21, v144, v14
	v_or_b32_e32 v20, v144, v12
	v_or_b32_e32 v19, v144, v16
	v_or_b32_e32 v18, v144, v23
	v_or_b32_e32 v17, v144, v27
	v_or_b32_e32 v15, v144, v28
	v_or_b32_e32 v14, v144, v29
	v_or_b32_e32 v13, v144, v30
	v_or_b32_e32 v12, v144, v31
	v_or_b32_e32 v11, v144, v32
	v_or_b32_e32 v9, v144, v33
	v_or_b32_e32 v8, v144, v34
	ds_bpermute_b32 v2, v142, v26
	ds_bpermute_b32 v3, v142, v25
	ds_bpermute_b32 v4, v142, v24
	ds_bpermute_b32 v5, v142, v22
	ds_bpermute_b32 v6, v142, v21
	ds_bpermute_b32 v7, v142, v20
	ds_bpermute_b32 v10, v142, v19
	ds_bpermute_b32 v16, v142, v18
	ds_bpermute_b32 v23, v142, v17
	ds_bpermute_b32 v27, v142, v15
	ds_bpermute_b32 v28, v142, v14
	ds_bpermute_b32 v29, v142, v13
	ds_bpermute_b32 v30, v142, v12
	ds_bpermute_b32 v31, v142, v11
	ds_bpermute_b32 v32, v142, v9
	ds_bpermute_b32 v33, v142, v8
	s_and_b64 vcc, exec, s[10:11]
	s_cbranch_vccnz .LBB0_926
; template <bool SIGNED4> __device__ __forceinline__ void qrow_store(const f32x4 (&v)[4], unsigned char* q, float* scale, int row, int lane) {
;     float ss = 0.f;
; #pragma unroll
;     for (int j = 0; j < 4; ++j) ss += v[j].x * v[j].x + v[j].y * v[j].y + v[j].z * v[j].z + v[j].w * v[j].w;
;     ss = wave_sum(ss);
;     const float sc = ss > 0.f ? 0.3352f * sqrtf(ss * (1.f / 1024.f)) : 1.f, inv = __builtin_amdgcn_rcpf(sc);
;     unsigned n[16];
; #pragma unroll
;     for (int j = 0; j < 4; ++j) {
; #pragma unroll
;         for (int i = 0; i < 4; ++i) { const float f = floorf(v[j][i] * inv) + 8.f; n[4 * j + i] = (unsigned)fminf(fmaxf(f, 0.f), 15.f); } }
;     u32x2 o;
; #pragma unroll
;     for (int m = 0; m < 2; ++m) { unsigned w = 0;
; #pragma unroll
;         for (int b = 0; b < 4; ++b) w |= (n[8 * m + b] | (n[8 * m + 4 + b] << 4)) << (8 * b);
;         o[m] = SIGNED4 ? (w ^ 0x88888888u) : w; }
;     *(u32x2*)(q + (size_t)row * 1024 + lane * 16) = o;
;     if (lane == 0) scale[row] = sc;
; }
	v_mul_f32_e32 v34, v67, v67
	v_mul_f32_e32 v35, v71, v71
	v_fmac_f32_e32 v34, v66, v66
	v_fmac_f32_e32 v35, v70, v70
	v_fmac_f32_e32 v34, v68, v68
	v_fmac_f32_e32 v35, v72, v72
	v_fmac_f32_e32 v34, v69, v69
	v_fmac_f32_e32 v35, v73, v73
	v_add_f32_e32 v34, v34, v35
	v_mul_f32_e32 v35, v75, v75
	v_fmac_f32_e32 v35, v74, v74
	v_fmac_f32_e32 v35, v76, v76
	v_fmac_f32_e32 v35, v77, v77
	v_add_f32_e32 v34, v35, v34
	v_mul_f32_e32 v35, v83, v83
	v_fmac_f32_e32 v35, v82, v82
	v_fmac_f32_e32 v35, v84, v84
	v_fmac_f32_e32 v35, v85, v85
	v_add_f32_e32 v34, v35, v34
	s_ashr_i32 s27, s26, 31
	s_lshl_b64 s[0:1], s[26:27], 10
	v_add_f32_dpp v34, v34, v34 quad_perm:[1,0,3,2] row_mask:0xf bank_mask:0xf bound_ctrl:1
	s_nop 1
	v_add_f32_dpp v34, v34, v34 quad_perm:[2,3,0,1] row_mask:0xf bank_mask:0xf bound_ctrl:1
	s_nop 1
	v_add_f32_dpp v34, v34, v34 row_ror:4 row_mask:0xf bank_mask:0xf bound_ctrl:1
	s_nop 1
	v_add_f32_dpp v34, v34, v34 row_ror:8 row_mask:0xf bank_mask:0xf bound_ctrl:1
	v_mov_b32_e32 v35, v34
	s_nop 1
	v_permlane16_swap_b32_e32 v34, v35
	v_add_f32_e32 v34, v34, v35
	v_mov_b32_e32 v35, v34
	s_nop 1
	v_permlane32_swap_b32_e32 v34, v35
	v_add_f32_e32 v34, v34, v35
	v_mul_f32_e32 v35, 0x3a800000, v34
	v_mul_f32_e32 v36, 0x4f800000, v35
	v_cmp_gt_f32_e32 vcc, s44, v35
	s_nop 1
	v_cndmask_b32_e32 v35, v35, v36, vcc
	v_sqrt_f32_e32 v36, v35
	s_nop 0
	v_add_u32_e32 v37, -1, v36
	v_fma_f32 v38, -v37, v36, v35
	v_cmp_ge_f32_e64 s[10:11], 0, v38
	v_add_u32_e32 v38, 1, v36
	s_nop 0
	v_cndmask_b32_e64 v37, v36, v37, s[10:11]
	v_fma_f32 v36, -v38, v36, v35
	v_cmp_lt_f32_e64 s[10:11], 0, v36
	s_nop 1
	v_cndmask_b32_e64 v36, v37, v38, s[10:11]
	v_mul_f32_e32 v37, 0x37800000, v36
	v_cndmask_b32_e32 v36, v36, v37, vcc
	v_cmp_class_f32_e32 vcc, v35, v147
	s_nop 1
	v_cndmask_b32_e32 v35, v36, v35, vcc
	v_mul_f32_e32 v35, 0x3eab9f56, v35
	v_cmp_lt_f32_e32 vcc, 0, v34
	s_nop 1
	v_cndmask_b32_e32 v34, 1.0, v35, vcc
	v_rcp_f32_e32 v35, v34
	s_nop 0
	v_mul_f32_e32 v36, v66, v35
	v_mul_f32_e32 v39, v69, v35
	v_mul_f32_e32 v43, v73, v35
	v_floor_f32_e32 v36, v36
	v_mul_f32_e32 v37, v67, v35
	v_mul_f32_e32 v38, v68, v35
	v_floor_f32_e32 v39, v39
	v_mul_f32_e32 v42, v72, v35
	v_floor_f32_e32 v43, v43
	v_add_f32_e32 v36, 0x41000000, v36
	v_floor_f32_e32 v37, v37
	v_floor_f32_e32 v38, v38
	v_add_f32_e32 v39, 0x41000000, v39
	v_mul_f32_e32 v40, v70, v35
	v_mul_f32_e32 v41, v71, v35
	v_floor_f32_e32 v42, v42
	v_add_f32_e32 v43, 0x41000000, v43
	v_med3_f32 v36, v36, 0, v148
	v_add_f32_e32 v37, 0x41000000, v37
	v_add_f32_e32 v38, 0x41000000, v38
	v_med3_f32 v39, v39, 0, v148
	v_floor_f32_e32 v40, v40
	v_floor_f32_e32 v41, v41
	v_add_f32_e32 v42, 0x41000000, v42
	v_med3_f32 v43, v43, 0, v148
	v_mul_f32_e32 v44, v74, v35
	v_mul_f32_e32 v45, v75, v35
	v_mul_f32_e32 v46, v76, v35
	v_mul_f32_e32 v47, v77, v35
	v_mul_f32_e32 v48, v82, v35
	v_mul_f32_e32 v49, v83, v35
	v_mul_f32_e32 v50, v84, v35
	v_mul_f32_e32 v35, v85, v35
	v_cvt_u32_f32_e32 v36, v36
	v_med3_f32 v37, v37, 0, v148
	v_med3_f32 v38, v38, 0, v148
	v_cvt_u32_f32_e32 v39, v39
	v_add_f32_e32 v40, 0x41000000, v40
	v_add_f32_e32 v41, 0x41000000, v41
	v_med3_f32 v42, v42, 0, v148
	v_cvt_u32_f32_e32 v43, v43
	v_floor_f32_e32 v44, v44
	v_floor_f32_e32 v47, v47
	v_floor_f32_e32 v35, v35
	v_cvt_u32_f32_e32 v37, v37
	v_cvt_u32_f32_sdwa v38, v38 dst_sel:WORD_1 dst_unused:UNUSED_PAD src0_sel:DWORD
	v_med3_f32 v40, v40, 0, v148
	v_med3_f32 v41, v41, 0, v148
	v_cvt_u32_f32_e32 v42, v42
	v_add_f32_e32 v44, 0x41000000, v44
	v_floor_f32_e32 v45, v45
	v_floor_f32_e32 v46, v46
	v_add_f32_e32 v47, 0x41000000, v47
	v_floor_f32_e32 v50, v50
	v_add_f32_e32 v35, 0x41000000, v35
	v_cvt_u32_f32_e32 v40, v40
	v_cvt_u32_f32_e32 v41, v41
	v_med3_f32 v44, v44, 0, v148
	v_add_f32_e32 v45, 0x41000000, v45
	v_add_f32_e32 v46, 0x41000000, v46
	v_med3_f32 v47, v47, 0, v148
	v_floor_f32_e32 v48, v48
	v_floor_f32_e32 v49, v49
	v_add_f32_e32 v50, 0x41000000, v50
	v_med3_f32 v35, v35, 0, v148
	v_cvt_u32_f32_e32 v44, v44
	v_med3_f32 v45, v45, 0, v148
	v_med3_f32 v46, v46, 0, v148
	v_cvt_u32_f32_e32 v47, v47
	v_add_f32_e32 v48, 0x41000000, v48
	v_add_f32_e32 v49, 0x41000000, v49
	v_med3_f32 v50, v50, 0, v148
	v_cvt_u32_f32_e32 v35, v35
	v_cvt_u32_f32_e32 v45, v45
	v_cvt_u32_f32_sdwa v46, v46 dst_sel:WORD_1 dst_unused:UNUSED_PAD src0_sel:DWORD
	v_med3_f32 v48, v48, 0, v148
	v_med3_f32 v49, v49, 0, v148
	v_cvt_u32_f32_e32 v50, v50
	v_lshlrev_b32_e32 v43, 28, v43
	v_lshl_or_b32 v36, v39, 24, v36
	v_cvt_u32_f32_e32 v48, v48
	v_cvt_u32_f32_e32 v49, v49
	v_lshlrev_b32_e32 v37, 8, v37
	v_lshlrev_b32_e32 v42, 20, v42
	v_or3_b32 v36, v36, v43, v38
	v_lshlrev_b32_e32 v40, 4, v40
	v_lshlrev_b32_e32 v41, 12, v41
	v_or3_b32 v36, v36, v42, v37
	v_or3_b32 v36, v36, v41, v40
	v_lshlrev_b32_e32 v35, 28, v35
	v_lshl_or_b32 v41, v47, 24, v44
	v_lshlrev_b32_e32 v39, 8, v45
	v_lshlrev_b32_e32 v40, 20, v50
	v_or3_b32 v35, v41, v35, v46
	v_lshlrev_b32_e32 v37, 4, v48
	v_lshlrev_b32_e32 v38, 12, v49
	v_or3_b32 v35, v35, v40, v39
	v_or3_b32 v37, v35, v38, v37
	v_lshl_add_u64 v[38:39], v[134:135], 0, s[0:1]
	global_store_dwordx2 v[38:39], v[36:37], off
	s_and_saveexec_b64 s[0:1], s[2:3]
	s_cbranch_execz .LBB0_925
	s_lshl_b64 s[4:5], s[26:27], 2
	s_add_u32 s4, s36, s4
	s_addc_u32 s5, s37, s5
	global_store_dword v127, v34, s[4:5]

; #define LAS __attribute__((address_space(3)))
; #define CE_DESC(a, b) do { const float _t = fmaxf(a, b); b = fminf(a, b); a = _t; } while (0)
; __device__ __forceinline__ void merge16_desc(float (&a)[16], const float (&b)[16]) {
; #pragma unroll
;     for (int i = 0; i < 16; ++i) a[i] = fmaxf(a[i], b[15 - i]);
; #pragma unroll
;     for (int j = 8; j > 0; j >>= 1)
; #pragma unroll
;         for (int i = 0; i < 16; ++i) { const int l = i ^ j; if (l > i) CE_DESC(a[i], a[l]); }
; }
; __device__ __forceinline__ void route_half(float (&top)[16], LAS const unsigned char* keys_lds, const bf16_t* __restrict__ qrow, int r32, int hi) {
;     ...
;     for (int i = 0; i < 16; ++i) { g[0][i] = __uint_as_float(__float_as_uint(g[0][i]) | hi4); o[i] = __shfl_xor(g[0][i], 32); }
;     merge16_desc(g[0], o);
; #pragma unroll
;     for (int i = 0; i < 16; ++i) top[i] = g[0][i];
; }
; __device__ __forceinline__ void route_final(const float (&A)[16], const float (&B)[16], LAS unsigned char* tab, int* idx_out, float* gate_out, bool writer) {
;     {
;         unsigned w[8];
; #pragma unroll
;         for (int q = 0; q < 4; ++q) {
;             w[q] = (__float_as_uint(A[4 * q]) & 127u) | ((__float_as_uint(A[4 * q + 1]) & 127u) << 8) | ((__float_as_uint(A[4 * q + 2]) & 127u) << 16) | ((__float_as_uint(A[4 * q + 3]) & 127u) << 24);
;             w[4 + q] = (__float_as_uint(B[4 * q]) & 127u) | ((__float_as_uint(B[4 * q + 1]) & 127u) << 8) | ((__float_as_uint(B[4 * q + 2]) & 127u) << 16) | ((__float_as_uint(B[4 * q + 3]) & 127u) << 24);
;         }
;         *(LAS u32x4*)(tab) = (u32x4){w[0], w[1], w[2], w[3]}; *(LAS u32x4*)(tab + 16) = (u32x4){w[4], w[5], w[6], w[7]};
;     }
.LBB0_930:
	s_waitcnt lgkmcnt(0)
	v_max_f32_e32 v26, v26, v33
	v_max_f32_e32 v25, v25, v32
	v_max_f32_e32 v24, v24, v31
	v_max_f32_e32 v22, v22, v30
	v_max_f32_e32 v21, v21, v29
	v_max_f32_e32 v20, v20, v28
	v_max_f32_e32 v19, v19, v27
	v_max_f32_e32 v18, v18, v23
	v_max_f32_e32 v16, v17, v16
	v_max_f32_e32 v10, v15, v10
	v_max_f32_e32 v7, v14, v7
	v_max_f32_e32 v6, v13, v6
	v_max_f32_e32 v5, v12, v5
	v_max_f32_e32 v4, v11, v4
	v_max_f32_e32 v3, v9, v3
	v_max_f32_e32 v2, v8, v2
	v_max_f32_e32 v8, v26, v16
	v_min_f32_e32 v9, v26, v16
	v_max_f32_e32 v11, v25, v10
	v_min_f32_e32 v10, v25, v10
	v_max_f32_e32 v12, v24, v7
	v_min_f32_e32 v7, v24, v7
	v_max_f32_e32 v13, v22, v6
	v_min_f32_e32 v6, v22, v6
	v_max_f32_e32 v14, v21, v5
	v_min_f32_e32 v5, v21, v5
	v_max_f32_e32 v15, v20, v4
	v_min_f32_e32 v4, v20, v4
	v_max_f32_e32 v16, v19, v3
	v_min_f32_e32 v3, v19, v3
	v_max_f32_e32 v17, v18, v2
	v_min_f32_e32 v2, v18, v2
	v_max_f32_e32 v18, v8, v14
	v_min_f32_e32 v8, v8, v14
	v_max_f32_e32 v14, v11, v15
	v_min_f32_e32 v11, v11, v15
	v_max_f32_e32 v15, v12, v16
	v_min_f32_e32 v12, v12, v16
	v_max_f32_e32 v16, v13, v17
	v_min_f32_e32 v13, v13, v17
	v_max_f32_e32 v17, v9, v5
	v_min_f32_e32 v5, v9, v5
	v_max_f32_e32 v9, v10, v4
	v_min_f32_e32 v4, v10, v4
	v_max_f32_e32 v10, v7, v3
	v_min_f32_e32 v3, v7, v3
	v_max_f32_e32 v7, v6, v2
	v_min_f32_e32 v2, v6, v2
	v_max_f32_e32 v6, v18, v15
	v_min_f32_e32 v15, v18, v15
	v_max_f32_e32 v18, v14, v16
	v_min_f32_e32 v16, v14, v16
	v_max_f32_e32 v19, v8, v12
	v_min_f32_e32 v20, v8, v12
	v_max_f32_e32 v12, v11, v13
	v_min_f32_e32 v11, v11, v13
	v_max_f32_e32 v13, v17, v10
	v_min_f32_e32 v10, v17, v10
	v_max_f32_e32 v17, v9, v7
	v_min_f32_e32 v7, v9, v7
	v_max_f32_e32 v22, v5, v3
	v_min_f32_e32 v5, v5, v3
	v_min_f32_e32 v25, v4, v2
	v_max_f32_e32 v24, v4, v2
	v_max_f32_e32 v8, v6, v18
	v_min_f32_e32 v14, v6, v18
	v_max_f32_e32 v3, v15, v16
	v_min_f32_e32 v2, v15, v16
	v_max_f32_e32 v16, v20, v11
	v_min_f32_e32 v9, v20, v11
	v_max_f32_e32 v23, v13, v17
	v_min_f32_e32 v15, v13, v17
	v_max_f32_e32 v18, v10, v7
	v_min_f32_e32 v11, v10, v7
	v_max_f32_e32 v17, v5, v25
	v_min_f32_e32 v10, v5, v25
	v_max_f32_e32 v5, v173, v180
	v_max_f32_e32 v4, v19, v12
	v_min_f32_e32 v12, v19, v12
	v_max_f32_e32 v6, v172, v179
	v_max_f32_e32 v7, v171, v178
	v_max_f32_e32 v21, v22, v24
	v_min_f32_e32 v13, v22, v24
	v_max_f32_e32 v19, v169, v177
	v_max_f32_e32 v20, v168, v176
	v_max_f32_e32 v22, v167, v175
	v_max_f32_e32 v24, v166, v174
	v_max_f32_e32 v25, v165, v170
	v_max_f32_e32 v26, v164, v163
	v_max_f32_e32 v27, v162, v157
	v_max_f32_e32 v28, v161, v154
	v_max_f32_e32 v29, v160, v153
	v_max_f32_e32 v30, v159, v152
	v_max_f32_e32 v31, v158, v151
	v_max_f32_e32 v32, v156, v150
	v_max_f32_e32 v33, v155, v149
	v_max_f32_e32 v34, v5, v26
	v_min_f32_e32 v5, v5, v26
	v_max_f32_e32 v26, v6, v27
	v_min_f32_e32 v6, v6, v27
	v_max_f32_e32 v27, v7, v28
	v_min_f32_e32 v7, v7, v28
	v_max_f32_e32 v28, v19, v29
	v_min_f32_e32 v19, v19, v29
	v_max_f32_e32 v29, v20, v30
	v_min_f32_e32 v20, v20, v30
	v_max_f32_e32 v30, v22, v31
	v_min_f32_e32 v22, v22, v31
	v_max_f32_e32 v31, v24, v32
	v_min_f32_e32 v24, v24, v32
	v_max_f32_e32 v32, v25, v33
	v_min_f32_e32 v25, v25, v33
	v_max_f32_e32 v33, v34, v29
	v_min_f32_e32 v29, v34, v29
	v_max_f32_e32 v34, v26, v30
	v_min_f32_e32 v26, v26, v30
	v_max_f32_e32 v30, v27, v31
	v_min_f32_e32 v27, v27, v31
	v_max_f32_e32 v31, v28, v32
	v_min_f32_e32 v28, v28, v32
	v_max_f32_e32 v32, v5, v20
	v_min_f32_e32 v5, v5, v20
	v_max_f32_e32 v20, v6, v22
	v_min_f32_e32 v6, v6, v22
	v_max_f32_e32 v22, v7, v24
	v_min_f32_e32 v7, v7, v24
	v_max_f32_e32 v24, v19, v25
	v_min_f32_e32 v19, v19, v25
	v_max_f32_e32 v25, v33, v30
	v_min_f32_e32 v30, v33, v30
	v_max_f32_e32 v33, v34, v31
	v_min_f32_e32 v31, v34, v31
	v_max_f32_e32 v34, v29, v27
	v_min_f32_e32 v27, v29, v27
	v_max_f32_e32 v29, v26, v28
	v_min_f32_e32 v26, v26, v28
	v_max_f32_e32 v28, v32, v22
	v_min_f32_e32 v32, v32, v22
	v_max_f32_e32 v22, v20, v24
	v_min_f32_e32 v35, v20, v24
	v_max_f32_e32 v36, v5, v7
	v_min_f32_e32 v37, v5, v7
	v_max_f32_e32 v38, v6, v19
	v_min_f32_e32 v39, v6, v19
	v_max_f32_e32 v20, v25, v33
	v_min_f32_e32 v19, v25, v33
	v_max_f32_e32 v7, v30, v31
	v_min_f32_e32 v5, v30, v31
	v_max_f32_e32 v6, v34, v29
	v_min_f32_e32 v24, v34, v29
	v_max_f32_e32 v30, v27, v26
	v_min_f32_e32 v27, v27, v26
	v_max_f32_e32 v33, v28, v22
	v_min_f32_e32 v22, v28, v22
	v_max_f32_e32 v29, v32, v35
	v_min_f32_e32 v26, v32, v35
	v_max_f32_e32 v32, v36, v38
	v_min_f32_e32 v25, v36, v38
	v_max_f32_e32 v31, v37, v39
	v_min_f32_e32 v28, v37, v39
	v_lshlrev_b32_e32 v37, 8, v19
	v_and_b32_e32 v41, 0x7f, v20
	v_lshlrev_b32_e32 v34, 8, v25
	v_lshlrev_b32_e32 v35, 8, v22
	v_lshlrev_b32_e32 v36, 8, v24
	v_and_b32_e32 v38, 0x7f, v32
	v_and_b32_e32 v39, 0x7f, v33
	v_and_b32_e32 v40, 0x7f, v6
	v_and_or_b32 v41, v37, s46, v41
	v_lshlrev_b32_e32 v37, 16, v29
	v_and_or_b32 v40, v36, s46, v40
	v_and_or_b32 v35, v35, s46, v39
	v_and_or_b32 v34, v34, s46, v38
	v_lshlrev_b32_e32 v36, 16, v31
	v_lshlrev_b32_e32 v38, 16, v30
	v_lshlrev_b32_e32 v39, 16, v7
	v_and_b32_e32 v42, 0x7f0000, v37
	v_lshlrev_b32_e32 v37, 24, v28
	v_lshlrev_b32_e32 v43, 24, v26
	v_lshlrev_b32_e32 v44, 24, v27
	v_lshlrev_b32_e32 v45, 24, v5
	v_and_b32_e32 v39, 0x7f0000, v39
	v_and_b32_e32 v38, 0x7f0000, v38
	v_and_b32_e32 v36, 0x7f0000, v36
	v_and_b32_e32 v45, 0x7f000000, v45
	v_and_b32_e32 v44, 0x7f000000, v44
	v_and_b32_e32 v43, 0x7f000000, v43
	v_and_b32_e32 v37, 0x7f000000, v37
	v_or3_b32 v37, v34, v36, v37
	v_or3_b32 v36, v35, v42, v43
	v_or3_b32 v35, v40, v38, v44
	v_or3_b32 v34, v41, v39, v45
	ds_write_b128 v145, v[34:37]
	v_lshlrev_b32_e32 v37, 8, v14
	v_and_b32_e32 v41, 0x7f, v8
	v_lshlrev_b32_e32 v34, 8, v13
	v_lshlrev_b32_e32 v35, 8, v15
	v_lshlrev_b32_e32 v36, 8, v12
	v_and_b32_e32 v38, 0x7f, v21
	v_and_b32_e32 v39, 0x7f, v23
	v_and_b32_e32 v40, 0x7f, v4
	v_and_or_b32 v41, v37, s46, v41
	v_lshlrev_b32_e32 v37, 16, v18
	v_and_or_b32 v40, v36, s46, v40
	v_and_or_b32 v35, v35, s46, v39
	v_and_or_b32 v34, v34, s46, v38
	v_lshlrev_b32_e32 v36, 16, v17
	v_lshlrev_b32_e32 v38, 16, v16
	v_lshlrev_b32_e32 v39, 16, v3
	v_and_b32_e32 v42, 0x7f0000, v37
	v_lshlrev_b32_e32 v37, 24, v10
	v_lshlrev_b32_e32 v43, 24, v11
	v_lshlrev_b32_e32 v44, 24, v9
	v_lshlrev_b32_e32 v45, 24, v2
	v_and_b32_e32 v39, 0x7f0000, v39
	v_and_b32_e32 v38, 0x7f0000, v38
	v_and_b32_e32 v36, 0x7f0000, v36
	v_and_b32_e32 v45, 0x7f000000, v45
	v_and_b32_e32 v44, 0x7f000000, v44
	v_and_b32_e32 v43, 0x7f000000, v43
	v_and_b32_e32 v37, 0x7f000000, v37
	v_or3_b32 v37, v34, v36, v37
	v_or3_b32 v36, v35, v42, v43
	v_or3_b32 v35, v40, v38, v44
	v_or3_b32 v34, v41, v39, v45
	ds_write_b128 v145, v[34:37] offset:16
	s_and_saveexec_b64 s[4:5], s[6:7]
	s_cbranch_execz .LBB0_905
; #define CAND(i, j) __uint_as_float((__float_as_uint(A[i] + B[j]) & 0xFFFFFF00u) | (unsigned)(((i) << 4) | (j)))
; __device__ __forceinline__ void route_final(const float (&A)[16], const float (&B)[16], LAS unsigned char* tab, int* idx_out, float* gate_out, bool writer) {
;     ...
;     const float NEG = -INFINITY;
;     ...
;     float m1[16], m2[16], m3[16];
; #pragma unroll
;     for (int j = 0; j < 16; ++j) m1[j] = CAND(0, j);
; #pragma unroll
;     for (int i = 0; i < 16; ++i) m2[i] = (i < 15) ? CAND((i < 15 ? i + 1 : 0), 0) : NEG;
;     merge16_desc(m1, m2);
;     __builtin_amdgcn_sched_barrier(0);
; #pragma unroll
;     for (int j = 0; j < 16; ++j) m3[j] = (j < 7) ? CAND(1, (j < 7 ? j + 1 : 0)) : NEG;
; #pragma unroll
;     for (int i = 0; i < 16; ++i) m2[i] = (i < 6) ? CAND((i < 6 ? i + 2 : 0), 1) : NEG;
;     merge16_desc(m3, m2);
;     __builtin_amdgcn_sched_barrier(0);
;     m2[0] = CAND(2, 2); m2[1] = CAND(2, 3); m2[2] = CAND(2, 4); m2[3] = CAND(3, 2); m2[4] = CAND(4, 2); m2[5] = CAND(3, 3);
; #pragma unroll
;     for (int i = 6; i < 16; ++i) m2[i] = NEG;
;     sort16_desc(m2);
;     merge16_desc(m3, m2);
;     merge16_desc(m1, m3);
;     __builtin_amdgcn_sched_barrier(0);
	v_add_f32_e32 v32, v32, v8
	v_add_f32_e32 v29, v29, v8
	v_add_f32_e32 v41, v19, v16
	v_add_f32_e32 v48, v20, v4
	v_and_b32_e32 v32, 0xffffff00, v32
	v_add_f32_e32 v16, v20, v16
	v_and_b32_e32 v29, 0xffffff00, v29
	v_and_or_b32 v48, v48, s47, 4
	v_or_b32_e32 v32, 0xc0, v32
	v_and_or_b32 v16, v16, s47, 6
	v_or_b32_e32 v29, 0xa0, v29
	v_add_f32_e32 v35, v30, v14
	v_add_f32_e32 v33, v33, v8
	v_add_f32_e32 v31, v31, v8
	v_add_f32_e32 v30, v30, v8
	v_add_f32_e32 v47, v20, v8
	v_add_f32_e32 v23, v20, v23
	v_and_b32_e32 v33, 0xffffff00, v33
	v_max_f32_e32 v32, v48, v32
	v_add_f32_e32 v21, v20, v21
	v_add_f32_e32 v48, v6, v8
	v_add_f32_e32 v50, v20, v3
	v_and_b32_e32 v31, 0xffffff00, v31
	v_add_f32_e32 v18, v20, v18
	v_and_b32_e32 v30, 0xffffff00, v30
	v_max_f32_e32 v16, v16, v29
	v_add_f32_e32 v17, v20, v17
	v_add_f32_e32 v29, v7, v8
	v_and_b32_e32 v47, 0xffffff00, v47
	v_and_or_b32 v23, v23, s47, 8
	v_or_b32_e32 v33, 0x80, v33
	v_and_or_b32 v21, v21, s47, 12
	v_and_or_b32 v48, v48, s47, 64
	v_and_or_b32 v50, v50, s47, 2
	v_or_b32_e32 v31, 0xe0, v31
	v_and_or_b32 v18, v18, s47, 10
	v_or_b32_e32 v30, 0x60, v30
	v_and_or_b32 v17, v17, s47, 14
	v_and_or_b32 v29, v29, s47, 32
	v_add_f32_e32 v34, v27, v14
	v_add_f32_e32 v36, v24, v14
	v_max_f32_e32 v47, 0xff800000, v47
	v_max_f32_e32 v23, v23, v33
	v_max_f32_e32 v21, v21, v48
	v_max_f32_e32 v31, v50, v31
	v_max_f32_e32 v18, v18, v30
	v_max_f32_e32 v17, v17, v29
	v_and_b32_e32 v34, 0xffffff00, v34
	v_and_b32_e32 v36, 0xffffff00, v36
	v_add_f32_e32 v38, v5, v14
	v_add_f32_e32 v40, v19, v9
	v_add_f32_e32 v42, v19, v12
	v_add_f32_e32 v44, v19, v2
	v_min_f32_e32 v33, v47, v23
	v_min_f32_e32 v48, v32, v21
	v_min_f32_e32 v30, v31, v18
	v_min_f32_e32 v29, v16, v17
	v_max_f32_e32 v23, v47, v23
	v_max_f32_e32 v21, v32, v21
	v_max_f32_e32 v18, v31, v18
	v_max_f32_e32 v16, v16, v17
	v_or_b32_e32 v34, 0x71, v34
	v_and_b32_e32 v35, 0xffffff00, v35
	v_or_b32_e32 v36, 0x51, v36
	v_and_or_b32 v38, v38, s47, 49
	v_and_or_b32 v40, v40, s47, 23
	v_and_or_b32 v42, v42, s47, 21
	v_add_f32_e32 v43, v19, v4
	v_and_or_b32 v44, v44, s47, 19
	v_min_f32_e32 v32, v23, v21
	v_min_f32_e32 v17, v18, v16
	v_or_b32_e32 v35, 0x61, v35
	v_add_f32_e32 v39, v7, v14
	v_and_or_b32 v43, v43, s47, 20
	v_min_f32_e32 v31, v32, v17
	v_max_f32_e32 v17, v32, v17
	v_max_f32_e32 v21, v23, v21
	v_max_f32_e32 v23, v42, v42
	v_and_or_b32 v39, v39, s47, 33
	v_add_f32_e32 v46, v19, v14
	v_min_f32_e32 v49, v33, v48
	v_min_f32_e32 v50, v30, v29
	v_max_f32_e32 v33, v33, v48
	v_max_f32_e32 v29, v30, v29
	v_max_f32_e32 v23, 0xff800000, v23
	v_max_f32_e32 v32, 0xff800000, v36
	v_max_f32_e32 v42, 0xff800000, v44
	v_max_f32_e32 v34, 0xff800000, v34
	v_max_f32_e32 v40, 0xff800000, v40
	v_max_f32_e32 v38, 0xff800000, v38
	v_and_or_b32 v46, v46, s47, 17
	v_add_f32_e32 v26, v26, v8
	v_min_f32_e32 v30, v33, v29
	v_max_f32_e32 v29, v33, v29
	v_max_f32_e32 v16, v18, v16
	v_max_f32_e32 v33, v23, v32
	v_max_f32_e32 v44, v42, v34
	v_max_f32_e32 v43, 0xff800000, v43
	v_max_f32_e32 v35, 0xff800000, v35
	v_min_f32_e32 v23, v23, v32
	v_min_f32_e32 v32, v42, v34
	v_min_f32_e32 v34, v40, v38
	v_add_f32_e32 v45, v19, v3
	v_add_f32_e32 v12, v20, v12
	v_and_b32_e32 v26, 0xffffff00, v26
	v_min_f32_e32 v18, v21, v16
	v_max_f32_e32 v16, v21, v16
	v_max_f32_e32 v21, v46, v46
	v_max_f32_e32 v46, v40, v38
	v_max_f32_e32 v53, v43, v35
	v_max_f32_e32 v39, 0xff800000, v39
	v_max_f32_e32 v38, v32, v34
	v_min_f32_e32 v32, v32, v34
	v_add_f32_e32 v34, v7, v3
	v_add_f32_e32 v58, v5, v3
	v_add_f32_e32 v3, v6, v3
	v_and_or_b32 v12, v12, s47, 5
	v_or_b32_e32 v26, 0xb0, v26
	v_add_f32_e32 v52, v20, v2
	v_max_f32_e32 v54, v53, v39
	v_min_f32_e32 v39, v53, v39
	v_add_f32_e32 v53, v7, v2
	v_add_f32_e32 v4, v7, v4
	v_and_b32_e32 v3, 0xffffff00, v3
	v_add_f32_e32 v2, v5, v2
	v_and_or_b32 v34, v34, s47, 34
	v_and_or_b32 v53, v53, s47, 35
	v_and_or_b32 v58, v58, s47, 50
	v_and_or_b32 v4, v4, s47, 36
	v_or_b32_e32 v3, 0x42, v3
	v_and_or_b32 v2, v2, s47, 51
	v_add_f32_e32 v37, v6, v14
	v_max_f32_e32 v12, v12, v26
	v_add_f32_e32 v26, v5, v8
	v_max_f32_e32 v7, v58, v58
	v_max_f32_e32 v6, v3, v3
	v_max_f32_e32 v57, v34, v53
	v_min_f32_e32 v58, v7, v4
	v_min_f32_e32 v34, v34, v53
	v_max_f32_e32 v4, v7, v4
	v_min_f32_e32 v5, v6, v2
	v_max_f32_e32 v59, v57, v58
	v_max_f32_e32 v7, v34, v4
	v_min_f32_e32 v57, v57, v58
	v_min_f32_e32 v4, v34, v4
	v_max_f32_e32 v5, 0xff800000, v5
	v_max3_f32 v2, v3, v2, s48
	v_max3_f32 v53, v59, v7, s48
	v_max_f32_e32 v34, v57, v4
	v_min_f32_e32 v3, v5, v2
	v_min_f32_e32 v7, v59, v7
	v_min_f32_e32 v4, v57, v4
	v_max_f32_e32 v2, v5, v2
	v_and_b32_e32 v37, 0xffffff00, v37
	v_max_f32_e32 v6, v34, v3
	v_max_f32_e32 v7, 0xff800000, v7
	v_max_f32_e32 v5, v4, v2
	v_min_f32_e32 v3, v34, v3
	v_min_f32_e32 v2, v4, v2
	v_or_b32_e32 v37, 0x41, v37
	v_and_or_b32 v41, v41, s47, 22
	v_add_f32_e32 v25, v25, v8
	v_max_f32_e32 v58, v53, v6
	v_max_f32_e32 v57, v7, v5
	v_max_f32_e32 v3, 0xff800000, v3
	v_max_f32_e32 v2, 0xff800000, v2
	v_and_or_b32 v45, v45, s47, 18
	v_and_b32_e32 v25, 0xffffff00, v25
	v_max3_f32 v59, v58, v57, s48
	v_max3_f32 v4, v3, v2, s48
	v_min_f32_e32 v57, v58, v57
	v_min_f32_e32 v2, v3, v2
	v_and_or_b32 v52, v52, s47, 3
	v_or_b32_e32 v25, 0xd0, v25
	v_max_f32_e32 v41, 0xff800000, v41
	v_max_f32_e32 v37, 0xff800000, v37
	v_min_f32_e32 v6, v53, v6
	v_min_f32_e32 v5, v7, v5
	v_max_f32_e32 v57, 0xff800000, v57
	v_max_f32_e32 v2, 0xff800000, v2
	v_min_f32_e32 v51, v49, v50
	v_max_f32_e32 v49, v49, v50
	v_max_f32_e32 v21, 0xff800000, v21
	v_max_f32_e32 v45, 0xff800000, v45
	v_max_f32_e32 v50, v41, v37
	v_min_f32_e32 v37, v41, v37
	v_min_f32_e32 v35, v43, v35
	v_max_f32_e32 v34, v59, v4
; #define CAND(i, j) __uint_as_float((__float_as_uint(A[i] + B[j]) & 0xFFFFFF00u) | (unsigned)(((i) << 4) | (j)))
; __device__ __forceinline__ void route_final(const float (&A)[16], const float (&B)[16], LAS unsigned char* tab, int* idx_out, float* gate_out, bool writer) {
;     ...
; #pragma unroll
;     for (int j = 0; j < 16; ++j) m3[j] = (j < 7) ? CAND(1, (j < 7 ? j + 1 : 0)) : NEG;
; #pragma unroll
;     for (int i = 0; i < 16; ++i) m2[i] = (i < 6) ? CAND((i < 6 ? i + 2 : 0), 1) : NEG;
;     merge16_desc(m3, m2);
;     __builtin_amdgcn_sched_barrier(0);
;     m2[0] = CAND(2, 2); m2[1] = CAND(2, 3); m2[2] = CAND(2, 4); m2[3] = CAND(3, 2); m2[4] = CAND(4, 2); m2[5] = CAND(3, 3);
; #pragma unroll
;     for (int i = 6; i < 16; ++i) m2[i] = NEG;
;     sort16_desc(m2);
;     merge16_desc(m3, m2);
;     merge16_desc(m1, m3);
;     __builtin_amdgcn_sched_barrier(0);
	v_max3_f32 v7, v6, v5, s48
	v_max_f32_e32 v3, v57, v2
	v_min_f32_e32 v5, v6, v5
	v_min_f32_e32 v4, v59, v4
	v_min_f32_e32 v2, v57, v2
	v_add_f32_e32 v28, v28, v8
	v_add_f32_e32 v27, v27, v8
	v_max_f32_e32 v25, v52, v25
	v_add_f32_e32 v24, v24, v8
	v_add_f32_e32 v22, v22, v8
	v_max_f32_e32 v36, v21, v33
	v_max_f32_e32 v47, v44, v46
	v_max_f32_e32 v52, v45, v50
	v_max_f32_e32 v23, 0xff800000, v23
	v_max_f32_e32 v37, 0xff800000, v37
	v_max_f32_e32 v35, 0xff800000, v35
	v_min_f32_e32 v21, v21, v33
	v_min_f32_e32 v33, v44, v46
	v_min_f32_e32 v45, v45, v50
	v_max_f32_e32 v5, 0xff800000, v5
	v_max_f32_e32 v4, 0xff800000, v4
	v_max_f32_e32 v2, 0xff800000, v2
	v_add_f32_e32 v14, v20, v14
	v_and_b32_e32 v28, 0xffffff00, v28
	v_add_f32_e32 v15, v20, v15
	v_and_b32_e32 v27, 0xffffff00, v27
	v_add_f32_e32 v13, v20, v13
	v_add_f32_e32 v11, v20, v11
	v_and_b32_e32 v24, 0xffffff00, v24
	v_add_f32_e32 v9, v20, v9
	v_and_b32_e32 v22, 0xffffff00, v22
	v_add_f32_e32 v10, v20, v10
	v_add_f32_e32 v8, v19, v8
	v_max_f32_e32 v48, v36, v47
	v_max_f32_e32 v55, v52, v54
	v_max_f32_e32 v40, v23, v38
	v_max_f32_e32 v41, v37, v35
	v_max_f32_e32 v44, v21, v33
	v_max_f32_e32 v46, v45, v39
	v_min_f32_e32 v53, v34, v7
	v_min_f32_e32 v6, v3, v5
	v_min_f32_e32 v36, v36, v47
	v_min_f32_e32 v47, v52, v54
	v_min_f32_e32 v23, v23, v38
	v_min_f32_e32 v35, v37, v35
	v_min_f32_e32 v37, v4, v2
	v_min_f32_e32 v21, v21, v33
	v_min_f32_e32 v33, v45, v39
	v_max_f32_e32 v7, v34, v7
	v_max_f32_e32 v3, v3, v5
	v_and_or_b32 v14, v14, s47, 1
	v_or_b32_e32 v28, 0xf0, v28
	v_and_or_b32 v15, v15, s47, 9
	v_or_b32_e32 v27, 0x70, v27
	v_and_or_b32 v13, v13, s47, 13
	v_and_or_b32 v26, v26, s47, 48
	v_and_or_b32 v11, v11, s47, 11
	v_or_b32_e32 v24, 0x50, v24
	v_and_or_b32 v9, v9, s47, 7
	v_or_b32_e32 v22, 0x90, v22
	v_and_or_b32 v10, v10, s47, 15
	v_and_or_b32 v8, v8, s47, 16
	v_max3_f32 v56, v48, v55, s48
	v_max3_f32 v42, v40, v41, s48
	v_max3_f32 v50, v44, v46, s48
	v_min_f32_e32 v58, v53, v6
	v_max3_f32 v52, v36, v47, s48
	v_max3_f32 v37, v23, v35, v37
	v_max3_f32 v39, v21, v33, s48
	v_min_f32_e32 v5, v7, v3
	v_min_f32_e32 v48, v48, v55
	v_min_f32_e32 v40, v40, v41
	v_min_f32_e32 v44, v44, v46
	v_min_f32_e32 v36, v36, v47
	v_min_f32_e32 v23, v23, v35
	v_min_f32_e32 v21, v21, v33
	v_max3_f32 v32, v32, s48, v58
	v_max_f32_e32 v5, 0xff800000, v5
	v_max_f32_e32 v48, 0xff800000, v48
	v_max_f32_e32 v40, 0xff800000, v40
	v_max_f32_e32 v44, 0xff800000, v44
	v_max3_f32 v6, v53, v6, s48
	v_max_f32_e32 v36, 0xff800000, v36
	v_max3_f32 v2, v23, v4, v2
	v_max_f32_e32 v21, 0xff800000, v21
	v_max3_f32 v3, v7, v3, s48
	v_max_f32_e32 v14, v14, v28
	v_max_f32_e32 v15, v15, v27
	v_max_f32_e32 v13, v13, v26
	v_max_f32_e32 v11, v11, v24
	v_max_f32_e32 v9, v9, v22
	v_max_f32_e32 v8, v10, v8
	v_min_f32_e32 v43, v56, v42
	v_min_f32_e32 v58, v50, v32
	v_min_f32_e32 v38, v52, v37
	v_min_f32_e32 v34, v39, v5
	v_min_f32_e32 v41, v48, v40
	v_min_f32_e32 v46, v44, v6
	v_min_f32_e32 v4, v36, v2
	v_min_f32_e32 v7, v21, v3
	v_min_f32_e32 v27, v14, v15
	v_min_f32_e32 v26, v12, v13
	v_min_f32_e32 v24, v25, v11
	v_min_f32_e32 v10, v9, v8
	v_max_f32_e32 v14, v14, v15
	v_max_f32_e32 v12, v12, v13
	v_max_f32_e32 v11, v25, v11
	v_max_f32_e32 v8, v9, v8
	v_min_f32_e32 v60, v43, v58
	v_min_f32_e32 v45, v38, v34
	v_min_f32_e32 v53, v41, v46
	v_min_f32_e32 v23, v4, v7
	v_min_f32_e32 v13, v14, v12
	v_min_f32_e32 v9, v11, v8
	v_max_f32_e32 v12, v14, v12
	v_max_f32_e32 v8, v11, v8
	v_min_f32_e32 v54, v60, v45
	v_min_f32_e32 v33, v53, v23
	v_min_f32_e32 v11, v12, v8
	v_max_f32_e32 v8, v12, v8
	v_min_f32_e32 v35, v54, v33
	v_max_f32_e32 v40, v48, v40
	v_max_f32_e32 v6, v44, v6
	v_min_f32_e32 v12, v16, v8
	v_max3_f32 v8, v16, v8, v35
	v_max_f32_e32 v16, v56, v42
	v_max_f32_e32 v32, v50, v32
	v_max_f32_e32 v37, v52, v37
	v_max_f32_e32 v5, v39, v5
	v_min_f32_e32 v44, v40, v6
	v_max_f32_e32 v2, v36, v2
	v_max_f32_e32 v3, v21, v3
	v_max_f32_e32 v43, v43, v58
	v_max_f32_e32 v34, v38, v34
	v_max_f32_e32 v41, v41, v46
	v_max_f32_e32 v4, v4, v7
	v_max_f32_e32 v6, v40, v6
	v_max_f32_e32 v40, v60, v45
	v_max_f32_e32 v23, v53, v23
	v_min_f32_e32 v35, v16, v32
	v_min_f32_e32 v39, v37, v5
	v_min_f32_e32 v21, v2, v3
	v_min_f32_e32 v38, v43, v34
	v_min_f32_e32 v7, v41, v4
	v_min_f32_e32 v45, v40, v23
	v_min_f32_e32 v28, v27, v26
	v_min_f32_e32 v19, v24, v10
	v_max_f32_e32 v26, v27, v26
	v_max_f32_e32 v10, v24, v10
	v_min_f32_e32 v15, v13, v9
	v_max_f32_e32 v9, v13, v9
	v_min_f32_e32 v14, v18, v11
	v_min_f32_e32 v36, v44, v21
	v_min_f32_e32 v46, v38, v7
	v_max_f32_e32 v16, v16, v32
	v_max_f32_e32 v5, v37, v5
	v_max_f32_e32 v2, v2, v3
	v_max3_f32 v11, v18, v11, v45
	v_max_f32_e32 v18, v35, v39
	v_max_f32_e32 v21, v44, v21
	v_min_f32_e32 v20, v28, v19
	v_max_f32_e32 v19, v28, v19
	v_min_f32_e32 v24, v26, v10
	v_max_f32_e32 v10, v26, v10
	v_min_f32_e32 v13, v17, v9
	v_min_f32_e32 v42, v35, v39
	v_max3_f32 v9, v17, v9, v46
	v_min_f32_e32 v17, v16, v5
	v_min_f32_e32 v3, v6, v2
	v_min_f32_e32 v35, v18, v21
	v_max_f32_e32 v34, v43, v34
	v_max_f32_e32 v4, v41, v4
	v_max_f32_e32 v5, v16, v5
	v_max_f32_e32 v2, v6, v2
	v_min_f32_e32 v22, v51, v20
	v_min_f32_e32 v28, v49, v19
	v_min_f32_e32 v27, v30, v24
	v_min_f32_e32 v26, v29, v10
	v_min_f32_e32 v25, v31, v15
	v_min_f32_e32 v47, v42, v36
	v_min_f32_e32 v32, v17, v3
	v_max3_f32 v24, v30, v24, v35
	v_min_f32_e32 v35, v34, v4
	v_min_f32_e32 v6, v5, v2
	v_max3_f32 v10, v29, v10, v47
	v_max3_f32 v19, v49, v19, v32
	v_max3_f32 v15, v31, v15, v35
	v_max3_f32 v6, v51, v20, v6
	v_max3_f32 v12, v12, v54, v33
	v_max3_f32 v26, v26, v42, v36
	v_max3_f32 v7, v13, v38, v7
	v_max3_f32 v3, v28, v17, v3
	v_max3_f32 v14, v14, v40, v23
; __device__ __forceinline__ void route_final(const float (&A)[16], const float (&B)[16], LAS unsigned char* tab, int* idx_out, float* gate_out, bool writer) {
;     ...
;     float e[16], den = 0.f; int ex[16];
; #pragma unroll
;     for (int i = 0; i < 16; ++i) { e[i] = __expf(m1[i] - m1[0]); den += e[i]; const unsigned r = __float_as_uint(m1[i]) & 255u; ex[i] = (int)tab[r >> 4] * 128 + (int)tab[16 + (r & 15u)]; }
;     const float inv = 1.f / den;
	v_max3_f32 v18, v27, v18, v21
	v_max3_f32 v4, v25, v34, v4
	v_max3_f32 v2, v22, v5, v2
	v_max_f32_e32 v29, v8, v10
	v_max_f32_e32 v32, v9, v19
	v_max_f32_e32 v30, v11, v24
	v_max_f32_e32 v16, v15, v6
	v_max_f32_e32 v33, v12, v26
	v_max_f32_e32 v13, v7, v3
	v_max_f32_e32 v21, v14, v18
	v_max_f32_e32 v5, v4, v2
	v_max_f32_e32 v37, v29, v32
	v_max_f32_e32 v20, v30, v16
	v_max_f32_e32 v17, v33, v13
	v_max_f32_e32 v22, v21, v5
	v_max_f32_e32 v31, v37, v20
	v_max_f32_e32 v23, v17, v22
	v_max_f32_e32 v25, v31, v23
	v_sub_f32_e32 v27, v25, v25
	v_min_f32_e32 v23, v31, v23
	v_min_f32_e32 v20, v37, v20
	v_min_f32_e32 v17, v17, v22
	v_mul_f32_e32 v27, 0x3fb8aa3b, v27
	v_sub_f32_e32 v28, v23, v25
	v_max_f32_e32 v22, v20, v17
	v_min_f32_e32 v29, v29, v32
	v_min_f32_e32 v16, v30, v16
	v_min_f32_e32 v13, v33, v13
	v_min_f32_e32 v5, v21, v5
	v_exp_f32_e32 v27, v27
	v_mul_f32_e32 v28, 0x3fb8aa3b, v28
	v_sub_f32_e32 v31, v22, v25
	v_min_f32_e32 v17, v20, v17
	v_max_f32_e32 v30, v29, v16
	v_max_f32_e32 v21, v13, v5
	v_exp_f32_e32 v28, v28
	v_mul_f32_e32 v31, 0x3fb8aa3b, v31
	v_sub_f32_e32 v20, v17, v25
	v_max_f32_e32 v32, v30, v21
	v_exp_f32_e32 v31, v31
	v_mul_f32_e32 v20, 0x3fb8aa3b, v20
	v_sub_f32_e32 v33, v32, v25
	v_min_f32_e32 v21, v30, v21
	v_min_f32_e32 v16, v29, v16
	v_min_f32_e32 v5, v13, v5
	v_min_f32_e32 v8, v8, v10
	v_min_f32_e32 v9, v9, v19
	v_min_f32_e32 v11, v11, v24
	v_min_f32_e32 v6, v15, v6
	v_min_f32_e32 v12, v12, v26
	v_min_f32_e32 v3, v7, v3
	v_min_f32_e32 v14, v14, v18
	v_min_f32_e32 v2, v4, v2
	v_exp_f32_e32 v20, v20
	v_mul_f32_e32 v33, 0x3fb8aa3b, v33
	v_sub_f32_e32 v30, v21, v25
	v_max_f32_e32 v13, v16, v5
	v_max_f32_e32 v10, v8, v9
	v_max_f32_e32 v15, v11, v6
	v_max_f32_e32 v7, v12, v3
	v_max_f32_e32 v4, v14, v2
	v_add_f32_e32 v34, 0, v27
	v_exp_f32_e32 v33, v33
	v_mul_f32_e32 v30, 0x3fb8aa3b, v30
	v_sub_f32_e32 v29, v13, v25
	v_min_f32_e32 v5, v16, v5
	v_max_f32_e32 v19, v10, v15
	v_max_f32_e32 v18, v7, v4
	v_add_f32_e32 v34, v28, v34
	v_exp_f32_e32 v30, v30
	v_mul_f32_e32 v29, 0x3fb8aa3b, v29
	v_sub_f32_e32 v16, v5, v25
	v_max_f32_e32 v24, v19, v18
	v_min_f32_e32 v10, v10, v15
	v_min_f32_e32 v4, v7, v4
	v_add_f32_e32 v34, v31, v34
	v_exp_f32_e32 v29, v29
	v_mul_f32_e32 v16, 0x3fb8aa3b, v16
	v_sub_f32_e32 v26, v24, v25
	v_min_f32_e32 v18, v19, v18
	v_max_f32_e32 v15, v10, v4
	v_add_f32_e32 v34, v20, v34
	v_exp_f32_e32 v16, v16
	v_mul_f32_e32 v26, 0x3fb8aa3b, v26
	v_sub_f32_e32 v19, v18, v25
	v_sub_f32_e32 v7, v15, v25
	v_min_f32_e32 v8, v8, v9
	v_min_f32_e32 v6, v11, v6
	v_min_f32_e32 v3, v12, v3
	v_min_f32_e32 v2, v14, v2
	v_add_f32_e32 v34, v33, v34
	v_exp_f32_e32 v26, v26
	v_mul_f32_e32 v19, 0x3fb8aa3b, v19
	v_mul_f32_e32 v7, 0x3fb8aa3b, v7
	v_min_f32_e32 v4, v10, v4
	v_max_f32_e32 v9, v8, v6
	v_max_f32_e32 v11, v3, v2
	v_add_f32_e32 v34, v30, v34
	v_exp_f32_e32 v19, v19
	v_exp_f32_e32 v35, v7
	v_sub_f32_e32 v7, v4, v25
	v_max_f32_e32 v12, v9, v11
	v_add_f32_e32 v34, v29, v34
	v_mul_f32_e32 v7, 0x3fb8aa3b, v7
	v_sub_f32_e32 v14, v12, v25
	v_min_f32_e32 v9, v9, v11
	v_min_f32_e32 v6, v8, v6
	v_min_f32_e32 v2, v3, v2
	v_add_f32_e32 v34, v16, v34
	v_exp_f32_e32 v10, v7
	v_mul_f32_e32 v14, 0x3fb8aa3b, v14
	v_sub_f32_e32 v11, v9, v25
	v_max_f32_e32 v8, v6, v2
	v_add_f32_e32 v7, v26, v34
	v_exp_f32_e32 v14, v14
	v_mul_f32_e32 v11, 0x3fb8aa3b, v11
	v_sub_f32_e32 v3, v8, v25
	v_min_f32_e32 v36, v6, v2
	v_add_f32_e32 v7, v19, v7
	v_exp_f32_e32 v11, v11
	v_mul_f32_e32 v3, 0x3fb8aa3b, v3
	v_sub_f32_e32 v2, v36, v25
	v_add_f32_e32 v7, v35, v7
	v_exp_f32_e32 v34, v3
	v_mul_f32_e32 v2, 0x3fb8aa3b, v2
	v_add_f32_e32 v7, v10, v7
	v_exp_f32_e32 v37, v2
	v_add_f32_e32 v2, v14, v7
	v_add_f32_e32 v2, v11, v2
	v_add_f32_e32 v2, v34, v2
	v_add_f32_e32 v38, v37, v2
	v_div_scale_f32 v39, s[0:1], v38, v38, 1.0
	v_rcp_f32_e32 v40, v39
	v_lshlrev_b64 v[2:3], 9, v[138:139]
	v_lshl_add_u64 v[6:7], s[22:23], 0, v[2:3]
	v_fma_f32 v2, -v39, v40, 1.0
	v_fmac_f32_e32 v40, v2, v40
	v_div_scale_f32 v2, vcc, 1.0, v38, 1.0
	v_mul_f32_e32 v3, v2, v40
	v_fma_f32 v41, -v39, v3, v2
	v_fmac_f32_e32 v3, v41, v40
	v_fma_f32 v2, -v39, v3, v2
	v_div_fmas_f32 v2, v2, v40, v3
	v_div_fixup_f32 v38, v2, v38, 1.0
	v_bfe_u32 v2, v36, 4, 4
	v_and_b32_e32 v3, 15, v36
	v_bfe_u32 v36, v8, 4, 4
	v_and_b32_e32 v8, 15, v8
	v_bfe_u32 v39, v9, 4, 4
	v_and_b32_e32 v9, 15, v9
	v_bfe_u32 v40, v12, 4, 4
	v_and_b32_e32 v12, 15, v12
	v_add_u32_e32 v2, v145, v2
	v_add_u32_e32 v3, v145, v3
	v_add_u32_e32 v36, v145, v36
	v_add_u32_e32 v8, v145, v8
	v_add_u32_e32 v39, v145, v39
	v_add_u32_e32 v9, v145, v9
	v_add_u32_e32 v40, v145, v40
	v_add_u32_e32 v12, v145, v12
	ds_read_u8 v2, v2
	ds_read_u8 v3, v3 offset:16
	ds_read_u8 v36, v36
	ds_read_u8 v8, v8 offset:16
	ds_read_u8 v39, v39
	ds_read_u8 v9, v9 offset:16
	ds_read_u8 v40, v40
	ds_read_u8 v12, v12 offset:16
	s_waitcnt lgkmcnt(6)
; __device__ __forceinline__ void route_final(const float (&A)[16], const float (&B)[16], LAS unsigned char* tab, int* idx_out, float* gate_out, bool writer) {
;     ...
;     for (int i = 0; i < 16; ++i) { e[i] = __expf(m1[i] - m1[0]); den += e[i]; const unsigned r = __float_as_uint(m1[i]) & 255u; ex[i] = (int)tab[r >> 4] * 128 + (int)tab[16 + (r & 15u)]; }
;     const float inv = 1.f / den;
;     if (writer) {
; #pragma unroll
;         for (int i = 0; i < 4; ++i) {
;             u32x4 w;
; #pragma unroll
;             for (int c = 0; c < 4; ++c) w[c] = (unsigned)ex[4 * i + c] | ((__float_as_uint(e[4 * i + c] * inv) + 0x8000u) & 0xFFFF0000u);
;             *(u32x4*)(idx_out + 4 * i) = w; }
;         (void)gate_out;
;     }
	v_lshl_add_u32 v41, v2, 7, v3
	s_waitcnt lgkmcnt(4)
	v_lshl_add_u32 v8, v36, 7, v8
	s_waitcnt lgkmcnt(2)
	v_lshl_add_u32 v9, v39, 7, v9
	v_bfe_u32 v2, v4, 4, 4
	v_and_b32_e32 v3, 15, v4
	v_bfe_u32 v4, v15, 4, 4
	v_and_b32_e32 v15, 15, v15
	v_bfe_u32 v36, v18, 4, 4
	v_and_b32_e32 v18, 15, v18
	v_bfe_u32 v39, v24, 4, 4
	v_and_b32_e32 v24, 15, v24
	v_add_u32_e32 v2, v145, v2
	v_add_u32_e32 v3, v145, v3
	v_add_u32_e32 v4, v145, v4
	v_add_u32_e32 v15, v145, v15
	v_add_u32_e32 v36, v145, v36
	v_add_u32_e32 v18, v145, v18
	v_add_u32_e32 v39, v145, v39
	v_add_u32_e32 v24, v145, v24
	ds_read_u8 v2, v2
	ds_read_u8 v3, v3 offset:16
	ds_read_u8 v4, v4
	ds_read_u8 v15, v15 offset:16
	ds_read_u8 v36, v36
	ds_read_u8 v18, v18 offset:16
	ds_read_u8 v39, v39
	ds_read_u8 v24, v24 offset:16
	s_waitcnt lgkmcnt(8)
	v_lshl_add_u32 v12, v40, 7, v12
	s_waitcnt lgkmcnt(6)
	v_lshl_add_u32 v40, v2, 7, v3
	s_waitcnt lgkmcnt(4)
	v_lshl_add_u32 v15, v4, 7, v15
	s_waitcnt lgkmcnt(2)
	v_lshl_add_u32 v18, v36, 7, v18
	v_bfe_u32 v2, v5, 4, 4
	v_and_b32_e32 v3, 15, v5
	v_bfe_u32 v4, v13, 4, 4
	v_and_b32_e32 v5, 15, v13
	v_bfe_u32 v13, v21, 4, 4
	v_and_b32_e32 v21, 15, v21
	v_bfe_u32 v36, v32, 4, 4
	v_and_b32_e32 v32, 15, v32
	v_add_u32_e32 v2, v145, v2
	v_add_u32_e32 v3, v145, v3
	v_add_u32_e32 v4, v145, v4
	v_add_u32_e32 v5, v145, v5
	v_add_u32_e32 v13, v145, v13
	v_add_u32_e32 v21, v145, v21
	v_add_u32_e32 v36, v145, v36
	v_add_u32_e32 v32, v145, v32
	ds_read_u8 v2, v2
	ds_read_u8 v3, v3 offset:16
	ds_read_u8 v4, v4
	ds_read_u8 v5, v5 offset:16
	ds_read_u8 v13, v13
	ds_read_u8 v21, v21 offset:16
	ds_read_u8 v36, v36
	ds_read_u8 v32, v32 offset:16
	s_waitcnt lgkmcnt(8)
	v_lshl_add_u32 v24, v39, 7, v24
	s_waitcnt lgkmcnt(6)
	v_lshl_add_u32 v39, v2, 7, v3
	s_waitcnt lgkmcnt(4)
	v_lshl_add_u32 v42, v4, 7, v5
	s_waitcnt lgkmcnt(2)
	v_lshl_add_u32 v13, v13, 7, v21
	v_bfe_u32 v2, v17, 4, 4
	v_and_b32_e32 v3, 15, v17
	v_bfe_u32 v4, v22, 4, 4
	v_and_b32_e32 v5, 15, v22
	v_bfe_u32 v17, v23, 4, 4
	v_and_b32_e32 v21, 15, v23
	v_bfe_u32 v22, v25, 4, 4
	v_and_b32_e32 v23, 15, v25
	v_add_u32_e32 v2, v145, v2
	v_add_u32_e32 v3, v145, v3
	v_add_u32_e32 v4, v145, v4
	v_add_u32_e32 v5, v145, v5
	v_add_u32_e32 v17, v145, v17
	v_add_u32_e32 v21, v145, v21
	v_add_u32_e32 v22, v145, v22
	v_add_u32_e32 v23, v145, v23
	ds_read_u8 v2, v2
	ds_read_u8 v3, v3 offset:16
	ds_read_u8 v4, v4
	ds_read_u8 v5, v5 offset:16
	ds_read_u8 v17, v17
	ds_read_u8 v21, v21 offset:16
	ds_read_u8 v22, v22
	ds_read_u8 v23, v23 offset:16
	s_waitcnt lgkmcnt(4)
	v_lshl_add_u32 v4, v4, 7, v5
	v_mul_f32_e32 v5, v27, v38
	v_lshl_add_u32 v25, v36, 7, v32
	v_lshl_add_u32 v32, v2, 7, v3
	s_waitcnt lgkmcnt(0)
	v_lshl_add_u32 v2, v22, 7, v23
	v_add_u32_e32 v5, 0x8000, v5
	v_and_or_b32 v2, v5, s39, v2
	v_mul_f32_e32 v5, v28, v38
	v_lshl_add_u32 v3, v17, 7, v21
	v_add_u32_e32 v5, 0x8000, v5
	v_and_or_b32 v3, v5, s39, v3
	v_mul_f32_e32 v5, v31, v38
	v_add_u32_e32 v5, 0x8000, v5
	v_and_or_b32 v4, v5, s39, v4
	v_mul_f32_e32 v5, v20, v38
	v_add_u32_e32 v5, 0x8000, v5
	v_and_or_b32 v5, v5, s39, v32
	global_store_dwordx4 v[6:7], v[2:5], off
	s_nop 1
	v_mul_f32_e32 v2, v33, v38
	v_mul_f32_e32 v3, v30, v38
	v_mul_f32_e32 v4, v29, v38
	v_mul_f32_e32 v5, v16, v38
	v_add_u32_e32 v2, 0x8000, v2
	v_add_u32_e32 v3, 0x8000, v3
	v_add_u32_e32 v4, 0x8000, v4
	v_add_u32_e32 v5, 0x8000, v5
	v_and_or_b32 v2, v2, s39, v25
	v_and_or_b32 v3, v3, s39, v13
	v_and_or_b32 v4, v4, s39, v42
	v_and_or_b32 v5, v5, s39, v39
	global_store_dwordx4 v[6:7], v[2:5], off offset:16
	s_nop 1
	v_mul_f32_e32 v2, v26, v38
	v_mul_f32_e32 v3, v19, v38
	v_mul_f32_e32 v4, v35, v38
	v_mul_f32_e32 v5, v10, v38
	v_add_u32_e32 v2, 0x8000, v2
	v_add_u32_e32 v3, 0x8000, v3
	v_add_u32_e32 v4, 0x8000, v4
	v_add_u32_e32 v5, 0x8000, v5
	v_and_or_b32 v2, v2, s39, v24
	v_and_or_b32 v3, v3, s39, v18
	v_and_or_b32 v4, v4, s39, v15
	v_and_or_b32 v5, v5, s39, v40
	global_store_dwordx4 v[6:7], v[2:5], off offset:32
	s_nop 1
	v_mul_f32_e32 v2, v14, v38
	v_mul_f32_e32 v3, v11, v38
	v_mul_f32_e32 v4, v34, v38
	v_mul_f32_e32 v5, v37, v38
	v_add_u32_e32 v2, 0x8000, v2
	v_add_u32_e32 v3, 0x8000, v3
	v_add_u32_e32 v4, 0x8000, v4
	v_add_u32_e32 v5, 0x8000, v5
	v_and_or_b32 v2, v2, s39, v12
	v_and_or_b32 v3, v3, s39, v9
	v_and_or_b32 v4, v4, s39, v8
	v_and_or_b32 v5, v5, s39, v41
	global_store_dwordx4 v[6:7], v[2:5], off offset:48
	s_branch .LBB0_905
